# weight-conversion loops pipelined one item deeper: next item loads issued before the LDS write into a second register set, loop unrolled x2, address math before the wait
# baseline (speedup 1.0000x reference)
.LBB0_218:
	v_add_u32_e32 v2, 0x800, v130
	s_lshr_b32 s0, s12, 8
	v_ashrrev_i32_e32 v41, 6, v2
	v_cvt_f32_u32_e32 v2, s0
	s_sub_i32 s13, 0, s0
	s_abs_i32 s9, s14
	s_ashr_i32 s8, s14, 31
	v_rcp_iflag_f32_e32 v2, v2
	v_add_u32_e32 v3, 0xa00, v130
	v_ashrrev_i32_e32 v42, 6, v3
	v_add_u32_e32 v3, 0xc00, v130
	v_mul_f32_e32 v2, 0x4f7ffffe, v2
	v_cvt_u32_f32_e32 v2, v2
	v_lshlrev_b32_e32 v1, 2, v130
	v_ashrrev_i32_e32 v43, 6, v3
	v_add_u32_e32 v3, 0xe00, v130
	v_readfirstlane_b32 s15, v2
	s_mul_i32 s13, s13, s15
	s_mul_hi_u32 s13, s15, s13
	s_add_i32 s15, s15, s13
	s_mul_hi_u32 s13, s9, s15
	s_mul_i32 s15, s13, s0
	s_sub_i32 s9, s9, s15
	s_add_i32 s15, s13, 1
	s_sub_i32 s16, s9, s0
	s_cmp_ge_u32 s9, s0
	s_cselect_b32 s13, s15, s13
	s_cselect_b32 s9, s16, s9
	s_add_i32 s15, s13, 1
	s_cmp_ge_u32 s9, s0
	s_cselect_b32 s9, s15, s13
	s_xor_b32 s9, s9, s8
	s_sub_i32 s13, s9, s8
	s_mul_i32 s0, s13, s0
	s_sub_i32 s0, s14, s0
	s_lshl_b32 s8, s0, 8
	s_ashr_i32 s9, s8, 31
	s_lshl_b64 s[14:15], s[8:9], 2
	s_add_u32 s10, s10, s14
	v_and_b32_e32 v36, 0xfc, v1
	v_ashrrev_i32_e32 v44, 6, v3
	s_addc_u32 s11, s11, s15
	s_lshl_b32 s16, s13, 6
	v_mov_b32_e32 v35, 0
	v_lshlrev_b32_e32 v34, 2, v36
	v_add_u32_e32 v4, s16, v44
	v_lshl_add_u64 v[2:3], s[10:11], 0, v[34:35]
	v_ashrrev_i32_e32 v7, 31, v4
	v_mad_u64_u32 v[4:5], s[10:11], v4, s12, 0
	v_mov_b32_e32 v6, v5
	v_mad_u64_u32 v[6:7], s[10:11], v7, s12, v[6:7]
	v_mov_b32_e32 v5, v6
	v_add_u32_e32 v6, s16, v43
	v_ashrrev_i32_e32 v9, 31, v6
	v_mad_u64_u32 v[6:7], s[10:11], v6, s12, 0
	v_mov_b32_e32 v8, v7
	v_mad_u64_u32 v[8:9], s[10:11], v9, s12, v[8:9]
	v_lshl_add_u64 v[4:5], v[4:5], 2, v[2:3]
	v_mov_b32_e32 v7, v8
	v_lshl_add_u64 v[6:7], v[6:7], 2, v[2:3]
	global_load_dwordx4 v[30:33], v[4:5], off
	global_load_dwordx4 v[26:29], v[6:7], off
	v_add_u32_e32 v4, s16, v42
	v_ashrrev_i32_e32 v7, 31, v4
	v_mad_u64_u32 v[4:5], s[10:11], v4, s12, 0
	v_mov_b32_e32 v6, v5
	v_mad_u64_u32 v[6:7], s[10:11], v7, s12, v[6:7]
	v_mov_b32_e32 v5, v6
	v_add_u32_e32 v6, s16, v41
	v_ashrrev_i32_e32 v9, 31, v6
	v_mad_u64_u32 v[6:7], s[10:11], v6, s12, 0
	v_mov_b32_e32 v8, v7
	v_add_u32_e32 v54, 0x600, v130
	v_mad_u64_u32 v[8:9], s[10:11], v9, s12, v[8:9]
	v_ashrrev_i32_e32 v40, 6, v54
	v_lshl_add_u64 v[4:5], v[4:5], 2, v[2:3]
	v_mov_b32_e32 v7, v8
	v_lshl_add_u64 v[6:7], v[6:7], 2, v[2:3]
	global_load_dwordx4 v[22:25], v[4:5], off
	global_load_dwordx4 v[18:21], v[6:7], off
	v_add_u32_e32 v4, s16, v40
	v_ashrrev_i32_e32 v7, 31, v4
	v_mad_u64_u32 v[4:5], s[10:11], v4, s12, 0
	v_add_u32_e32 v51, 0x400, v130
	v_mov_b32_e32 v6, v5
	v_ashrrev_i32_e32 v39, 6, v51
	v_mad_u64_u32 v[6:7], s[10:11], v7, s12, v[6:7]
	v_mov_b32_e32 v5, v6
	v_add_u32_e32 v6, s16, v39
	v_ashrrev_i32_e32 v9, 31, v6
	v_mad_u64_u32 v[6:7], s[10:11], v6, s12, 0
	v_mov_b32_e32 v8, v7
	v_add_u32_e32 v37, 0x200, v130
	v_mad_u64_u32 v[8:9], s[10:11], v9, s12, v[8:9]
	v_ashrrev_i32_e32 v38, 6, v37
	v_lshl_add_u64 v[4:5], v[4:5], 2, v[2:3]
	v_mov_b32_e32 v7, v8
	v_lshl_add_u64 v[6:7], v[6:7], 2, v[2:3]
	global_load_dwordx4 v[14:17], v[4:5], off
	global_load_dwordx4 v[10:13], v[6:7], off
	v_add_u32_e32 v4, s16, v38
	v_ashrrev_i32_e32 v7, 31, v4
	v_mad_u64_u32 v[4:5], s[10:11], v4, s12, 0
	v_mov_b32_e32 v6, v5
	v_ashrrev_i32_e32 v1, 6, v130
	v_mad_u64_u32 v[6:7], s[10:11], v7, s12, v[6:7]
	v_mov_b32_e32 v5, v6
	v_add_u32_e32 v6, s16, v1
	v_ashrrev_i32_e32 v9, 31, v6
	v_mad_u64_u32 v[6:7], s[10:11], v6, s12, 0
	v_mov_b32_e32 v8, v7
	v_mad_u64_u32 v[8:9], s[10:11], v9, s12, v[8:9]
	v_mov_b32_e32 v7, v8
	v_lshl_add_u64 v[4:5], v[4:5], 2, v[2:3]
	v_lshl_add_u64 v[2:3], v[6:7], 2, v[2:3]
	global_load_dwordx4 v[6:9], v[4:5], off
	s_nop 0
	global_load_dwordx4 v[2:5], v[2:3], off
	v_lshlrev_b32_e32 v45, 3, v130
	v_and_b32_e32 v66, 56, v45
	s_movk_i32 s0, 0x404
	v_mad_u32_u24 v55, v66, s0, 0
	v_mul_lo_u32 v57, v1, s0
	v_mul_lo_u32 v58, v38, s0
	v_mul_lo_u32 v59, v39, s0
	v_mul_lo_u32 v60, v40, s0
	v_mul_lo_u32 v61, v41, s0
	v_mul_lo_u32 v62, v42, s0
	v_mul_lo_u32 v63, v43, s0
	v_mul_lo_u32 v64, v44, s0
	s_add_u32 s0, s6, 0x1e940000
	s_addc_u32 s9, s7, 0
	s_add_u32 s12, s6, 0x16940000
	s_addc_u32 s13, s7, 0
	s_add_u32 s14, s6, 0x16140000
	s_addc_u32 s15, s7, 0
	s_add_u32 s30, s6, 0x15540000
	s_addc_u32 s31, s7, 0
	s_add_u32 s6, s6, 0x11f40000
	v_add_u32_e32 v34, 0, v34
	v_ashrrev_i32_e32 v45, 3, v130
	v_ashrrev_i32_e32 v48, 3, v37
	v_ashrrev_i32_e32 v51, 3, v51
	v_ashrrev_i32_e32 v54, 3, v54
	s_addc_u32 s7, s7, 0
	s_add_i32 s10, s33, s38
	s_mov_b32 s11, 0
	v_lshl_add_u32 v46, v45, 2, v55
	v_and_b32_e32 v47, 15, v45
	v_lshl_add_u32 v49, v48, 2, v55
	v_and_b32_e32 v50, 15, v48
	v_lshl_add_u32 v52, v51, 2, v55
	v_and_b32_e32 v53, 15, v51
	v_lshl_add_u32 v55, v54, 2, v55
	v_and_b32_e32 v56, 15, v54
	s_add_i32 s34, s10, 0xfffff5c0
	s_add_i32 s35, s10, 0xfffff6c0
	v_add_u32_e32 v57, v34, v57
	v_add_u32_e32 v58, v34, v58
	v_add_u32_e32 v59, v34, v59
	v_add_u32_e32 v60, v34, v60
	v_add_u32_e32 v61, v34, v61
	v_add_u32_e32 v62, v34, v62
	v_add_u32_e32 v63, v34, v63
	v_add_u32_e32 v64, v34, v64
	v_lshlrev_b32_e32 v34, 2, v36
	v_lshlrev_b32_e32 v36, 1, v66
	s_movk_i32 s36, 0x7fff
	v_mov_b32_e32 v65, 1
	s_mov_b32 s26, s17
	s_mov_b32 s27, s29
	s_mov_b64 s[20:21], s[2:3]
	s_waitcnt vmcnt(0)
	s_branch .LBB0_222
.LBB0_222:
	s_add_i32 s33, s33, s38
	s_cmp_lt_u32 s28, 2
	s_cselect_b64 s[18:19], -1, 0
	s_and_b64 vcc, exec, s[18:19]
	s_mov_b32 s37, s1
	s_mov_b32 s22, s8
	s_mov_b32 s10, s16
	s_cbranch_vccnz .Lcwp_222
	s_add_i32 s10, s34, 0xa40
	s_cmpk_lt_i32 s10, 0x6c0
	s_cbranch_scc1 .LBB0_219
	s_cmpk_gt_u32 s10, 0x83f
	s_mov_b64 s[22:23], -1
	s_cbranch_scc0 .LBB0_237
	s_cmpk_gt_u32 s10, 0x93f
	s_cbranch_scc0 .LBB0_234
	s_mul_hi_u32 s10, s35, 0xaaaaaaab
	s_lshr_b32 s10, s10, 8
	s_mul_i32 s20, s10, 0xfffffe80
	s_add_i32 s10, s34, 0x100
	s_mul_hi_u32 s10, s10, 0xaaaaaaab
	s_lshr_b32 s10, s10, 8
	s_mul_i32 s21, s10, 0xfffffe80
	s_add_i32 s41, s33, s21
	s_add_i32 s40, s34, s20
	s_addk_i32 s41, 0xf6c0
	s_add_i32 s42, s40, 0x100
	s_cmpk_gt_i32 s42, 0x7f
	s_cbranch_scc0 .LBB0_231
	s_lshl_b64 s[22:23], s[10:11], 23
	s_cmpk_gt_u32 s42, 0xff
	s_mov_b64 s[26:27], -1
	s_cbranch_scc0 .LBB0_229
	s_add_u32 s24, s88, s22
	s_addc_u32 s25, s89, s23
	s_lshl_b64 s[20:21], s[10:11], 22
	s_add_u32 s20, s0, s20
	s_addc_u32 s21, s9, s21
	s_mov_b64 s[26:27], 0

.LBB0_239:
	s_movk_i32 s27, 0x400
	s_movk_i32 s39, 0x800
	s_mov_b32 s37, 0
	s_mov_b32 s26, 0
	s_cbranch_execz .LBB0_232
	s_branch .LBB0_233
.LBB0_219:
	v_readlane_b32 s56, v250, 7
	v_readlane_b32 s70, v250, 21
	v_readlane_b32 s71, v250, 22
	s_mov_b32 s26, 0
	s_movk_i32 s39, 0x3600
	s_movk_i32 s27, 0x800
	s_mov_b64 s[24:25], s[70:71]
	s_mov_b64 s[20:21], s[6:7]
	s_mov_b32 s40, s33
	s_mov_b32 s37, 0
	v_readlane_b32 s57, v250, 8
	v_readlane_b32 s58, v250, 9
	v_readlane_b32 s59, v250, 10
	v_readlane_b32 s60, v250, 11
	v_readlane_b32 s61, v250, 12
	v_readlane_b32 s62, v250, 13
	v_readlane_b32 s63, v250, 14
	v_readlane_b32 s64, v250, 15
	v_readlane_b32 s65, v250, 16
	v_readlane_b32 s66, v250, 17
	v_readlane_b32 s67, v250, 18
	v_readlane_b32 s68, v250, 19
	v_readlane_b32 s69, v250, 20
.LBB0_220:
	s_lshr_b32 s22, s39, 8
	v_cvt_f32_u32_e32 v182, s22
	s_sub_i32 s41, 0, s22
	s_abs_i32 s23, s40
	s_ashr_i32 s10, s40, 31
	v_rcp_iflag_f32_e32 v182, v182
	s_nop 0
	v_mul_f32_e32 v182, 0x4f7ffffe, v182
	v_cvt_u32_f32_e32 v182, v182
	s_nop 0
	v_readfirstlane_b32 s42, v182
	s_mul_i32 s41, s41, s42
	s_mul_hi_u32 s41, s42, s41
	s_add_i32 s42, s42, s41
	s_mul_hi_u32 s41, s23, s42
	s_mul_i32 s42, s41, s22
	s_sub_i32 s23, s23, s42
	s_add_i32 s43, s41, 1
	s_sub_i32 s42, s23, s22
	s_cmp_ge_u32 s23, s22
	s_cselect_b32 s41, s43, s41
	s_cselect_b32 s23, s42, s23
	s_add_i32 s42, s41, 1
	s_cmp_ge_u32 s23, s22
	s_cselect_b32 s23, s42, s41
	s_xor_b32 s23, s23, s10
	s_sub_i32 s23, s23, s10
	s_lshl_b32 s10, s23, 6
	s_mul_i32 s23, s23, s22
	s_sub_i32 s22, s40, s23
	s_lshl_b32 s22, s22, 8
	s_ashr_i32 s23, s22, 31
	s_lshl_b64 s[40:41], s[22:23], 2
	s_add_u32 s24, s24, s40
	v_add_u32_e32 v182, s10, v1
	s_addc_u32 s25, s25, s41
	v_add_u32_e32 v190, s10, v39
	v_add_u32_e32 v198, s10, v41
	v_add_u32_e32 v208, s10, v43
	v_ashrrev_i32_e32 v185, 31, v182
	v_lshl_add_u64 v[206:207], s[24:25], 0, v[34:35]
	v_mad_u64_u32 v[182:183], s[24:25], v182, s39, 0
	v_ashrrev_i32_e32 v193, 31, v190
	v_mad_u64_u32 v[190:191], s[24:25], v190, s39, 0
	v_ashrrev_i32_e32 v201, 31, v198
	v_mad_u64_u32 v[198:199], s[24:25], v198, s39, 0
	v_ashrrev_i32_e32 v211, 31, v208
	v_mad_u64_u32 v[208:209], s[24:25], v208, s39, 0
	v_mov_b32_e32 v184, v183
	v_mov_b32_e32 v192, v191
	v_mov_b32_e32 v200, v199
	v_mov_b32_e32 v210, v209
	v_mad_u64_u32 v[184:185], s[24:25], v185, s39, v[184:185]
	v_mad_u64_u32 v[192:193], s[24:25], v193, s39, v[192:193]
	v_mad_u64_u32 v[200:201], s[24:25], v201, s39, v[200:201]
	v_mad_u64_u32 v[210:211], s[24:25], v211, s39, v[210:211]
	v_mov_b32_e32 v183, v184
	v_add_u32_e32 v184, s10, v38
	v_mov_b32_e32 v191, v192
	v_add_u32_e32 v192, s10, v40
	v_mov_b32_e32 v199, v200
	v_add_u32_e32 v200, s10, v42
	v_mov_b32_e32 v209, v210
	v_add_u32_e32 v210, s10, v44
	v_ashrrev_i32_e32 v187, 31, v184
	v_mad_u64_u32 v[184:185], s[24:25], v184, s39, 0
	v_ashrrev_i32_e32 v195, 31, v192
	v_mad_u64_u32 v[192:193], s[24:25], v192, s39, 0
	v_ashrrev_i32_e32 v203, 31, v200
	v_mad_u64_u32 v[200:201], s[24:25], v200, s39, 0
	v_ashrrev_i32_e32 v213, 31, v210
	v_mad_u64_u32 v[210:211], s[24:25], v210, s39, 0
	v_mov_b32_e32 v186, v185
	v_mov_b32_e32 v194, v193
	v_mov_b32_e32 v202, v201
	v_mov_b32_e32 v212, v211
	v_mad_u64_u32 v[186:187], s[24:25], v187, s39, v[186:187]
	v_mad_u64_u32 v[194:195], s[24:25], v195, s39, v[194:195]
	v_mad_u64_u32 v[202:203], s[24:25], v203, s39, v[202:203]
	v_mad_u64_u32 v[212:213], s[24:25], v213, s39, v[212:213]
	v_mov_b32_e32 v185, v186
	v_mov_b32_e32 v193, v194
	v_mov_b32_e32 v201, v202
	v_mov_b32_e32 v211, v212
	v_lshl_add_u64 v[182:183], v[182:183], 2, v[206:207]
	v_lshl_add_u64 v[186:187], v[184:185], 2, v[206:207]
	v_lshl_add_u64 v[190:191], v[190:191], 2, v[206:207]
	v_lshl_add_u64 v[194:195], v[192:193], 2, v[206:207]
	v_lshl_add_u64 v[198:199], v[198:199], 2, v[206:207]
	v_lshl_add_u64 v[202:203], v[200:201], 2, v[206:207]
	v_lshl_add_u64 v[208:209], v[208:209], 2, v[206:207]
	v_lshl_add_u64 v[210:211], v[210:211], 2, v[206:207]
	v_mov_b32_e32 v188, v182
	v_mov_b32_e32 v189, v183
	v_mov_b32_e32 v196, v186
	v_mov_b32_e32 v197, v187
	v_mov_b32_e32 v204, v190
	v_mov_b32_e32 v205, v191
	v_mov_b32_e32 v214, v194
	v_mov_b32_e32 v215, v195
	v_mov_b32_e32 v216, v198
	v_mov_b32_e32 v217, v199
	v_mov_b32_e32 v218, v202
	v_mov_b32_e32 v219, v203
	v_mov_b32_e32 v220, v208
	v_mov_b32_e32 v221, v209
	v_mov_b32_e32 v222, v210
	v_mov_b32_e32 v223, v211
.Lcwp_222:
	s_waitcnt vmcnt(4)
	s_and_b64 vcc, exec, s[18:19]
	s_cbranch_vccnz .Lcnp_222
	global_load_dwordx4 v[150:153], v[188:189], off
	s_nop 0
	global_load_dwordx4 v[154:157], v[196:197], off
	s_nop 0
	global_load_dwordx4 v[158:161], v[204:205], off
	s_nop 0
	global_load_dwordx4 v[162:165], v[214:215], off
	s_nop 0
	global_load_dwordx4 v[166:169], v[216:217], off
	s_nop 0
	global_load_dwordx4 v[170:173], v[218:219], off
	s_nop 0
	global_load_dwordx4 v[174:177], v[220:221], off
	s_nop 0
	global_load_dwordx4 v[178:181], v[222:223], off
.Lcnp_222:
	ds_write2_b32 v57, v2, v3 offset1:1
	ds_write2_b32 v57, v4, v5 offset0:2 offset1:3
	ds_write2_b32 v58, v6, v7 offset1:1
	ds_write2_b32 v58, v8, v9 offset0:2 offset1:3
	ds_write2_b32 v59, v10, v11 offset1:1
	ds_write2_b32 v59, v12, v13 offset0:2 offset1:3
	ds_write2_b32 v60, v14, v15 offset1:1
	ds_write2_b32 v60, v16, v17 offset0:2 offset1:3
	ds_write2_b32 v61, v18, v19 offset1:1
	ds_write2_b32 v61, v20, v21 offset0:2 offset1:3
	ds_write2_b32 v62, v22, v23 offset1:1
	ds_write2_b32 v62, v24, v25 offset0:2 offset1:3
	ds_write2_b32 v63, v26, v27 offset1:1
	ds_write2_b32 v63, v28, v29 offset0:2 offset1:3
	ds_write2_b32 v64, v30, v31 offset1:1
	ds_write2_b32 v64, v32, v33 offset0:2 offset1:3
	s_waitcnt lgkmcnt(0)
	s_barrier

.Lcq222_239:
	s_movk_i32 s27, 0x400
	s_movk_i32 s39, 0x800
	s_mov_b32 s37, 0
	s_mov_b32 s26, 0
	s_cbranch_execz .Lcq222_232
	s_branch .Lcq222_233
.Lcq222_219:
	v_readlane_b32 s56, v250, 7
	v_readlane_b32 s70, v250, 21
	v_readlane_b32 s71, v250, 22
	s_mov_b32 s26, 0
	s_movk_i32 s39, 0x3600
	s_movk_i32 s27, 0x800
	s_mov_b64 s[24:25], s[70:71]
	s_mov_b64 s[20:21], s[6:7]
	s_mov_b32 s40, s33
	s_mov_b32 s37, 0
	v_readlane_b32 s57, v250, 8
	v_readlane_b32 s58, v250, 9
	v_readlane_b32 s59, v250, 10
	v_readlane_b32 s60, v250, 11
	v_readlane_b32 s61, v250, 12
	v_readlane_b32 s62, v250, 13
	v_readlane_b32 s63, v250, 14
	v_readlane_b32 s64, v250, 15
	v_readlane_b32 s65, v250, 16
	v_readlane_b32 s66, v250, 17
	v_readlane_b32 s67, v250, 18
	v_readlane_b32 s68, v250, 19
	v_readlane_b32 s69, v250, 20

.Lcwq_222:
	s_waitcnt vmcnt(4)
	s_and_b64 vcc, exec, s[18:19]
	s_cbranch_vccnz .Lcnq_222
	global_load_dwordx4 v[2:5], v[188:189], off
	s_nop 0
	global_load_dwordx4 v[6:9], v[196:197], off
	s_nop 0
	global_load_dwordx4 v[10:13], v[204:205], off
	s_nop 0
	global_load_dwordx4 v[14:17], v[214:215], off
	s_nop 0
	global_load_dwordx4 v[18:21], v[216:217], off
	s_nop 0
	global_load_dwordx4 v[22:25], v[218:219], off
	s_nop 0
	global_load_dwordx4 v[26:29], v[220:221], off
	s_nop 0
	global_load_dwordx4 v[30:33], v[222:223], off
.Lcnq_222:
	ds_write2_b32 v57, v150, v151 offset1:1
	ds_write2_b32 v57, v152, v153 offset0:2 offset1:3
	ds_write2_b32 v58, v154, v155 offset1:1
	ds_write2_b32 v58, v156, v157 offset0:2 offset1:3
	ds_write2_b32 v59, v158, v159 offset1:1
	ds_write2_b32 v59, v160, v161 offset0:2 offset1:3
	ds_write2_b32 v60, v162, v163 offset1:1
	ds_write2_b32 v60, v164, v165 offset0:2 offset1:3
	ds_write2_b32 v61, v166, v167 offset1:1
	ds_write2_b32 v61, v168, v169 offset0:2 offset1:3
	ds_write2_b32 v62, v170, v171 offset1:1
	ds_write2_b32 v62, v172, v173 offset0:2 offset1:3
	ds_write2_b32 v63, v174, v175 offset1:1
	ds_write2_b32 v63, v176, v177 offset0:2 offset1:3
	ds_write2_b32 v64, v178, v179 offset1:1
	ds_write2_b32 v64, v180, v181 offset0:2 offset1:3
	s_waitcnt lgkmcnt(0)
	s_barrier
.Lcq222_221:
	s_add_i32 s28, s28, -1
	s_cmp_eq_u32 s17, 0
	v_add_u32_e32 v66, s8, v45
	v_lshlrev_b32_e32 v37, 1, v66
	s_cselect_b64 vcc, -1, 0
	s_ashr_i32 s17, s16, 31
	v_and_b32_e32 v37, 0xffffffe0, v37
	s_lshl_b64 s[16:17], s[16:17], 1
	v_add3_u32 v67, s1, v47, v37
	s_add_u32 s2, s2, s16
	s_addc_u32 s3, s3, s17
	v_mov_b32_e32 v37, v35
	v_cndmask_b32_e32 v66, v67, v66, vcc
	v_lshl_add_u64 v[70:71], s[2:3], 0, v[36:37]
	v_ashrrev_i32_e32 v69, 31, v66
	v_mad_u64_u32 v[66:67], s[2:3], v66, s29, 0
	v_mov_b32_e32 v68, v67
	ds_read_b32 v37, v46
	ds_read_b32 v74, v46 offset:1028
	ds_read_b32 v75, v46 offset:2056
	ds_read_b32 v76, v46 offset:3084
	ds_read_b32 v77, v46 offset:4112
	ds_read_b32 v78, v46 offset:5140
	ds_read_b32 v79, v46 offset:6168
	ds_read_b32 v80, v46 offset:7196
	v_mad_u64_u32 v[68:69], s[2:3], v69, s29, v[68:69]
	v_mov_b32_e32 v67, v68
	v_lshl_add_u64 v[72:73], v[66:67], 1, v[70:71]
	s_waitcnt lgkmcnt(7)
	v_and_b32_sdwa v67, v37, v65 dst_sel:DWORD dst_unused:UNUSED_PAD src0_sel:WORD_1 src1_sel:DWORD
	v_add3_u32 v37, v37, v67, s36
	s_waitcnt lgkmcnt(4)
	v_and_b32_sdwa v67, v76, v65 dst_sel:DWORD dst_unused:UNUSED_PAD src0_sel:WORD_1 src1_sel:DWORD
	v_and_b32_sdwa v68, v74, v65 dst_sel:DWORD dst_unused:UNUSED_PAD src0_sel:WORD_1 src1_sel:DWORD
	v_and_b32_sdwa v66, v75, v65 dst_sel:DWORD dst_unused:UNUSED_PAD src0_sel:WORD_1 src1_sel:DWORD
	v_add3_u32 v67, v76, v67, s36
	v_add3_u32 v68, v74, v68, s36
	v_add3_u32 v66, v75, v66, s36
	v_and_b32_e32 v67, 0xffff0000, v67
	v_and_b32_e32 v68, 0xffff0000, v68
	s_waitcnt lgkmcnt(0)
	v_and_b32_sdwa v69, v80, v65 dst_sel:DWORD dst_unused:UNUSED_PAD src0_sel:WORD_1 src1_sel:DWORD
	v_and_b32_sdwa v74, v78, v65 dst_sel:DWORD dst_unused:UNUSED_PAD src0_sel:WORD_1 src1_sel:DWORD
	v_or_b32_sdwa v67, v67, v66 dst_sel:DWORD dst_unused:UNUSED_PAD src0_sel:DWORD src1_sel:WORD_1
	v_or_b32_sdwa v66, v68, v37 dst_sel:DWORD dst_unused:UNUSED_PAD src0_sel:DWORD src1_sel:WORD_1
	v_and_b32_sdwa v37, v79, v65 dst_sel:DWORD dst_unused:UNUSED_PAD src0_sel:WORD_1 src1_sel:DWORD
	v_and_b32_sdwa v68, v77, v65 dst_sel:DWORD dst_unused:UNUSED_PAD src0_sel:WORD_1 src1_sel:DWORD
	v_add3_u32 v69, v80, v69, s36
	v_add3_u32 v74, v78, v74, s36
	v_add3_u32 v68, v77, v68, s36
	v_add3_u32 v37, v79, v37, s36
	v_and_b32_e32 v69, 0xffff0000, v69
	v_and_b32_e32 v74, 0xffff0000, v74
	v_or_b32_sdwa v69, v69, v37 dst_sel:DWORD dst_unused:UNUSED_PAD src0_sel:DWORD src1_sel:WORD_1
	v_or_b32_sdwa v68, v74, v68 dst_sel:DWORD dst_unused:UNUSED_PAD src0_sel:DWORD src1_sel:WORD_1
	global_store_dwordx4 v[72:73], v[66:69], off
	ds_read_b32 v37, v49
	ds_read_b32 v74, v49 offset:1028
	ds_read_b32 v75, v49 offset:2056
	ds_read_b32 v76, v49 offset:3084
	ds_read_b32 v77, v49 offset:4112
	ds_read_b32 v78, v49 offset:5140
	ds_read_b32 v79, v49 offset:6168
	ds_read_b32 v80, v49 offset:7196
	v_add_u32_e32 v66, s8, v48
	v_lshlrev_b32_e32 v67, 1, v66
	v_and_b32_e32 v67, 0xffffffe0, v67
	v_add3_u32 v67, s1, v50, v67
	v_cndmask_b32_e32 v66, v67, v66, vcc
	v_ashrrev_i32_e32 v69, 31, v66
	v_mad_u64_u32 v[66:67], s[2:3], v66, s29, 0
	v_mov_b32_e32 v68, v67
	v_mad_u64_u32 v[68:69], s[2:3], v69, s29, v[68:69]
	v_mov_b32_e32 v67, v68
	v_lshl_add_u64 v[72:73], v[66:67], 1, v[70:71]
	s_waitcnt lgkmcnt(7)
	v_and_b32_sdwa v67, v37, v65 dst_sel:DWORD dst_unused:UNUSED_PAD src0_sel:WORD_1 src1_sel:DWORD
	v_add3_u32 v37, v37, v67, s36
	s_waitcnt lgkmcnt(4)
	v_and_b32_sdwa v67, v76, v65 dst_sel:DWORD dst_unused:UNUSED_PAD src0_sel:WORD_1 src1_sel:DWORD
	v_and_b32_sdwa v68, v74, v65 dst_sel:DWORD dst_unused:UNUSED_PAD src0_sel:WORD_1 src1_sel:DWORD
	v_and_b32_sdwa v66, v75, v65 dst_sel:DWORD dst_unused:UNUSED_PAD src0_sel:WORD_1 src1_sel:DWORD
	v_add3_u32 v67, v76, v67, s36
	v_add3_u32 v68, v74, v68, s36
	v_add3_u32 v66, v75, v66, s36
	v_and_b32_e32 v67, 0xffff0000, v67
	v_and_b32_e32 v68, 0xffff0000, v68
	s_waitcnt lgkmcnt(0)
	v_and_b32_sdwa v69, v80, v65 dst_sel:DWORD dst_unused:UNUSED_PAD src0_sel:WORD_1 src1_sel:DWORD
	v_and_b32_sdwa v74, v78, v65 dst_sel:DWORD dst_unused:UNUSED_PAD src0_sel:WORD_1 src1_sel:DWORD
	v_or_b32_sdwa v67, v67, v66 dst_sel:DWORD dst_unused:UNUSED_PAD src0_sel:DWORD src1_sel:WORD_1
	v_or_b32_sdwa v66, v68, v37 dst_sel:DWORD dst_unused:UNUSED_PAD src0_sel:DWORD src1_sel:WORD_1
	v_and_b32_sdwa v37, v79, v65 dst_sel:DWORD dst_unused:UNUSED_PAD src0_sel:WORD_1 src1_sel:DWORD
	v_and_b32_sdwa v68, v77, v65 dst_sel:DWORD dst_unused:UNUSED_PAD src0_sel:WORD_1 src1_sel:DWORD
	v_add3_u32 v69, v80, v69, s36
	v_add3_u32 v74, v78, v74, s36
	v_add3_u32 v68, v77, v68, s36
	v_add3_u32 v37, v79, v37, s36
	v_and_b32_e32 v69, 0xffff0000, v69
	v_and_b32_e32 v74, 0xffff0000, v74
	v_or_b32_sdwa v69, v69, v37 dst_sel:DWORD dst_unused:UNUSED_PAD src0_sel:DWORD src1_sel:WORD_1
	v_or_b32_sdwa v68, v74, v68 dst_sel:DWORD dst_unused:UNUSED_PAD src0_sel:DWORD src1_sel:WORD_1
	global_store_dwordx4 v[72:73], v[66:69], off
	ds_read_b32 v37, v52
	ds_read_b32 v74, v52 offset:1028
	ds_read_b32 v75, v52 offset:2056
	ds_read_b32 v76, v52 offset:3084
	ds_read_b32 v77, v52 offset:4112
	ds_read_b32 v78, v52 offset:5140
	ds_read_b32 v79, v52 offset:6168
	ds_read_b32 v80, v52 offset:7196
	v_add_u32_e32 v66, s8, v51
	v_lshlrev_b32_e32 v67, 1, v66
	v_and_b32_e32 v67, 0xffffffe0, v67
	v_add3_u32 v67, s1, v53, v67
	v_cndmask_b32_e32 v66, v67, v66, vcc
	v_ashrrev_i32_e32 v69, 31, v66
	v_mad_u64_u32 v[66:67], s[2:3], v66, s29, 0
	v_mov_b32_e32 v68, v67
	v_mad_u64_u32 v[68:69], s[2:3], v69, s29, v[68:69]
	v_mov_b32_e32 v67, v68
	v_lshl_add_u64 v[72:73], v[66:67], 1, v[70:71]
	s_waitcnt lgkmcnt(7)
	v_and_b32_sdwa v67, v37, v65 dst_sel:DWORD dst_unused:UNUSED_PAD src0_sel:WORD_1 src1_sel:DWORD
	v_add3_u32 v37, v37, v67, s36
	s_waitcnt lgkmcnt(4)
	v_and_b32_sdwa v67, v76, v65 dst_sel:DWORD dst_unused:UNUSED_PAD src0_sel:WORD_1 src1_sel:DWORD
	v_and_b32_sdwa v68, v74, v65 dst_sel:DWORD dst_unused:UNUSED_PAD src0_sel:WORD_1 src1_sel:DWORD
	v_and_b32_sdwa v66, v75, v65 dst_sel:DWORD dst_unused:UNUSED_PAD src0_sel:WORD_1 src1_sel:DWORD
	v_add3_u32 v67, v76, v67, s36
	v_add3_u32 v68, v74, v68, s36
	v_add3_u32 v66, v75, v66, s36
	v_and_b32_e32 v67, 0xffff0000, v67
	v_and_b32_e32 v68, 0xffff0000, v68
	s_waitcnt lgkmcnt(0)
	v_and_b32_sdwa v69, v80, v65 dst_sel:DWORD dst_unused:UNUSED_PAD src0_sel:WORD_1 src1_sel:DWORD
	v_and_b32_sdwa v74, v78, v65 dst_sel:DWORD dst_unused:UNUSED_PAD src0_sel:WORD_1 src1_sel:DWORD
	v_or_b32_sdwa v67, v67, v66 dst_sel:DWORD dst_unused:UNUSED_PAD src0_sel:DWORD src1_sel:WORD_1
	v_or_b32_sdwa v66, v68, v37 dst_sel:DWORD dst_unused:UNUSED_PAD src0_sel:DWORD src1_sel:WORD_1
	v_and_b32_sdwa v37, v79, v65 dst_sel:DWORD dst_unused:UNUSED_PAD src0_sel:WORD_1 src1_sel:DWORD
	v_and_b32_sdwa v68, v77, v65 dst_sel:DWORD dst_unused:UNUSED_PAD src0_sel:WORD_1 src1_sel:DWORD
	v_add3_u32 v69, v80, v69, s36
	v_add3_u32 v74, v78, v74, s36
	v_add3_u32 v68, v77, v68, s36
	v_add3_u32 v37, v79, v37, s36
	v_and_b32_e32 v69, 0xffff0000, v69
	v_and_b32_e32 v74, 0xffff0000, v74
	v_or_b32_sdwa v69, v69, v37 dst_sel:DWORD dst_unused:UNUSED_PAD src0_sel:DWORD src1_sel:WORD_1
	v_or_b32_sdwa v68, v74, v68 dst_sel:DWORD dst_unused:UNUSED_PAD src0_sel:DWORD src1_sel:WORD_1
	global_store_dwordx4 v[72:73], v[66:69], off
	ds_read_b32 v37, v55
	ds_read_b32 v72, v55 offset:1028
	ds_read_b32 v73, v55 offset:2056
	ds_read_b32 v74, v55 offset:3084
	ds_read_b32 v75, v55 offset:4112
	ds_read_b32 v76, v55 offset:5140
	ds_read_b32 v77, v55 offset:6168
	ds_read_b32 v78, v55 offset:7196
	v_add_u32_e32 v66, s8, v54
	v_lshlrev_b32_e32 v67, 1, v66
	v_and_b32_e32 v67, 0xffffffe0, v67
	v_add3_u32 v67, s1, v56, v67
	v_cndmask_b32_e32 v66, v67, v66, vcc
	v_ashrrev_i32_e32 v69, 31, v66
	v_mad_u64_u32 v[66:67], s[2:3], v66, s29, 0
	v_mov_b32_e32 v68, v67
	v_mad_u64_u32 v[68:69], s[2:3], v69, s29, v[68:69]
	v_mov_b32_e32 v67, v68
	v_lshl_add_u64 v[70:71], v[66:67], 1, v[70:71]
	s_waitcnt lgkmcnt(7)
	v_and_b32_sdwa v67, v37, v65 dst_sel:DWORD dst_unused:UNUSED_PAD src0_sel:WORD_1 src1_sel:DWORD
	v_add3_u32 v37, v37, v67, s36
	s_waitcnt lgkmcnt(4)
	v_and_b32_sdwa v67, v74, v65 dst_sel:DWORD dst_unused:UNUSED_PAD src0_sel:WORD_1 src1_sel:DWORD
	v_and_b32_sdwa v68, v72, v65 dst_sel:DWORD dst_unused:UNUSED_PAD src0_sel:WORD_1 src1_sel:DWORD
	v_and_b32_sdwa v66, v73, v65 dst_sel:DWORD dst_unused:UNUSED_PAD src0_sel:WORD_1 src1_sel:DWORD
	v_add3_u32 v67, v74, v67, s36
	v_add3_u32 v68, v72, v68, s36
	v_add3_u32 v66, v73, v66, s36
	v_and_b32_e32 v67, 0xffff0000, v67
	v_and_b32_e32 v68, 0xffff0000, v68
	s_waitcnt lgkmcnt(0)
	v_and_b32_sdwa v69, v78, v65 dst_sel:DWORD dst_unused:UNUSED_PAD src0_sel:WORD_1 src1_sel:DWORD
	v_and_b32_sdwa v72, v76, v65 dst_sel:DWORD dst_unused:UNUSED_PAD src0_sel:WORD_1 src1_sel:DWORD
	v_or_b32_sdwa v67, v67, v66 dst_sel:DWORD dst_unused:UNUSED_PAD src0_sel:DWORD src1_sel:WORD_1
	v_or_b32_sdwa v66, v68, v37 dst_sel:DWORD dst_unused:UNUSED_PAD src0_sel:DWORD src1_sel:WORD_1
	v_and_b32_sdwa v37, v77, v65 dst_sel:DWORD dst_unused:UNUSED_PAD src0_sel:WORD_1 src1_sel:DWORD
	v_and_b32_sdwa v68, v75, v65 dst_sel:DWORD dst_unused:UNUSED_PAD src0_sel:WORD_1 src1_sel:DWORD
	v_add3_u32 v69, v78, v69, s36
	v_add3_u32 v72, v76, v72, s36
	v_add3_u32 v68, v75, v68, s36
	v_add3_u32 v37, v77, v37, s36
	v_and_b32_e32 v69, 0xffff0000, v69
	v_and_b32_e32 v72, 0xffff0000, v72
	v_or_b32_sdwa v69, v69, v37 dst_sel:DWORD dst_unused:UNUSED_PAD src0_sel:DWORD src1_sel:WORD_1
	v_or_b32_sdwa v68, v72, v68 dst_sel:DWORD dst_unused:UNUSED_PAD src0_sel:DWORD src1_sel:WORD_1
	s_add_i32 s34, s34, s38
	s_add_i32 s35, s35, s38
	s_andn2_b64 vcc, exec, s[18:19]
	s_mov_b32 s1, s37
	s_mov_b32 s17, s26
	s_mov_b32 s8, s22
	s_mov_b32 s16, s10
	s_mov_b32 s29, s27
	s_mov_b64 s[2:3], s[20:21]
	global_store_dwordx4 v[70:71], v[66:69], off
	s_barrier
	s_cbranch_vccz .LBB0_240
	s_branch .LBB0_222

.LBB0_1942:
	s_waitcnt vmcnt(11)
	v_add_u32_e32 v2, 0x800, v34
	s_lshr_b32 s4, s8, 8
	v_ashrrev_i32_e32 v42, 6, v2
	v_cvt_f32_u32_e32 v2, s4
	s_sub_i32 s11, 0, s4
	s_abs_i32 s10, s9
	s_ashr_i32 s5, s9, 31
	v_rcp_iflag_f32_e32 v2, v2
	v_add_u32_e32 v3, 0xa00, v34
	v_ashrrev_i32_e32 v43, 6, v3
	v_add_u32_e32 v3, 0xc00, v34
	v_mul_f32_e32 v2, 0x4f7ffffe, v2
	v_cvt_u32_f32_e32 v2, v2
	v_lshlrev_b32_e32 v1, 2, v34
	v_ashrrev_i32_e32 v44, 6, v3
	v_add_u32_e32 v3, 0xe00, v34
	v_readfirstlane_b32 s12, v2
	s_mul_i32 s11, s11, s12
	s_mul_hi_u32 s11, s12, s11
	s_add_i32 s12, s12, s11
	s_mul_hi_u32 s11, s10, s12
	s_mul_i32 s12, s11, s4
	s_sub_i32 s10, s10, s12
	s_add_i32 s12, s11, 1
	s_sub_i32 s13, s10, s4
	s_cmp_ge_u32 s10, s4
	s_cselect_b32 s11, s12, s11
	s_cselect_b32 s10, s13, s10
	s_add_i32 s12, s11, 1
	s_cmp_ge_u32 s10, s4
	s_cselect_b32 s10, s12, s11
	s_xor_b32 s10, s10, s5
	s_sub_i32 s12, s10, s5
	s_mul_i32 s4, s12, s4
	s_sub_i32 s4, s9, s4
	s_lshl_b32 s4, s4, 8
	s_ashr_i32 s5, s4, 31
	s_lshl_b64 s[10:11], s[4:5], 2
	s_add_u32 s6, s6, s10
	v_and_b32_e32 v38, 0xfc, v1
	v_ashrrev_i32_e32 v45, 6, v3
	s_addc_u32 s7, s7, s11
	s_lshl_b32 s14, s12, 6
	v_mov_b32_e32 v37, 0
	v_lshlrev_b32_e32 v36, 2, v38
	v_add_u32_e32 v4, s14, v45
	v_lshl_add_u64 v[2:3], s[6:7], 0, v[36:37]
	s_waitcnt vmcnt(10)
	v_ashrrev_i32_e32 v7, 31, v4
	v_mad_u64_u32 v[4:5], s[6:7], v4, s8, 0
	v_mov_b32_e32 v6, v5
	v_mad_u64_u32 v[6:7], s[6:7], v7, s8, v[6:7]
	v_mov_b32_e32 v5, v6
	v_add_u32_e32 v6, s14, v44
	v_ashrrev_i32_e32 v9, 31, v6
	v_mad_u64_u32 v[6:7], s[6:7], v6, s8, 0
	v_mov_b32_e32 v8, v7
	v_mad_u64_u32 v[8:9], s[6:7], v9, s8, v[8:9]
	v_lshl_add_u64 v[4:5], v[4:5], 2, v[2:3]
	v_mov_b32_e32 v7, v8
	v_lshl_add_u64 v[6:7], v[6:7], 2, v[2:3]
	global_load_dwordx4 v[30:33], v[4:5], off
	global_load_dwordx4 v[26:29], v[6:7], off
	v_add_u32_e32 v4, s14, v43
	v_ashrrev_i32_e32 v7, 31, v4
	v_mad_u64_u32 v[4:5], s[6:7], v4, s8, 0
	v_mov_b32_e32 v6, v5
	v_mad_u64_u32 v[6:7], s[6:7], v7, s8, v[6:7]
	v_mov_b32_e32 v5, v6
	v_add_u32_e32 v6, s14, v42
	v_ashrrev_i32_e32 v9, 31, v6
	v_mad_u64_u32 v[6:7], s[6:7], v6, s8, 0
	v_mov_b32_e32 v8, v7
	v_add_u32_e32 v55, 0x600, v34
	v_mad_u64_u32 v[8:9], s[6:7], v9, s8, v[8:9]
	v_ashrrev_i32_e32 v41, 6, v55
	v_lshl_add_u64 v[4:5], v[4:5], 2, v[2:3]
	v_mov_b32_e32 v7, v8
	v_lshl_add_u64 v[6:7], v[6:7], 2, v[2:3]
	global_load_dwordx4 v[22:25], v[4:5], off
	global_load_dwordx4 v[18:21], v[6:7], off
	v_add_u32_e32 v4, s14, v41
	v_ashrrev_i32_e32 v7, 31, v4
	v_mad_u64_u32 v[4:5], s[6:7], v4, s8, 0
	v_add_u32_e32 v52, 0x400, v34
	v_mov_b32_e32 v6, v5
	v_ashrrev_i32_e32 v40, 6, v52
	v_mad_u64_u32 v[6:7], s[6:7], v7, s8, v[6:7]
	v_mov_b32_e32 v5, v6
	v_add_u32_e32 v6, s14, v40
	v_ashrrev_i32_e32 v9, 31, v6
	v_mad_u64_u32 v[6:7], s[6:7], v6, s8, 0
	v_mov_b32_e32 v8, v7
	v_add_u32_e32 v39, 0x200, v34
	v_mad_u64_u32 v[8:9], s[6:7], v9, s8, v[8:9]
	v_ashrrev_i32_e32 v35, 6, v39
	v_lshl_add_u64 v[4:5], v[4:5], 2, v[2:3]
	v_mov_b32_e32 v7, v8
	v_lshl_add_u64 v[6:7], v[6:7], 2, v[2:3]
	global_load_dwordx4 v[14:17], v[4:5], off
	global_load_dwordx4 v[10:13], v[6:7], off
	v_add_u32_e32 v4, s14, v35
	v_ashrrev_i32_e32 v7, 31, v4
	v_mad_u64_u32 v[4:5], s[6:7], v4, s8, 0
	v_mov_b32_e32 v6, v5
	v_ashrrev_i32_e32 v1, 6, v34
	v_mad_u64_u32 v[6:7], s[6:7], v7, s8, v[6:7]
	v_mov_b32_e32 v5, v6
	v_add_u32_e32 v6, s14, v1
	v_ashrrev_i32_e32 v9, 31, v6
	v_mad_u64_u32 v[6:7], s[6:7], v6, s8, 0
	v_mov_b32_e32 v8, v7
	v_mad_u64_u32 v[8:9], s[6:7], v9, s8, v[8:9]
	v_mov_b32_e32 v7, v8
	v_lshl_add_u64 v[4:5], v[4:5], 2, v[2:3]
	v_lshl_add_u64 v[2:3], v[6:7], 2, v[2:3]
	global_load_dwordx4 v[6:9], v[4:5], off
	s_nop 0
	global_load_dwordx4 v[2:5], v[2:3], off
	v_lshlrev_b32_e32 v46, 3, v34
	v_and_b32_e32 v66, 56, v46
	s_movk_i32 s5, 0x404
	v_readlane_b32 s12, v251, 60
	v_mad_u32_u24 v56, v66, s5, 0
	v_mul_lo_u32 v58, v1, s5
	v_mul_lo_u32 v59, v35, s5
	v_mul_lo_u32 v60, v40, s5
	v_mul_lo_u32 v61, v41, s5
	v_mul_lo_u32 v62, v42, s5
	v_mul_lo_u32 v63, v43, s5
	v_mul_lo_u32 v64, v44, s5
	v_mul_lo_u32 v65, v45, s5
	v_readlane_b32 s13, v251, 61
	s_add_u32 s5, s12, 0x1e940000
	s_addc_u32 s26, s13, 0
	s_add_u32 s8, s12, 0x16940000
	s_addc_u32 s9, s13, 0
	s_add_u32 s10, s12, 0x16140000
	s_addc_u32 s11, s13, 0
	s_add_u32 s27, s12, 0x15540000
	s_addc_u32 s28, s13, 0
	v_add_u32_e32 v36, 0, v36
	v_ashrrev_i32_e32 v46, 3, v34
	v_ashrrev_i32_e32 v49, 3, v39
	v_ashrrev_i32_e32 v52, 3, v52
	v_ashrrev_i32_e32 v55, 3, v55
	s_add_u32 s12, s12, 0x11f40000
	s_mov_b32 s7, 0
	v_lshl_add_u32 v47, v46, 2, v56
	v_and_b32_e32 v48, 15, v46
	v_lshl_add_u32 v50, v49, 2, v56
	v_and_b32_e32 v51, 15, v49
	v_lshl_add_u32 v53, v52, 2, v56
	v_and_b32_e32 v54, 15, v52
	v_lshl_add_u32 v56, v55, 2, v56
	v_and_b32_e32 v57, 15, v55
	s_addc_u32 s13, s13, 0
	s_add_i32 s29, s16, 0x15e1
	s_mov_b32 s30, 17
	v_add_u32_e32 v58, v36, v58
	v_add_u32_e32 v59, v36, v59
	v_add_u32_e32 v60, v36, v60
	v_add_u32_e32 v61, v36, v61
	v_add_u32_e32 v62, v36, v62
	v_add_u32_e32 v63, v36, v63
	v_add_u32_e32 v64, v36, v64
	v_add_u32_e32 v65, v36, v65
	v_lshlrev_b32_e32 v36, 2, v38
	v_lshlrev_b32_e32 v38, 1, v66
	s_movk_i32 s31, 0x7fff
	v_mov_b32_e32 v66, 1
	s_mov_b32 s24, s15
	s_mov_b32 s25, s0
	s_mov_b64 s[18:19], s[2:3]
	v_readlane_b32 s42, v251, 58
	v_readlane_b32 s43, v251, 59
	s_waitcnt vmcnt(0)
	s_branch .LBB0_1946
.LBB0_1946:
	s_add_i32 s33, s34, 1
	s_cmp_lt_u32 s30, 2
	s_cselect_b64 s[16:17], -1, 0
	s_and_b64 vcc, exec, s[16:17]
	s_mov_b32 s35, s1
	s_mov_b32 s20, s4
	s_mov_b32 s6, s14
	s_cbranch_vccnz .Lcwp_1946
	s_add_i32 s6, s29, 0x93f
	s_cmpk_lt_i32 s6, 0x6bf
	s_cbranch_scc1 .LBB0_1943
	s_add_i32 s6, s29, 0x940
	s_cmpk_gt_u32 s6, 0x83f
	s_mov_b64 s[20:21], -1
	s_cbranch_scc0 .LBB0_1961
	s_cmpk_gt_u32 s6, 0x93f
	s_cbranch_scc0 .LBB0_1958
	s_mul_hi_u32 s6, s29, 0xaaaaaaab
	s_lshr_b32 s6, s6, 8
	s_mul_i32 s18, s6, 0xfffffe80
	s_add_i32 s34, s34, s18
	s_addk_i32 s34, 0xf6c1
	s_add_i32 s38, s29, s18
	s_cmpk_gt_i32 s38, 0x7f
	s_cbranch_scc0 .LBB0_1955
	s_lshl_b64 s[20:21], s[6:7], 23
	s_cmpk_gt_u32 s38, 0xff
	s_mov_b64 s[24:25], -1
	s_cbranch_scc0 .LBB0_1953
	s_add_i32 s37, s34, 0xffffff00
	s_add_u32 s22, s88, s20
	s_addc_u32 s23, s89, s21
	s_lshl_b64 s[18:19], s[6:7], 22
	s_add_u32 s18, s5, s18
	s_addc_u32 s19, s26, s19
	s_mov_b64 s[24:25], 0

.LBB0_1963:
	s_movk_i32 s25, 0x400
	s_movk_i32 s36, 0x800
	s_mov_b32 s35, 0
	s_mov_b32 s24, 0
	s_cbranch_execz .LBB0_1956
	s_branch .LBB0_1957
.LBB0_1943:
	v_readlane_b32 s56, v250, 7
	v_readlane_b32 s70, v250, 21
	v_readlane_b32 s71, v250, 22
	s_mov_b32 s24, 0
	s_movk_i32 s36, 0x3600
	s_movk_i32 s25, 0x800
	s_mov_b64 s[22:23], s[70:71]
	s_mov_b64 s[18:19], s[12:13]
	s_mov_b32 s37, s33
	s_mov_b32 s35, 0
	v_readlane_b32 s57, v250, 8
	v_readlane_b32 s58, v250, 9
	v_readlane_b32 s59, v250, 10
	v_readlane_b32 s60, v250, 11
	v_readlane_b32 s61, v250, 12
	v_readlane_b32 s62, v250, 13
	v_readlane_b32 s63, v250, 14
	v_readlane_b32 s64, v250, 15
	v_readlane_b32 s65, v250, 16
	v_readlane_b32 s66, v250, 17
	v_readlane_b32 s67, v250, 18
	v_readlane_b32 s68, v250, 19
	v_readlane_b32 s69, v250, 20
.LBB0_1944:
	s_lshr_b32 s20, s36, 8
	v_cvt_f32_u32_e32 v182, s20
	s_sub_i32 s34, 0, s20
	s_abs_i32 s21, s37
	s_ashr_i32 s6, s37, 31
	v_rcp_iflag_f32_e32 v182, v182
	s_nop 0
	v_mul_f32_e32 v182, 0x4f7ffffe, v182
	v_cvt_u32_f32_e32 v182, v182
	s_nop 0
	v_readfirstlane_b32 s38, v182
	s_mul_i32 s34, s34, s38
	s_mul_hi_u32 s34, s38, s34
	s_add_i32 s38, s38, s34
	s_mul_hi_u32 s34, s21, s38
	s_mul_i32 s38, s34, s20
	s_sub_i32 s21, s21, s38
	s_add_i32 s39, s34, 1
	s_sub_i32 s38, s21, s20
	s_cmp_ge_u32 s21, s20
	s_cselect_b32 s34, s39, s34
	s_cselect_b32 s21, s38, s21
	s_add_i32 s38, s34, 1
	s_cmp_ge_u32 s21, s20
	s_cselect_b32 s21, s38, s34
	s_xor_b32 s21, s21, s6
	s_sub_i32 s21, s21, s6
	s_lshl_b32 s6, s21, 6
	s_mul_i32 s21, s21, s20
	s_sub_i32 s20, s37, s21
	s_lshl_b32 s20, s20, 8
	s_ashr_i32 s21, s20, 31
	s_lshl_b64 s[38:39], s[20:21], 2
	s_add_u32 s22, s22, s38
	v_add_u32_e32 v182, s6, v1
	s_addc_u32 s23, s23, s39
	v_add_u32_e32 v190, s6, v40
	v_add_u32_e32 v198, s6, v42
	v_add_u32_e32 v208, s6, v44
	v_ashrrev_i32_e32 v185, 31, v182
	v_lshl_add_u64 v[206:207], s[22:23], 0, v[36:37]
	v_mad_u64_u32 v[182:183], s[22:23], v182, s36, 0
	v_ashrrev_i32_e32 v193, 31, v190
	v_mad_u64_u32 v[190:191], s[22:23], v190, s36, 0
	v_ashrrev_i32_e32 v201, 31, v198
	v_mad_u64_u32 v[198:199], s[22:23], v198, s36, 0
	v_ashrrev_i32_e32 v211, 31, v208
	v_mad_u64_u32 v[208:209], s[22:23], v208, s36, 0
	v_mov_b32_e32 v184, v183
	v_mov_b32_e32 v192, v191
	v_mov_b32_e32 v200, v199
	v_mov_b32_e32 v210, v209
	v_mad_u64_u32 v[184:185], s[22:23], v185, s36, v[184:185]
	v_mad_u64_u32 v[192:193], s[22:23], v193, s36, v[192:193]
	v_mad_u64_u32 v[200:201], s[22:23], v201, s36, v[200:201]
	v_mad_u64_u32 v[210:211], s[22:23], v211, s36, v[210:211]
	v_mov_b32_e32 v183, v184
	v_add_u32_e32 v184, s6, v35
	v_mov_b32_e32 v191, v192
	v_add_u32_e32 v192, s6, v41
	v_mov_b32_e32 v199, v200
	v_add_u32_e32 v200, s6, v43
	v_mov_b32_e32 v209, v210
	v_add_u32_e32 v210, s6, v45
	v_ashrrev_i32_e32 v187, 31, v184
	v_mad_u64_u32 v[184:185], s[22:23], v184, s36, 0
	v_ashrrev_i32_e32 v195, 31, v192
	v_mad_u64_u32 v[192:193], s[22:23], v192, s36, 0
	v_ashrrev_i32_e32 v203, 31, v200
	v_mad_u64_u32 v[200:201], s[22:23], v200, s36, 0
	v_ashrrev_i32_e32 v213, 31, v210
	v_mad_u64_u32 v[210:211], s[22:23], v210, s36, 0
	v_mov_b32_e32 v186, v185
	v_mov_b32_e32 v194, v193
	v_mov_b32_e32 v202, v201
	v_mov_b32_e32 v212, v211
	v_mad_u64_u32 v[186:187], s[22:23], v187, s36, v[186:187]
	v_mad_u64_u32 v[194:195], s[22:23], v195, s36, v[194:195]
	v_mad_u64_u32 v[202:203], s[22:23], v203, s36, v[202:203]
	v_mad_u64_u32 v[212:213], s[22:23], v213, s36, v[212:213]
	v_mov_b32_e32 v185, v186
	v_mov_b32_e32 v193, v194
	v_mov_b32_e32 v201, v202
	v_mov_b32_e32 v211, v212
	v_lshl_add_u64 v[182:183], v[182:183], 2, v[206:207]
	v_lshl_add_u64 v[186:187], v[184:185], 2, v[206:207]
	v_lshl_add_u64 v[190:191], v[190:191], 2, v[206:207]
	v_lshl_add_u64 v[194:195], v[192:193], 2, v[206:207]
	v_lshl_add_u64 v[198:199], v[198:199], 2, v[206:207]
	v_lshl_add_u64 v[202:203], v[200:201], 2, v[206:207]
	v_lshl_add_u64 v[208:209], v[208:209], 2, v[206:207]
	v_lshl_add_u64 v[210:211], v[210:211], 2, v[206:207]
	v_mov_b32_e32 v188, v182
	v_mov_b32_e32 v189, v183
	v_mov_b32_e32 v196, v186
	v_mov_b32_e32 v197, v187
	v_mov_b32_e32 v204, v190
	v_mov_b32_e32 v205, v191
	v_mov_b32_e32 v214, v194
	v_mov_b32_e32 v215, v195
	v_mov_b32_e32 v216, v198
	v_mov_b32_e32 v217, v199
	v_mov_b32_e32 v218, v202
	v_mov_b32_e32 v219, v203
	v_mov_b32_e32 v220, v208
	v_mov_b32_e32 v221, v209
	v_mov_b32_e32 v222, v210
	v_mov_b32_e32 v223, v211
.Lcwp_1946:
	s_waitcnt vmcnt(4)
	s_and_b64 vcc, exec, s[16:17]
	s_cbranch_vccnz .Lcnp_1946
	global_load_dwordx4 v[150:153], v[188:189], off
	s_nop 0
	global_load_dwordx4 v[154:157], v[196:197], off
	s_nop 0
	global_load_dwordx4 v[158:161], v[204:205], off
	s_nop 0
	global_load_dwordx4 v[162:165], v[214:215], off
	s_nop 0
	global_load_dwordx4 v[166:169], v[216:217], off
	s_nop 0
	global_load_dwordx4 v[170:173], v[218:219], off
	s_nop 0
	global_load_dwordx4 v[174:177], v[220:221], off
	s_nop 0
	global_load_dwordx4 v[178:181], v[222:223], off
.Lcnp_1946:
	ds_write2_b32 v58, v2, v3 offset1:1
	ds_write2_b32 v58, v4, v5 offset0:2 offset1:3
	ds_write2_b32 v59, v6, v7 offset1:1
	ds_write2_b32 v59, v8, v9 offset0:2 offset1:3
	ds_write2_b32 v60, v10, v11 offset1:1
	ds_write2_b32 v60, v12, v13 offset0:2 offset1:3
	ds_write2_b32 v61, v14, v15 offset1:1
	ds_write2_b32 v61, v16, v17 offset0:2 offset1:3
	ds_write2_b32 v62, v18, v19 offset1:1
	ds_write2_b32 v62, v20, v21 offset0:2 offset1:3
	ds_write2_b32 v63, v22, v23 offset1:1
	ds_write2_b32 v63, v24, v25 offset0:2 offset1:3
	ds_write2_b32 v64, v26, v27 offset1:1
	ds_write2_b32 v64, v28, v29 offset0:2 offset1:3
	ds_write2_b32 v65, v30, v31 offset1:1
	ds_write2_b32 v65, v32, v33 offset0:2 offset1:3
	s_waitcnt lgkmcnt(0)
	s_barrier

.Lcq1946_1963:
	s_movk_i32 s25, 0x400
	s_movk_i32 s36, 0x800
	s_mov_b32 s35, 0
	s_mov_b32 s24, 0
	s_cbranch_execz .Lcq1946_1956
	s_branch .Lcq1946_1957
.Lcq1946_1943:
	v_readlane_b32 s56, v250, 7
	v_readlane_b32 s70, v250, 21
	v_readlane_b32 s71, v250, 22
	s_mov_b32 s24, 0
	s_movk_i32 s36, 0x3600
	s_movk_i32 s25, 0x800
	s_mov_b64 s[22:23], s[70:71]
	s_mov_b64 s[18:19], s[12:13]
	s_mov_b32 s37, s33
	s_mov_b32 s35, 0
	v_readlane_b32 s57, v250, 8
	v_readlane_b32 s58, v250, 9
	v_readlane_b32 s59, v250, 10
	v_readlane_b32 s60, v250, 11
	v_readlane_b32 s61, v250, 12
	v_readlane_b32 s62, v250, 13
	v_readlane_b32 s63, v250, 14
	v_readlane_b32 s64, v250, 15
	v_readlane_b32 s65, v250, 16
	v_readlane_b32 s66, v250, 17
	v_readlane_b32 s67, v250, 18
	v_readlane_b32 s68, v250, 19
	v_readlane_b32 s69, v250, 20

.Lcwq_1946:
	s_waitcnt vmcnt(4)
	s_and_b64 vcc, exec, s[16:17]
	s_cbranch_vccnz .Lcnq_1946
	global_load_dwordx4 v[2:5], v[188:189], off
	s_nop 0
	global_load_dwordx4 v[6:9], v[196:197], off
	s_nop 0
	global_load_dwordx4 v[10:13], v[204:205], off
	s_nop 0
	global_load_dwordx4 v[14:17], v[214:215], off
	s_nop 0
	global_load_dwordx4 v[18:21], v[216:217], off
	s_nop 0
	global_load_dwordx4 v[22:25], v[218:219], off
	s_nop 0
	global_load_dwordx4 v[26:29], v[220:221], off
	s_nop 0
	global_load_dwordx4 v[30:33], v[222:223], off
.Lcnq_1946:
	ds_write2_b32 v58, v150, v151 offset1:1
	ds_write2_b32 v58, v152, v153 offset0:2 offset1:3
	ds_write2_b32 v59, v154, v155 offset1:1
	ds_write2_b32 v59, v156, v157 offset0:2 offset1:3
	ds_write2_b32 v60, v158, v159 offset1:1
	ds_write2_b32 v60, v160, v161 offset0:2 offset1:3
	ds_write2_b32 v61, v162, v163 offset1:1
	ds_write2_b32 v61, v164, v165 offset0:2 offset1:3
	ds_write2_b32 v62, v166, v167 offset1:1
	ds_write2_b32 v62, v168, v169 offset0:2 offset1:3
	ds_write2_b32 v63, v170, v171 offset1:1
	ds_write2_b32 v63, v172, v173 offset0:2 offset1:3
	ds_write2_b32 v64, v174, v175 offset1:1
	ds_write2_b32 v64, v176, v177 offset0:2 offset1:3
	ds_write2_b32 v65, v178, v179 offset1:1
	ds_write2_b32 v65, v180, v181 offset0:2 offset1:3
	s_waitcnt lgkmcnt(0)
	s_barrier
.Lcq1946_1945:
	s_add_i32 s30, s30, -1
	s_cmp_eq_u32 s15, 0
	v_add_u32_e32 v67, s4, v46
	v_lshlrev_b32_e32 v39, 1, v67
	s_cselect_b64 vcc, -1, 0
	s_ashr_i32 s15, s14, 31
	v_and_b32_e32 v39, 0xffffffe0, v39
	s_lshl_b64 s[14:15], s[14:15], 1
	v_add3_u32 v68, s1, v48, v39
	s_add_u32 s2, s2, s14
	s_addc_u32 s3, s3, s15
	v_mov_b32_e32 v39, v37
	v_cndmask_b32_e32 v67, v68, v67, vcc
	v_lshl_add_u64 v[72:73], s[2:3], 0, v[38:39]
	v_mad_u64_u32 v[68:69], s[2:3], v67, s0, 0
	v_ashrrev_i32_e32 v71, 31, v67
	v_mov_b32_e32 v70, v69
	v_mad_u64_u32 v[70:71], s[2:3], v71, s0, v[70:71]
	ds_read_b32 v39, v47
	ds_read_b32 v76, v47 offset:1028
	ds_read_b32 v77, v47 offset:2056
	ds_read_b32 v78, v47 offset:3084
	ds_read_b32 v79, v47 offset:4112
	ds_read_b32 v80, v47 offset:5140
	ds_read_b32 v81, v47 offset:6168
	ds_read_b32 v82, v47 offset:7196
	v_mov_b32_e32 v69, v70
	v_lshl_add_u64 v[74:75], v[68:69], 1, v[72:73]
	s_waitcnt lgkmcnt(7)
	v_and_b32_sdwa v68, v39, v66 dst_sel:DWORD dst_unused:UNUSED_PAD src0_sel:WORD_1 src1_sel:DWORD
	v_add3_u32 v39, v39, v68, s31
	s_waitcnt lgkmcnt(4)
	v_and_b32_sdwa v68, v78, v66 dst_sel:DWORD dst_unused:UNUSED_PAD src0_sel:WORD_1 src1_sel:DWORD
	v_and_b32_sdwa v69, v76, v66 dst_sel:DWORD dst_unused:UNUSED_PAD src0_sel:WORD_1 src1_sel:DWORD
	v_and_b32_sdwa v67, v77, v66 dst_sel:DWORD dst_unused:UNUSED_PAD src0_sel:WORD_1 src1_sel:DWORD
	v_add3_u32 v68, v78, v68, s31
	v_add3_u32 v69, v76, v69, s31
	v_add3_u32 v67, v77, v67, s31
	v_and_b32_e32 v68, 0xffff0000, v68
	v_and_b32_e32 v70, 0xffff0000, v69
	v_or_b32_sdwa v69, v68, v67 dst_sel:DWORD dst_unused:UNUSED_PAD src0_sel:DWORD src1_sel:WORD_1
	v_or_b32_sdwa v68, v70, v39 dst_sel:DWORD dst_unused:UNUSED_PAD src0_sel:DWORD src1_sel:WORD_1
	s_waitcnt lgkmcnt(0)
	v_and_b32_sdwa v70, v82, v66 dst_sel:DWORD dst_unused:UNUSED_PAD src0_sel:WORD_1 src1_sel:DWORD
	v_and_b32_sdwa v71, v80, v66 dst_sel:DWORD dst_unused:UNUSED_PAD src0_sel:WORD_1 src1_sel:DWORD
	v_and_b32_sdwa v39, v81, v66 dst_sel:DWORD dst_unused:UNUSED_PAD src0_sel:WORD_1 src1_sel:DWORD
	v_and_b32_sdwa v67, v79, v66 dst_sel:DWORD dst_unused:UNUSED_PAD src0_sel:WORD_1 src1_sel:DWORD
	v_add3_u32 v70, v82, v70, s31
	v_add3_u32 v71, v80, v71, s31
	v_add3_u32 v67, v79, v67, s31
	v_add3_u32 v39, v81, v39, s31
	v_and_b32_e32 v70, 0xffff0000, v70
	v_and_b32_e32 v76, 0xffff0000, v71
	v_or_b32_sdwa v71, v70, v39 dst_sel:DWORD dst_unused:UNUSED_PAD src0_sel:DWORD src1_sel:WORD_1
	v_or_b32_sdwa v70, v76, v67 dst_sel:DWORD dst_unused:UNUSED_PAD src0_sel:DWORD src1_sel:WORD_1
	global_store_dwordx4 v[74:75], v[68:71], off
	ds_read_b32 v39, v50
	ds_read_b32 v67, v50 offset:1028
	ds_read_b32 v76, v50 offset:2056
	ds_read_b32 v77, v50 offset:3084
	ds_read_b32 v78, v50 offset:4112
	ds_read_b32 v79, v50 offset:5140
	ds_read_b32 v80, v50 offset:6168
	ds_read_b32 v81, v50 offset:7196
	v_add_u32_e32 v68, s4, v49
	v_lshlrev_b32_e32 v69, 1, v68
	v_and_b32_e32 v69, 0xffffffe0, v69
	v_add3_u32 v69, s1, v51, v69
	v_cndmask_b32_e32 v68, v69, v68, vcc
	v_ashrrev_i32_e32 v71, 31, v68
	v_mad_u64_u32 v[68:69], s[2:3], v68, s0, 0
	v_mov_b32_e32 v70, v69
	v_mad_u64_u32 v[70:71], s[2:3], v71, s0, v[70:71]
	v_mov_b32_e32 v69, v70
	v_lshl_add_u64 v[74:75], v[68:69], 1, v[72:73]
	s_waitcnt lgkmcnt(7)
	v_and_b32_sdwa v69, v39, v66 dst_sel:DWORD dst_unused:UNUSED_PAD src0_sel:WORD_1 src1_sel:DWORD
	v_add3_u32 v39, v39, v69, s31
	s_waitcnt lgkmcnt(4)
	v_and_b32_sdwa v69, v77, v66 dst_sel:DWORD dst_unused:UNUSED_PAD src0_sel:WORD_1 src1_sel:DWORD
	v_and_b32_sdwa v70, v67, v66 dst_sel:DWORD dst_unused:UNUSED_PAD src0_sel:WORD_1 src1_sel:DWORD
	v_and_b32_sdwa v68, v76, v66 dst_sel:DWORD dst_unused:UNUSED_PAD src0_sel:WORD_1 src1_sel:DWORD
	v_add3_u32 v69, v77, v69, s31
	v_add3_u32 v67, v67, v70, s31
	v_add3_u32 v68, v76, v68, s31
	v_and_b32_e32 v69, 0xffff0000, v69
	v_and_b32_e32 v67, 0xffff0000, v67
	s_waitcnt lgkmcnt(0)
	v_and_b32_sdwa v70, v81, v66 dst_sel:DWORD dst_unused:UNUSED_PAD src0_sel:WORD_1 src1_sel:DWORD
	v_and_b32_sdwa v71, v79, v66 dst_sel:DWORD dst_unused:UNUSED_PAD src0_sel:WORD_1 src1_sel:DWORD
	v_or_b32_sdwa v69, v69, v68 dst_sel:DWORD dst_unused:UNUSED_PAD src0_sel:DWORD src1_sel:WORD_1
	v_or_b32_sdwa v68, v67, v39 dst_sel:DWORD dst_unused:UNUSED_PAD src0_sel:DWORD src1_sel:WORD_1
	v_and_b32_sdwa v39, v80, v66 dst_sel:DWORD dst_unused:UNUSED_PAD src0_sel:WORD_1 src1_sel:DWORD
	v_and_b32_sdwa v67, v78, v66 dst_sel:DWORD dst_unused:UNUSED_PAD src0_sel:WORD_1 src1_sel:DWORD
	v_add3_u32 v70, v81, v70, s31
	v_add3_u32 v71, v79, v71, s31
	v_add3_u32 v67, v78, v67, s31
	v_add3_u32 v39, v80, v39, s31
	v_and_b32_e32 v70, 0xffff0000, v70
	v_and_b32_e32 v76, 0xffff0000, v71
	v_or_b32_sdwa v71, v70, v39 dst_sel:DWORD dst_unused:UNUSED_PAD src0_sel:DWORD src1_sel:WORD_1
	v_or_b32_sdwa v70, v76, v67 dst_sel:DWORD dst_unused:UNUSED_PAD src0_sel:DWORD src1_sel:WORD_1
	global_store_dwordx4 v[74:75], v[68:71], off
	ds_read_b32 v39, v53
	ds_read_b32 v67, v53 offset:1028
	ds_read_b32 v76, v53 offset:2056
	ds_read_b32 v77, v53 offset:3084
	ds_read_b32 v78, v53 offset:4112
	ds_read_b32 v79, v53 offset:5140
	ds_read_b32 v80, v53 offset:6168
	ds_read_b32 v81, v53 offset:7196
	v_add_u32_e32 v68, s4, v52
	v_lshlrev_b32_e32 v69, 1, v68
	v_and_b32_e32 v69, 0xffffffe0, v69
	v_add3_u32 v69, s1, v54, v69
	v_cndmask_b32_e32 v68, v69, v68, vcc
	v_ashrrev_i32_e32 v71, 31, v68
	v_mad_u64_u32 v[68:69], s[2:3], v68, s0, 0
	v_mov_b32_e32 v70, v69
	v_mad_u64_u32 v[70:71], s[2:3], v71, s0, v[70:71]
	v_mov_b32_e32 v69, v70
	v_lshl_add_u64 v[74:75], v[68:69], 1, v[72:73]
	s_waitcnt lgkmcnt(7)
	v_and_b32_sdwa v69, v39, v66 dst_sel:DWORD dst_unused:UNUSED_PAD src0_sel:WORD_1 src1_sel:DWORD
	v_add3_u32 v39, v39, v69, s31
	s_waitcnt lgkmcnt(4)
	v_and_b32_sdwa v69, v77, v66 dst_sel:DWORD dst_unused:UNUSED_PAD src0_sel:WORD_1 src1_sel:DWORD
	v_and_b32_sdwa v70, v67, v66 dst_sel:DWORD dst_unused:UNUSED_PAD src0_sel:WORD_1 src1_sel:DWORD
	v_and_b32_sdwa v68, v76, v66 dst_sel:DWORD dst_unused:UNUSED_PAD src0_sel:WORD_1 src1_sel:DWORD
	v_add3_u32 v69, v77, v69, s31
	v_add3_u32 v67, v67, v70, s31
	v_add3_u32 v68, v76, v68, s31
	v_and_b32_e32 v69, 0xffff0000, v69
	v_and_b32_e32 v67, 0xffff0000, v67
	s_waitcnt lgkmcnt(0)
	v_and_b32_sdwa v70, v81, v66 dst_sel:DWORD dst_unused:UNUSED_PAD src0_sel:WORD_1 src1_sel:DWORD
	v_and_b32_sdwa v71, v79, v66 dst_sel:DWORD dst_unused:UNUSED_PAD src0_sel:WORD_1 src1_sel:DWORD
	v_or_b32_sdwa v69, v69, v68 dst_sel:DWORD dst_unused:UNUSED_PAD src0_sel:DWORD src1_sel:WORD_1
	v_or_b32_sdwa v68, v67, v39 dst_sel:DWORD dst_unused:UNUSED_PAD src0_sel:DWORD src1_sel:WORD_1
	v_and_b32_sdwa v39, v80, v66 dst_sel:DWORD dst_unused:UNUSED_PAD src0_sel:WORD_1 src1_sel:DWORD
	v_and_b32_sdwa v67, v78, v66 dst_sel:DWORD dst_unused:UNUSED_PAD src0_sel:WORD_1 src1_sel:DWORD
	v_add3_u32 v70, v81, v70, s31
	v_add3_u32 v71, v79, v71, s31
	v_add3_u32 v67, v78, v67, s31
	v_add3_u32 v39, v80, v39, s31
	v_and_b32_e32 v70, 0xffff0000, v70
	v_and_b32_e32 v76, 0xffff0000, v71
	v_or_b32_sdwa v71, v70, v39 dst_sel:DWORD dst_unused:UNUSED_PAD src0_sel:DWORD src1_sel:WORD_1
	v_or_b32_sdwa v70, v76, v67 dst_sel:DWORD dst_unused:UNUSED_PAD src0_sel:DWORD src1_sel:WORD_1
	global_store_dwordx4 v[74:75], v[68:71], off
	ds_read_b32 v39, v56
	ds_read_b32 v67, v56 offset:1028
	ds_read_b32 v74, v56 offset:2056
	ds_read_b32 v75, v56 offset:3084
	ds_read_b32 v76, v56 offset:4112
	ds_read_b32 v77, v56 offset:5140
	ds_read_b32 v78, v56 offset:6168
	ds_read_b32 v79, v56 offset:7196
	v_add_u32_e32 v68, s4, v55
	v_lshlrev_b32_e32 v69, 1, v68
	v_and_b32_e32 v69, 0xffffffe0, v69
	v_add3_u32 v69, s1, v57, v69
	v_cndmask_b32_e32 v68, v69, v68, vcc
	v_ashrrev_i32_e32 v71, 31, v68
	v_mad_u64_u32 v[68:69], s[2:3], v68, s0, 0
	v_mov_b32_e32 v70, v69
	v_mad_u64_u32 v[70:71], s[0:1], v71, s0, v[70:71]
	v_mov_b32_e32 v69, v70
	v_lshl_add_u64 v[72:73], v[68:69], 1, v[72:73]
	s_waitcnt lgkmcnt(7)
	v_and_b32_sdwa v69, v39, v66 dst_sel:DWORD dst_unused:UNUSED_PAD src0_sel:WORD_1 src1_sel:DWORD
	v_add3_u32 v39, v39, v69, s31
	s_waitcnt lgkmcnt(4)
	v_and_b32_sdwa v69, v75, v66 dst_sel:DWORD dst_unused:UNUSED_PAD src0_sel:WORD_1 src1_sel:DWORD
	v_and_b32_sdwa v70, v67, v66 dst_sel:DWORD dst_unused:UNUSED_PAD src0_sel:WORD_1 src1_sel:DWORD
	v_and_b32_sdwa v68, v74, v66 dst_sel:DWORD dst_unused:UNUSED_PAD src0_sel:WORD_1 src1_sel:DWORD
	v_add3_u32 v69, v75, v69, s31
	v_add3_u32 v67, v67, v70, s31
	v_add3_u32 v68, v74, v68, s31
	v_and_b32_e32 v69, 0xffff0000, v69
	v_and_b32_e32 v67, 0xffff0000, v67
	s_waitcnt lgkmcnt(0)
	v_and_b32_sdwa v70, v79, v66 dst_sel:DWORD dst_unused:UNUSED_PAD src0_sel:WORD_1 src1_sel:DWORD
	v_and_b32_sdwa v71, v77, v66 dst_sel:DWORD dst_unused:UNUSED_PAD src0_sel:WORD_1 src1_sel:DWORD
	v_or_b32_sdwa v69, v69, v68 dst_sel:DWORD dst_unused:UNUSED_PAD src0_sel:DWORD src1_sel:WORD_1
	v_or_b32_sdwa v68, v67, v39 dst_sel:DWORD dst_unused:UNUSED_PAD src0_sel:DWORD src1_sel:WORD_1
	v_and_b32_sdwa v39, v78, v66 dst_sel:DWORD dst_unused:UNUSED_PAD src0_sel:WORD_1 src1_sel:DWORD
	v_and_b32_sdwa v67, v76, v66 dst_sel:DWORD dst_unused:UNUSED_PAD src0_sel:WORD_1 src1_sel:DWORD
	v_add3_u32 v70, v79, v70, s31
	v_add3_u32 v71, v77, v71, s31
	v_add3_u32 v67, v76, v67, s31
	v_add3_u32 v39, v78, v39, s31
	v_and_b32_e32 v70, 0xffff0000, v70
	v_and_b32_e32 v74, 0xffff0000, v71
	v_or_b32_sdwa v71, v70, v39 dst_sel:DWORD dst_unused:UNUSED_PAD src0_sel:DWORD src1_sel:WORD_1
	v_or_b32_sdwa v70, v74, v67 dst_sel:DWORD dst_unused:UNUSED_PAD src0_sel:DWORD src1_sel:WORD_1
	s_add_i32 s29, s29, 1
	s_and_b64 vcc, exec, s[16:17]
	s_mov_b32 s34, s33
	s_mov_b32 s1, s35
	s_mov_b32 s15, s24
	s_mov_b32 s4, s20
	s_mov_b32 s14, s6
	s_mov_b32 s0, s25
	s_mov_b64 s[2:3], s[18:19]
	global_store_dwordx4 v[72:73], v[68:71], off
	s_barrier
	s_cbranch_vccnz .LBB0_1964
	s_branch .LBB0_1946

.LBB0_1991:
	s_waitcnt vmcnt(11)
	v_add_u32_e32 v2, 0x800, v34
	s_lshr_b32 s0, s8, 8
	v_ashrrev_i32_e32 v42, 6, v2
	v_cvt_f32_u32_e32 v2, s0
	s_sub_i32 s9, 0, s0
	s_abs_i32 s5, s10
	s_ashr_i32 s4, s10, 31
	v_rcp_iflag_f32_e32 v2, v2
	v_add_u32_e32 v3, 0xa00, v34
	v_ashrrev_i32_e32 v43, 6, v3
	v_add_u32_e32 v3, 0xc00, v34
	v_mul_f32_e32 v2, 0x4f7ffffe, v2
	v_cvt_u32_f32_e32 v2, v2
	v_lshlrev_b32_e32 v1, 2, v34
	v_ashrrev_i32_e32 v44, 6, v3
	v_add_u32_e32 v3, 0xe00, v34
	v_readfirstlane_b32 s11, v2
	s_mul_i32 s9, s9, s11
	s_mul_hi_u32 s9, s11, s9
	s_add_i32 s11, s11, s9
	s_mul_hi_u32 s9, s5, s11
	s_mul_i32 s11, s9, s0
	s_sub_i32 s5, s5, s11
	s_add_i32 s11, s9, 1
	s_sub_i32 s12, s5, s0
	s_cmp_ge_u32 s5, s0
	s_cselect_b32 s9, s11, s9
	s_cselect_b32 s5, s12, s5
	s_add_i32 s11, s9, 1
	s_cmp_ge_u32 s5, s0
	s_cselect_b32 s5, s11, s9
	s_xor_b32 s5, s5, s4
	s_sub_i32 s9, s5, s4
	s_mul_i32 s0, s9, s0
	s_sub_i32 s0, s10, s0
	s_lshl_b32 s4, s0, 8
	s_ashr_i32 s5, s4, 31
	s_lshl_b64 s[10:11], s[4:5], 2
	s_add_u32 s6, s6, s10
	v_and_b32_e32 v38, 0xfc, v1
	v_ashrrev_i32_e32 v45, 6, v3
	s_addc_u32 s7, s7, s11
	s_lshl_b32 s14, s9, 6
	v_mov_b32_e32 v37, 0
	v_lshlrev_b32_e32 v36, 2, v38
	v_add_u32_e32 v4, s14, v45
	v_lshl_add_u64 v[2:3], s[6:7], 0, v[36:37]
	s_waitcnt vmcnt(10)
	v_ashrrev_i32_e32 v7, 31, v4
	v_mad_u64_u32 v[4:5], s[6:7], v4, s8, 0
	v_mov_b32_e32 v6, v5
	v_mad_u64_u32 v[6:7], s[6:7], v7, s8, v[6:7]
	v_mov_b32_e32 v5, v6
	v_add_u32_e32 v6, s14, v44
	v_ashrrev_i32_e32 v9, 31, v6
	v_mad_u64_u32 v[6:7], s[6:7], v6, s8, 0
	v_mov_b32_e32 v8, v7
	v_mad_u64_u32 v[8:9], s[6:7], v9, s8, v[8:9]
	v_lshl_add_u64 v[4:5], v[4:5], 2, v[2:3]
	v_mov_b32_e32 v7, v8
	v_lshl_add_u64 v[6:7], v[6:7], 2, v[2:3]
	global_load_dwordx4 v[30:33], v[4:5], off
	global_load_dwordx4 v[26:29], v[6:7], off
	v_add_u32_e32 v4, s14, v43
	v_ashrrev_i32_e32 v7, 31, v4
	v_mad_u64_u32 v[4:5], s[6:7], v4, s8, 0
	v_mov_b32_e32 v6, v5
	v_mad_u64_u32 v[6:7], s[6:7], v7, s8, v[6:7]
	v_mov_b32_e32 v5, v6
	v_add_u32_e32 v6, s14, v42
	v_ashrrev_i32_e32 v9, 31, v6
	v_mad_u64_u32 v[6:7], s[6:7], v6, s8, 0
	v_mov_b32_e32 v8, v7
	v_add_u32_e32 v55, 0x600, v34
	v_mad_u64_u32 v[8:9], s[6:7], v9, s8, v[8:9]
	v_ashrrev_i32_e32 v41, 6, v55
	v_lshl_add_u64 v[4:5], v[4:5], 2, v[2:3]
	v_mov_b32_e32 v7, v8
	v_lshl_add_u64 v[6:7], v[6:7], 2, v[2:3]
	global_load_dwordx4 v[22:25], v[4:5], off
	global_load_dwordx4 v[18:21], v[6:7], off
	v_add_u32_e32 v4, s14, v41
	v_ashrrev_i32_e32 v7, 31, v4
	v_mad_u64_u32 v[4:5], s[6:7], v4, s8, 0
	v_add_u32_e32 v52, 0x400, v34
	v_mov_b32_e32 v6, v5
	v_ashrrev_i32_e32 v40, 6, v52
	v_mad_u64_u32 v[6:7], s[6:7], v7, s8, v[6:7]
	v_mov_b32_e32 v5, v6
	v_add_u32_e32 v6, s14, v40
	v_ashrrev_i32_e32 v9, 31, v6
	v_mad_u64_u32 v[6:7], s[6:7], v6, s8, 0
	v_mov_b32_e32 v8, v7
	v_add_u32_e32 v35, 0x200, v34
	v_mad_u64_u32 v[8:9], s[6:7], v9, s8, v[8:9]
	v_ashrrev_i32_e32 v39, 6, v35
	v_lshl_add_u64 v[4:5], v[4:5], 2, v[2:3]
	v_mov_b32_e32 v7, v8
	v_lshl_add_u64 v[6:7], v[6:7], 2, v[2:3]
	global_load_dwordx4 v[14:17], v[4:5], off
	global_load_dwordx4 v[10:13], v[6:7], off
	v_add_u32_e32 v4, s14, v39
	v_ashrrev_i32_e32 v7, 31, v4
	v_mad_u64_u32 v[4:5], s[6:7], v4, s8, 0
	v_mov_b32_e32 v6, v5
	v_ashrrev_i32_e32 v1, 6, v34
	v_mad_u64_u32 v[6:7], s[6:7], v7, s8, v[6:7]
	v_mov_b32_e32 v5, v6
	v_add_u32_e32 v6, s14, v1
	v_ashrrev_i32_e32 v9, 31, v6
	v_mad_u64_u32 v[6:7], s[6:7], v6, s8, 0
	v_mov_b32_e32 v8, v7
	v_mad_u64_u32 v[8:9], s[6:7], v9, s8, v[8:9]
	v_mov_b32_e32 v7, v8
	v_lshl_add_u64 v[4:5], v[4:5], 2, v[2:3]
	v_lshl_add_u64 v[2:3], v[6:7], 2, v[2:3]
	global_load_dwordx4 v[6:9], v[4:5], off
	s_nop 0
	global_load_dwordx4 v[2:5], v[2:3], off
	v_lshlrev_b32_e32 v46, 3, v34
	v_and_b32_e32 v66, 56, v46
	s_movk_i32 s0, 0x404
	v_readlane_b32 s12, v251, 60
	v_mad_u32_u24 v56, v66, s0, 0
	v_mul_lo_u32 v58, v1, s0
	v_mul_lo_u32 v59, v39, s0
	v_mul_lo_u32 v60, v40, s0
	v_mul_lo_u32 v61, v41, s0
	v_mul_lo_u32 v62, v42, s0
	v_mul_lo_u32 v63, v43, s0
	v_mul_lo_u32 v64, v44, s0
	v_mul_lo_u32 v65, v45, s0
	v_readlane_b32 s13, v251, 61
	s_add_u32 s0, s12, 0x1e940000
	s_addc_u32 s5, s13, 0
	s_add_u32 s8, s12, 0x16940000
	s_addc_u32 s9, s13, 0
	s_add_u32 s10, s12, 0x16140000
	s_addc_u32 s11, s13, 0
	s_add_u32 s27, s12, 0x15540000
	s_addc_u32 s28, s13, 0
	v_add_u32_e32 v36, 0, v36
	v_ashrrev_i32_e32 v46, 3, v34
	v_ashrrev_i32_e32 v49, 3, v35
	v_ashrrev_i32_e32 v52, 3, v52
	v_ashrrev_i32_e32 v55, 3, v55
	s_add_u32 s12, s12, 0x11f40000
	s_mov_b32 s7, 0
	v_lshl_add_u32 v47, v46, 2, v56
	v_and_b32_e32 v48, 15, v46
	v_lshl_add_u32 v50, v49, 2, v56
	v_and_b32_e32 v51, 15, v49
	v_lshl_add_u32 v53, v52, 2, v56
	v_and_b32_e32 v54, 15, v52
	v_lshl_add_u32 v56, v55, 2, v56
	v_and_b32_e32 v57, 15, v55
	s_addc_u32 s13, s13, 0
	s_add_i32 s29, s16, 0xfffffce1
	s_mov_b32 s30, 25
	v_add_u32_e32 v58, v36, v58
	v_add_u32_e32 v59, v36, v59
	v_add_u32_e32 v60, v36, v60
	v_add_u32_e32 v61, v36, v61
	v_add_u32_e32 v62, v36, v62
	v_add_u32_e32 v63, v36, v63
	v_add_u32_e32 v64, v36, v64
	v_add_u32_e32 v65, v36, v65
	v_lshlrev_b32_e32 v36, 2, v38
	v_lshlrev_b32_e32 v34, 1, v66
	s_movk_i32 s31, 0x7fff
	v_mov_b32_e32 v38, 1
	s_mov_b32 s24, s15
	s_mov_b32 s25, s26
	s_mov_b64 s[18:19], s[2:3]
	s_waitcnt vmcnt(0)
	s_branch .LBB0_1995
.LBB0_1995:
	s_add_i32 s33, s34, 1
	s_cmp_lt_u32 s30, 2
	s_cselect_b64 s[16:17], -1, 0
	s_and_b64 vcc, exec, s[16:17]
	s_mov_b32 s35, s1
	s_mov_b32 s20, s4
	s_mov_b32 s6, s14
	s_cbranch_vccnz .Lcwp_1995
	s_add_i32 s6, s29, 0x93f
	s_cmpk_lt_i32 s6, 0x6bf
	s_cbranch_scc1 .LBB0_1992
	s_add_i32 s6, s29, 0x940
	s_cmpk_gt_u32 s6, 0x83f
	s_mov_b64 s[20:21], -1
	s_cbranch_scc0 .LBB0_2010
	s_cmpk_gt_u32 s6, 0x93f
	s_cbranch_scc0 .LBB0_2007
	s_mul_hi_u32 s6, s29, 0xaaaaaaab
	s_lshr_b32 s6, s6, 8
	s_mul_i32 s18, s6, 0xfffffe80
	s_add_i32 s34, s34, s18
	s_addk_i32 s34, 0xf6c1
	s_add_i32 s38, s29, s18
	s_cmpk_gt_i32 s38, 0x7f
	s_cbranch_scc0 .LBB0_2004
	s_lshl_b64 s[20:21], s[6:7], 23
	s_cmpk_gt_u32 s38, 0xff
	s_mov_b64 s[24:25], -1
	s_cbranch_scc0 .LBB0_2002
	s_add_i32 s37, s34, 0xffffff00
	s_add_u32 s22, s88, s20
	s_addc_u32 s23, s89, s21
	s_lshl_b64 s[18:19], s[6:7], 22
	s_add_u32 s18, s0, s18
	s_addc_u32 s19, s5, s19
	s_mov_b64 s[24:25], 0

.LBB0_2012:
	s_movk_i32 s25, 0x400
	s_movk_i32 s36, 0x800
	s_mov_b32 s35, 0
	s_mov_b32 s24, 0
	s_cbranch_execz .LBB0_2005
	s_branch .LBB0_2006
.LBB0_1992:
	v_readlane_b32 s56, v250, 7
	v_readlane_b32 s70, v250, 21
	v_readlane_b32 s71, v250, 22
	s_mov_b32 s24, 0
	s_movk_i32 s36, 0x3600
	s_movk_i32 s25, 0x800
	s_mov_b64 s[22:23], s[70:71]
	s_mov_b64 s[18:19], s[12:13]
	s_mov_b32 s37, s33
	s_mov_b32 s35, 0
	v_readlane_b32 s57, v250, 8
	v_readlane_b32 s58, v250, 9
	v_readlane_b32 s59, v250, 10
	v_readlane_b32 s60, v250, 11
	v_readlane_b32 s61, v250, 12
	v_readlane_b32 s62, v250, 13
	v_readlane_b32 s63, v250, 14
	v_readlane_b32 s64, v250, 15
	v_readlane_b32 s65, v250, 16
	v_readlane_b32 s66, v250, 17
	v_readlane_b32 s67, v250, 18
	v_readlane_b32 s68, v250, 19
	v_readlane_b32 s69, v250, 20
.LBB0_1993:
	s_lshr_b32 s20, s36, 8
	v_cvt_f32_u32_e32 v182, s20
	s_sub_i32 s34, 0, s20
	s_abs_i32 s21, s37
	s_ashr_i32 s6, s37, 31
	v_rcp_iflag_f32_e32 v182, v182
	s_nop 0
	v_mul_f32_e32 v182, 0x4f7ffffe, v182
	v_cvt_u32_f32_e32 v182, v182
	s_nop 0
	v_readfirstlane_b32 s38, v182
	s_mul_i32 s34, s34, s38
	s_mul_hi_u32 s34, s38, s34
	s_add_i32 s38, s38, s34
	s_mul_hi_u32 s34, s21, s38
	s_mul_i32 s38, s34, s20
	s_sub_i32 s21, s21, s38
	s_add_i32 s39, s34, 1
	s_sub_i32 s38, s21, s20
	s_cmp_ge_u32 s21, s20
	s_cselect_b32 s34, s39, s34
	s_cselect_b32 s21, s38, s21
	s_add_i32 s38, s34, 1
	s_cmp_ge_u32 s21, s20
	s_cselect_b32 s21, s38, s34
	s_xor_b32 s21, s21, s6
	s_sub_i32 s21, s21, s6
	s_lshl_b32 s6, s21, 6
	s_mul_i32 s21, s21, s20
	s_sub_i32 s20, s37, s21
	s_lshl_b32 s20, s20, 8
	s_ashr_i32 s21, s20, 31
	s_lshl_b64 s[38:39], s[20:21], 2
	s_add_u32 s22, s22, s38
	v_add_u32_e32 v182, s6, v1
	s_addc_u32 s23, s23, s39
	v_add_u32_e32 v190, s6, v40
	v_add_u32_e32 v198, s6, v42
	v_add_u32_e32 v208, s6, v44
	v_ashrrev_i32_e32 v185, 31, v182
	v_lshl_add_u64 v[206:207], s[22:23], 0, v[36:37]
	v_mad_u64_u32 v[182:183], s[22:23], v182, s36, 0
	v_ashrrev_i32_e32 v193, 31, v190
	v_mad_u64_u32 v[190:191], s[22:23], v190, s36, 0
	v_ashrrev_i32_e32 v201, 31, v198
	v_mad_u64_u32 v[198:199], s[22:23], v198, s36, 0
	v_ashrrev_i32_e32 v211, 31, v208
	v_mad_u64_u32 v[208:209], s[22:23], v208, s36, 0
	v_mov_b32_e32 v184, v183
	v_mov_b32_e32 v192, v191
	v_mov_b32_e32 v200, v199
	v_mov_b32_e32 v210, v209
	v_mad_u64_u32 v[184:185], s[22:23], v185, s36, v[184:185]
	v_mad_u64_u32 v[192:193], s[22:23], v193, s36, v[192:193]
	v_mad_u64_u32 v[200:201], s[22:23], v201, s36, v[200:201]
	v_mad_u64_u32 v[210:211], s[22:23], v211, s36, v[210:211]
	v_mov_b32_e32 v183, v184
	v_add_u32_e32 v184, s6, v39
	v_mov_b32_e32 v191, v192
	v_add_u32_e32 v192, s6, v41
	v_mov_b32_e32 v199, v200
	v_add_u32_e32 v200, s6, v43
	v_mov_b32_e32 v209, v210
	v_add_u32_e32 v210, s6, v45
	v_ashrrev_i32_e32 v187, 31, v184
	v_mad_u64_u32 v[184:185], s[22:23], v184, s36, 0
	v_ashrrev_i32_e32 v195, 31, v192
	v_mad_u64_u32 v[192:193], s[22:23], v192, s36, 0
	v_ashrrev_i32_e32 v203, 31, v200
	v_mad_u64_u32 v[200:201], s[22:23], v200, s36, 0
	v_ashrrev_i32_e32 v213, 31, v210
	v_mad_u64_u32 v[210:211], s[22:23], v210, s36, 0
	v_mov_b32_e32 v186, v185
	v_mov_b32_e32 v194, v193
	v_mov_b32_e32 v202, v201
	v_mov_b32_e32 v212, v211
	v_mad_u64_u32 v[186:187], s[22:23], v187, s36, v[186:187]
	v_mad_u64_u32 v[194:195], s[22:23], v195, s36, v[194:195]
	v_mad_u64_u32 v[202:203], s[22:23], v203, s36, v[202:203]
	v_mad_u64_u32 v[212:213], s[22:23], v213, s36, v[212:213]
	v_mov_b32_e32 v185, v186
	v_mov_b32_e32 v193, v194
	v_mov_b32_e32 v201, v202
	v_mov_b32_e32 v211, v212
	v_lshl_add_u64 v[182:183], v[182:183], 2, v[206:207]
	v_lshl_add_u64 v[186:187], v[184:185], 2, v[206:207]
	v_lshl_add_u64 v[190:191], v[190:191], 2, v[206:207]
	v_lshl_add_u64 v[194:195], v[192:193], 2, v[206:207]
	v_lshl_add_u64 v[198:199], v[198:199], 2, v[206:207]
	v_lshl_add_u64 v[202:203], v[200:201], 2, v[206:207]
	v_lshl_add_u64 v[208:209], v[208:209], 2, v[206:207]
	v_lshl_add_u64 v[210:211], v[210:211], 2, v[206:207]
	v_mov_b32_e32 v188, v182
	v_mov_b32_e32 v189, v183
	v_mov_b32_e32 v196, v186
	v_mov_b32_e32 v197, v187
	v_mov_b32_e32 v204, v190
	v_mov_b32_e32 v205, v191
	v_mov_b32_e32 v214, v194
	v_mov_b32_e32 v215, v195
	v_mov_b32_e32 v216, v198
	v_mov_b32_e32 v217, v199
	v_mov_b32_e32 v218, v202
	v_mov_b32_e32 v219, v203
	v_mov_b32_e32 v220, v208
	v_mov_b32_e32 v221, v209
	v_mov_b32_e32 v222, v210
	v_mov_b32_e32 v223, v211

.Lcq1995_2012:
	s_movk_i32 s25, 0x400
	s_movk_i32 s36, 0x800
	s_mov_b32 s35, 0
	s_mov_b32 s24, 0
	s_cbranch_execz .Lcq1995_2005
	s_branch .Lcq1995_2006
.Lcq1995_1992:
	v_readlane_b32 s56, v250, 7
	v_readlane_b32 s70, v250, 21
	v_readlane_b32 s71, v250, 22
	s_mov_b32 s24, 0
	s_movk_i32 s36, 0x3600
	s_movk_i32 s25, 0x800
	s_mov_b64 s[22:23], s[70:71]
	s_mov_b64 s[18:19], s[12:13]
	s_mov_b32 s37, s33
	s_mov_b32 s35, 0
	v_readlane_b32 s57, v250, 8
	v_readlane_b32 s58, v250, 9
	v_readlane_b32 s59, v250, 10
	v_readlane_b32 s60, v250, 11
	v_readlane_b32 s61, v250, 12
	v_readlane_b32 s62, v250, 13
	v_readlane_b32 s63, v250, 14
	v_readlane_b32 s64, v250, 15
	v_readlane_b32 s65, v250, 16
	v_readlane_b32 s66, v250, 17
	v_readlane_b32 s67, v250, 18
	v_readlane_b32 s68, v250, 19
	v_readlane_b32 s69, v250, 20

.Lcq1995_1994:
	s_add_i32 s30, s30, -1
	s_cmp_eq_u32 s15, 0
	v_add_u32_e32 v66, s4, v46
	v_lshlrev_b32_e32 v35, 1, v66
	s_cselect_b64 vcc, -1, 0
	s_ashr_i32 s15, s14, 31
	v_and_b32_e32 v35, 0xffffffe0, v35
	s_lshl_b64 s[14:15], s[14:15], 1
	v_add3_u32 v67, s1, v48, v35
	s_add_u32 s2, s2, s14
	s_addc_u32 s3, s3, s15
	v_mov_b32_e32 v35, v37
	v_cndmask_b32_e32 v66, v67, v66, vcc
	v_lshl_add_u64 v[70:71], s[2:3], 0, v[34:35]
	v_ashrrev_i32_e32 v69, 31, v66
	v_mad_u64_u32 v[66:67], s[2:3], v66, s26, 0
	v_mov_b32_e32 v68, v67
	ds_read_b32 v35, v47
	ds_read_b32 v74, v47 offset:1028
	ds_read_b32 v75, v47 offset:2056
	ds_read_b32 v76, v47 offset:3084
	ds_read_b32 v77, v47 offset:4112
	ds_read_b32 v78, v47 offset:5140
	ds_read_b32 v79, v47 offset:6168
	ds_read_b32 v80, v47 offset:7196
	v_mad_u64_u32 v[68:69], s[2:3], v69, s26, v[68:69]
	v_mov_b32_e32 v67, v68
	v_lshl_add_u64 v[72:73], v[66:67], 1, v[70:71]
	s_waitcnt lgkmcnt(7)
	v_and_b32_sdwa v67, v35, v38 dst_sel:DWORD dst_unused:UNUSED_PAD src0_sel:WORD_1 src1_sel:DWORD
	v_add3_u32 v35, v35, v67, s31
	s_waitcnt lgkmcnt(4)
	v_and_b32_sdwa v67, v76, v38 dst_sel:DWORD dst_unused:UNUSED_PAD src0_sel:WORD_1 src1_sel:DWORD
	v_and_b32_sdwa v68, v74, v38 dst_sel:DWORD dst_unused:UNUSED_PAD src0_sel:WORD_1 src1_sel:DWORD
	v_and_b32_sdwa v66, v75, v38 dst_sel:DWORD dst_unused:UNUSED_PAD src0_sel:WORD_1 src1_sel:DWORD
	v_add3_u32 v67, v76, v67, s31
	v_add3_u32 v68, v74, v68, s31
	v_add3_u32 v66, v75, v66, s31
	v_and_b32_e32 v67, 0xffff0000, v67
	v_and_b32_e32 v68, 0xffff0000, v68
	s_waitcnt lgkmcnt(0)
	v_and_b32_sdwa v69, v80, v38 dst_sel:DWORD dst_unused:UNUSED_PAD src0_sel:WORD_1 src1_sel:DWORD
	v_and_b32_sdwa v74, v78, v38 dst_sel:DWORD dst_unused:UNUSED_PAD src0_sel:WORD_1 src1_sel:DWORD
	v_or_b32_sdwa v67, v67, v66 dst_sel:DWORD dst_unused:UNUSED_PAD src0_sel:DWORD src1_sel:WORD_1
	v_or_b32_sdwa v66, v68, v35 dst_sel:DWORD dst_unused:UNUSED_PAD src0_sel:DWORD src1_sel:WORD_1
	v_and_b32_sdwa v35, v79, v38 dst_sel:DWORD dst_unused:UNUSED_PAD src0_sel:WORD_1 src1_sel:DWORD
	v_and_b32_sdwa v68, v77, v38 dst_sel:DWORD dst_unused:UNUSED_PAD src0_sel:WORD_1 src1_sel:DWORD
	v_add3_u32 v69, v80, v69, s31
	v_add3_u32 v74, v78, v74, s31
	v_add3_u32 v68, v77, v68, s31
	v_add3_u32 v35, v79, v35, s31
	v_and_b32_e32 v69, 0xffff0000, v69
	v_and_b32_e32 v74, 0xffff0000, v74
	v_or_b32_sdwa v69, v69, v35 dst_sel:DWORD dst_unused:UNUSED_PAD src0_sel:DWORD src1_sel:WORD_1
	v_or_b32_sdwa v68, v74, v68 dst_sel:DWORD dst_unused:UNUSED_PAD src0_sel:DWORD src1_sel:WORD_1
	global_store_dwordx4 v[72:73], v[66:69], off
	ds_read_b32 v35, v50
	ds_read_b32 v74, v50 offset:1028
	ds_read_b32 v75, v50 offset:2056
	ds_read_b32 v76, v50 offset:3084
	ds_read_b32 v77, v50 offset:4112
	ds_read_b32 v78, v50 offset:5140
	ds_read_b32 v79, v50 offset:6168
	ds_read_b32 v80, v50 offset:7196
	v_add_u32_e32 v66, s4, v49
	v_lshlrev_b32_e32 v67, 1, v66
	v_and_b32_e32 v67, 0xffffffe0, v67
	v_add3_u32 v67, s1, v51, v67
	v_cndmask_b32_e32 v66, v67, v66, vcc
	v_ashrrev_i32_e32 v69, 31, v66
	v_mad_u64_u32 v[66:67], s[2:3], v66, s26, 0
	v_mov_b32_e32 v68, v67
	v_mad_u64_u32 v[68:69], s[2:3], v69, s26, v[68:69]
	v_mov_b32_e32 v67, v68
	v_lshl_add_u64 v[72:73], v[66:67], 1, v[70:71]
	s_waitcnt lgkmcnt(7)
	v_and_b32_sdwa v67, v35, v38 dst_sel:DWORD dst_unused:UNUSED_PAD src0_sel:WORD_1 src1_sel:DWORD
	v_add3_u32 v35, v35, v67, s31
	s_waitcnt lgkmcnt(4)
	v_and_b32_sdwa v67, v76, v38 dst_sel:DWORD dst_unused:UNUSED_PAD src0_sel:WORD_1 src1_sel:DWORD
	v_and_b32_sdwa v68, v74, v38 dst_sel:DWORD dst_unused:UNUSED_PAD src0_sel:WORD_1 src1_sel:DWORD
	v_and_b32_sdwa v66, v75, v38 dst_sel:DWORD dst_unused:UNUSED_PAD src0_sel:WORD_1 src1_sel:DWORD
	v_add3_u32 v67, v76, v67, s31
	v_add3_u32 v68, v74, v68, s31
	v_add3_u32 v66, v75, v66, s31
	v_and_b32_e32 v67, 0xffff0000, v67
	v_and_b32_e32 v68, 0xffff0000, v68
	s_waitcnt lgkmcnt(0)
	v_and_b32_sdwa v69, v80, v38 dst_sel:DWORD dst_unused:UNUSED_PAD src0_sel:WORD_1 src1_sel:DWORD
	v_and_b32_sdwa v74, v78, v38 dst_sel:DWORD dst_unused:UNUSED_PAD src0_sel:WORD_1 src1_sel:DWORD
	v_or_b32_sdwa v67, v67, v66 dst_sel:DWORD dst_unused:UNUSED_PAD src0_sel:DWORD src1_sel:WORD_1
	v_or_b32_sdwa v66, v68, v35 dst_sel:DWORD dst_unused:UNUSED_PAD src0_sel:DWORD src1_sel:WORD_1
	v_and_b32_sdwa v35, v79, v38 dst_sel:DWORD dst_unused:UNUSED_PAD src0_sel:WORD_1 src1_sel:DWORD
	v_and_b32_sdwa v68, v77, v38 dst_sel:DWORD dst_unused:UNUSED_PAD src0_sel:WORD_1 src1_sel:DWORD
	v_add3_u32 v69, v80, v69, s31
	v_add3_u32 v74, v78, v74, s31
	v_add3_u32 v68, v77, v68, s31
	v_add3_u32 v35, v79, v35, s31
	v_and_b32_e32 v69, 0xffff0000, v69
	v_and_b32_e32 v74, 0xffff0000, v74
	v_or_b32_sdwa v69, v69, v35 dst_sel:DWORD dst_unused:UNUSED_PAD src0_sel:DWORD src1_sel:WORD_1
	v_or_b32_sdwa v68, v74, v68 dst_sel:DWORD dst_unused:UNUSED_PAD src0_sel:DWORD src1_sel:WORD_1
	global_store_dwordx4 v[72:73], v[66:69], off
	ds_read_b32 v35, v53
	ds_read_b32 v74, v53 offset:1028
	ds_read_b32 v75, v53 offset:2056
	ds_read_b32 v76, v53 offset:3084
	ds_read_b32 v77, v53 offset:4112
	ds_read_b32 v78, v53 offset:5140
	ds_read_b32 v79, v53 offset:6168
	ds_read_b32 v80, v53 offset:7196
	v_add_u32_e32 v66, s4, v52
	v_lshlrev_b32_e32 v67, 1, v66
	v_and_b32_e32 v67, 0xffffffe0, v67
	v_add3_u32 v67, s1, v54, v67
	v_cndmask_b32_e32 v66, v67, v66, vcc
	v_ashrrev_i32_e32 v69, 31, v66
	v_mad_u64_u32 v[66:67], s[2:3], v66, s26, 0
	v_mov_b32_e32 v68, v67
	v_mad_u64_u32 v[68:69], s[2:3], v69, s26, v[68:69]
	v_mov_b32_e32 v67, v68
	v_lshl_add_u64 v[72:73], v[66:67], 1, v[70:71]
	s_waitcnt lgkmcnt(7)
	v_and_b32_sdwa v67, v35, v38 dst_sel:DWORD dst_unused:UNUSED_PAD src0_sel:WORD_1 src1_sel:DWORD
	v_add3_u32 v35, v35, v67, s31
	s_waitcnt lgkmcnt(4)
	v_and_b32_sdwa v67, v76, v38 dst_sel:DWORD dst_unused:UNUSED_PAD src0_sel:WORD_1 src1_sel:DWORD
	v_and_b32_sdwa v68, v74, v38 dst_sel:DWORD dst_unused:UNUSED_PAD src0_sel:WORD_1 src1_sel:DWORD
	v_and_b32_sdwa v66, v75, v38 dst_sel:DWORD dst_unused:UNUSED_PAD src0_sel:WORD_1 src1_sel:DWORD
	v_add3_u32 v67, v76, v67, s31
	v_add3_u32 v68, v74, v68, s31
	v_add3_u32 v66, v75, v66, s31
	v_and_b32_e32 v67, 0xffff0000, v67
	v_and_b32_e32 v68, 0xffff0000, v68
	s_waitcnt lgkmcnt(0)
	v_and_b32_sdwa v69, v80, v38 dst_sel:DWORD dst_unused:UNUSED_PAD src0_sel:WORD_1 src1_sel:DWORD
	v_and_b32_sdwa v74, v78, v38 dst_sel:DWORD dst_unused:UNUSED_PAD src0_sel:WORD_1 src1_sel:DWORD
	v_or_b32_sdwa v67, v67, v66 dst_sel:DWORD dst_unused:UNUSED_PAD src0_sel:DWORD src1_sel:WORD_1
	v_or_b32_sdwa v66, v68, v35 dst_sel:DWORD dst_unused:UNUSED_PAD src0_sel:DWORD src1_sel:WORD_1
	v_and_b32_sdwa v35, v79, v38 dst_sel:DWORD dst_unused:UNUSED_PAD src0_sel:WORD_1 src1_sel:DWORD
	v_and_b32_sdwa v68, v77, v38 dst_sel:DWORD dst_unused:UNUSED_PAD src0_sel:WORD_1 src1_sel:DWORD
	v_add3_u32 v69, v80, v69, s31
	v_add3_u32 v74, v78, v74, s31
	v_add3_u32 v68, v77, v68, s31
	v_add3_u32 v35, v79, v35, s31
	v_and_b32_e32 v69, 0xffff0000, v69
	v_and_b32_e32 v74, 0xffff0000, v74
	v_or_b32_sdwa v69, v69, v35 dst_sel:DWORD dst_unused:UNUSED_PAD src0_sel:DWORD src1_sel:WORD_1
	v_or_b32_sdwa v68, v74, v68 dst_sel:DWORD dst_unused:UNUSED_PAD src0_sel:DWORD src1_sel:WORD_1
	global_store_dwordx4 v[72:73], v[66:69], off
	ds_read_b32 v35, v56
	ds_read_b32 v72, v56 offset:1028
	ds_read_b32 v73, v56 offset:2056
	ds_read_b32 v74, v56 offset:3084
	ds_read_b32 v75, v56 offset:4112
	ds_read_b32 v76, v56 offset:5140
	ds_read_b32 v77, v56 offset:6168
	ds_read_b32 v78, v56 offset:7196
	v_add_u32_e32 v66, s4, v55
	v_lshlrev_b32_e32 v67, 1, v66
	v_and_b32_e32 v67, 0xffffffe0, v67
	v_add3_u32 v67, s1, v57, v67
	v_cndmask_b32_e32 v66, v67, v66, vcc
	v_ashrrev_i32_e32 v69, 31, v66
	v_mad_u64_u32 v[66:67], s[2:3], v66, s26, 0
	v_mov_b32_e32 v68, v67
	v_mad_u64_u32 v[68:69], s[2:3], v69, s26, v[68:69]
	v_mov_b32_e32 v67, v68
	v_lshl_add_u64 v[70:71], v[66:67], 1, v[70:71]
	s_waitcnt lgkmcnt(7)
	v_and_b32_sdwa v67, v35, v38 dst_sel:DWORD dst_unused:UNUSED_PAD src0_sel:WORD_1 src1_sel:DWORD
	v_add3_u32 v35, v35, v67, s31
	s_waitcnt lgkmcnt(4)
	v_and_b32_sdwa v67, v74, v38 dst_sel:DWORD dst_unused:UNUSED_PAD src0_sel:WORD_1 src1_sel:DWORD
	v_and_b32_sdwa v68, v72, v38 dst_sel:DWORD dst_unused:UNUSED_PAD src0_sel:WORD_1 src1_sel:DWORD
	v_and_b32_sdwa v66, v73, v38 dst_sel:DWORD dst_unused:UNUSED_PAD src0_sel:WORD_1 src1_sel:DWORD
	v_add3_u32 v67, v74, v67, s31
	v_add3_u32 v68, v72, v68, s31
	v_add3_u32 v66, v73, v66, s31
	v_and_b32_e32 v67, 0xffff0000, v67
	v_and_b32_e32 v68, 0xffff0000, v68
	s_waitcnt lgkmcnt(0)
	v_and_b32_sdwa v69, v78, v38 dst_sel:DWORD dst_unused:UNUSED_PAD src0_sel:WORD_1 src1_sel:DWORD
	v_and_b32_sdwa v72, v76, v38 dst_sel:DWORD dst_unused:UNUSED_PAD src0_sel:WORD_1 src1_sel:DWORD
	v_or_b32_sdwa v67, v67, v66 dst_sel:DWORD dst_unused:UNUSED_PAD src0_sel:DWORD src1_sel:WORD_1
	v_or_b32_sdwa v66, v68, v35 dst_sel:DWORD dst_unused:UNUSED_PAD src0_sel:DWORD src1_sel:WORD_1
	v_and_b32_sdwa v35, v77, v38 dst_sel:DWORD dst_unused:UNUSED_PAD src0_sel:WORD_1 src1_sel:DWORD
	v_and_b32_sdwa v68, v75, v38 dst_sel:DWORD dst_unused:UNUSED_PAD src0_sel:WORD_1 src1_sel:DWORD
	v_add3_u32 v69, v78, v69, s31
	v_add3_u32 v72, v76, v72, s31
	v_add3_u32 v68, v75, v68, s31
	v_add3_u32 v35, v77, v35, s31
	v_and_b32_e32 v69, 0xffff0000, v69
	v_and_b32_e32 v72, 0xffff0000, v72
	v_or_b32_sdwa v69, v69, v35 dst_sel:DWORD dst_unused:UNUSED_PAD src0_sel:DWORD src1_sel:WORD_1
	v_or_b32_sdwa v68, v72, v68 dst_sel:DWORD dst_unused:UNUSED_PAD src0_sel:DWORD src1_sel:WORD_1
	s_add_i32 s29, s29, 1
	s_and_b64 vcc, exec, s[16:17]
	s_mov_b32 s34, s33
	s_mov_b32 s1, s35
	s_mov_b32 s15, s24
	s_mov_b32 s4, s20
	s_mov_b32 s14, s6
	s_mov_b32 s26, s25
	s_mov_b64 s[2:3], s[18:19]
	global_store_dwordx4 v[70:71], v[66:69], off
	s_barrier
	s_cbranch_vccnz .LBB0_2013
	s_branch .LBB0_1995

.LBB0_2313:
	s_waitcnt vmcnt(11)
	v_add_u32_e32 v2, 0x800, v130
	s_lshr_b32 s0, s12, 8
	v_ashrrev_i32_e32 v41, 6, v2
	v_cvt_f32_u32_e32 v2, s0
	s_sub_i32 s14, 0, s0
	s_abs_i32 s9, s13
	s_ashr_i32 s8, s13, 31
	v_rcp_iflag_f32_e32 v2, v2
	v_add_u32_e32 v3, 0xa00, v130
	v_ashrrev_i32_e32 v42, 6, v3
	v_add_u32_e32 v3, 0xc00, v130
	v_mul_f32_e32 v2, 0x4f7ffffe, v2
	v_cvt_u32_f32_e32 v2, v2
	v_lshlrev_b32_e32 v1, 2, v130
	v_ashrrev_i32_e32 v43, 6, v3
	v_add_u32_e32 v3, 0xe00, v130
	v_readfirstlane_b32 s15, v2
	s_mul_i32 s14, s14, s15
	s_mul_hi_u32 s14, s15, s14
	s_add_i32 s15, s15, s14
	s_mul_hi_u32 s14, s9, s15
	s_mul_i32 s15, s14, s0
	s_sub_i32 s9, s9, s15
	s_add_i32 s15, s14, 1
	s_sub_i32 s16, s9, s0
	s_cmp_ge_u32 s9, s0
	s_cselect_b32 s14, s15, s14
	s_cselect_b32 s9, s16, s9
	s_add_i32 s15, s14, 1
	s_cmp_ge_u32 s9, s0
	s_cselect_b32 s9, s15, s14
	s_xor_b32 s9, s9, s8
	s_sub_i32 s16, s9, s8
	s_mul_i32 s0, s16, s0
	s_sub_i32 s0, s13, s0
	s_lshl_b32 s8, s0, 8
	s_ashr_i32 s9, s8, 31
	s_lshl_b64 s[14:15], s[8:9], 2
	s_add_u32 s10, s10, s14
	v_and_b32_e32 v36, 0xfc, v1
	v_ashrrev_i32_e32 v44, 6, v3
	s_addc_u32 s11, s11, s15
	s_lshl_b32 s20, s16, 6
	v_mov_b32_e32 v35, 0
	v_lshlrev_b32_e32 v34, 2, v36
	v_add_u32_e32 v4, s20, v44
	v_lshl_add_u64 v[2:3], s[10:11], 0, v[34:35]
	s_waitcnt vmcnt(10)
	v_ashrrev_i32_e32 v7, 31, v4
	v_mad_u64_u32 v[4:5], s[10:11], v4, s12, 0
	v_mov_b32_e32 v6, v5
	v_mad_u64_u32 v[6:7], s[10:11], v7, s12, v[6:7]
	v_mov_b32_e32 v5, v6
	v_add_u32_e32 v6, s20, v43
	v_ashrrev_i32_e32 v9, 31, v6
	v_mad_u64_u32 v[6:7], s[10:11], v6, s12, 0
	v_mov_b32_e32 v8, v7
	v_mad_u64_u32 v[8:9], s[10:11], v9, s12, v[8:9]
	v_lshl_add_u64 v[4:5], v[4:5], 2, v[2:3]
	v_mov_b32_e32 v7, v8
	v_lshl_add_u64 v[6:7], v[6:7], 2, v[2:3]
	global_load_dwordx4 v[30:33], v[4:5], off
	global_load_dwordx4 v[26:29], v[6:7], off
	v_add_u32_e32 v4, s20, v42
	v_ashrrev_i32_e32 v7, 31, v4
	v_mad_u64_u32 v[4:5], s[10:11], v4, s12, 0
	v_mov_b32_e32 v6, v5
	v_mad_u64_u32 v[6:7], s[10:11], v7, s12, v[6:7]
	v_mov_b32_e32 v5, v6
	v_add_u32_e32 v6, s20, v41
	v_ashrrev_i32_e32 v9, 31, v6
	v_mad_u64_u32 v[6:7], s[10:11], v6, s12, 0
	v_mov_b32_e32 v8, v7
	v_add_u32_e32 v54, 0x600, v130
	v_mad_u64_u32 v[8:9], s[10:11], v9, s12, v[8:9]
	v_ashrrev_i32_e32 v40, 6, v54
	v_lshl_add_u64 v[4:5], v[4:5], 2, v[2:3]
	v_mov_b32_e32 v7, v8
	v_lshl_add_u64 v[6:7], v[6:7], 2, v[2:3]
	global_load_dwordx4 v[22:25], v[4:5], off
	global_load_dwordx4 v[18:21], v[6:7], off
	v_add_u32_e32 v4, s20, v40
	v_ashrrev_i32_e32 v7, 31, v4
	v_mad_u64_u32 v[4:5], s[10:11], v4, s12, 0
	v_add_u32_e32 v51, 0x400, v130
	v_mov_b32_e32 v6, v5
	v_ashrrev_i32_e32 v39, 6, v51
	v_mad_u64_u32 v[6:7], s[10:11], v7, s12, v[6:7]
	v_mov_b32_e32 v5, v6
	v_add_u32_e32 v6, s20, v39
	v_ashrrev_i32_e32 v9, 31, v6
	v_mad_u64_u32 v[6:7], s[10:11], v6, s12, 0
	v_mov_b32_e32 v8, v7
	v_add_u32_e32 v37, 0x200, v130
	v_mad_u64_u32 v[8:9], s[10:11], v9, s12, v[8:9]
	v_ashrrev_i32_e32 v38, 6, v37
	v_lshl_add_u64 v[4:5], v[4:5], 2, v[2:3]
	v_mov_b32_e32 v7, v8
	v_lshl_add_u64 v[6:7], v[6:7], 2, v[2:3]
	global_load_dwordx4 v[14:17], v[4:5], off
	global_load_dwordx4 v[10:13], v[6:7], off
	v_add_u32_e32 v4, s20, v38
	v_ashrrev_i32_e32 v7, 31, v4
	v_mad_u64_u32 v[4:5], s[10:11], v4, s12, 0
	v_mov_b32_e32 v6, v5
	v_ashrrev_i32_e32 v1, 6, v130
	v_mad_u64_u32 v[6:7], s[10:11], v7, s12, v[6:7]
	v_mov_b32_e32 v5, v6
	v_add_u32_e32 v6, s20, v1
	v_ashrrev_i32_e32 v9, 31, v6
	v_mad_u64_u32 v[6:7], s[10:11], v6, s12, 0
	v_mov_b32_e32 v8, v7
	v_mad_u64_u32 v[8:9], s[10:11], v9, s12, v[8:9]
	v_mov_b32_e32 v7, v8
	v_lshl_add_u64 v[4:5], v[4:5], 2, v[2:3]
	v_lshl_add_u64 v[2:3], v[6:7], 2, v[2:3]
	global_load_dwordx4 v[6:9], v[4:5], off
	s_nop 0
	global_load_dwordx4 v[2:5], v[2:3], off
	v_lshlrev_b32_e32 v45, 3, v130
	v_and_b32_e32 v66, 56, v45
	s_movk_i32 s0, 0x404
	v_mad_u32_u24 v55, v66, s0, 0
	v_mul_lo_u32 v57, v1, s0
	v_mul_lo_u32 v58, v38, s0
	v_mul_lo_u32 v59, v39, s0
	v_mul_lo_u32 v60, v40, s0
	v_mul_lo_u32 v61, v41, s0
	v_mul_lo_u32 v62, v42, s0
	v_mul_lo_u32 v63, v43, s0
	v_mul_lo_u32 v64, v44, s0
	s_add_u32 s0, s6, 0x1e940000
	s_addc_u32 s9, s7, 0
	s_add_u32 s12, s6, 0x16940000
	s_addc_u32 s13, s7, 0
	s_add_u32 s14, s78, 0x1000000
	s_addc_u32 s15, s79, 0
	s_add_u32 s16, s6, 0x16140000
	s_addc_u32 s17, s7, 0
	v_readlane_b32 s56, v250, 7
	s_add_u32 s36, s6, 0x15540000
	v_readlane_b32 s70, v250, 21
	v_readlane_b32 s71, v250, 22
	s_addc_u32 s37, s7, 0
	s_mov_b64 s[18:19], s[70:71]
	s_add_u32 s18, s18, 0x6c00000
	s_addc_u32 s19, s19, 0
	s_add_u32 s6, s6, 0x11f40000
	v_add_u32_e32 v34, 0, v34
	v_ashrrev_i32_e32 v45, 3, v130
	v_ashrrev_i32_e32 v48, 3, v37
	v_ashrrev_i32_e32 v51, 3, v51
	v_ashrrev_i32_e32 v54, 3, v54
	s_addc_u32 s7, s7, 0
	s_add_i32 s10, s33, s40
	s_mov_b32 s11, 0
	v_lshl_add_u32 v46, v45, 2, v55
	v_and_b32_e32 v47, 15, v45
	v_lshl_add_u32 v49, v48, 2, v55
	v_and_b32_e32 v50, 15, v48
	v_lshl_add_u32 v52, v51, 2, v55
	v_and_b32_e32 v53, 15, v51
	v_lshl_add_u32 v55, v54, 2, v55
	v_and_b32_e32 v56, 15, v54
	s_add_i32 s38, s10, 0xfffff5c0
	s_add_i32 s39, s10, 0xfffff6c0
	v_add_u32_e32 v57, v34, v57
	v_add_u32_e32 v58, v34, v58
	v_add_u32_e32 v59, v34, v59
	v_add_u32_e32 v60, v34, v60
	v_add_u32_e32 v61, v34, v61
	v_add_u32_e32 v62, v34, v62
	v_add_u32_e32 v63, v34, v63
	v_add_u32_e32 v64, v34, v64
	v_lshlrev_b32_e32 v34, 2, v36
	v_lshlrev_b32_e32 v36, 1, v66
	s_movk_i32 s41, 0x7fff
	v_mov_b32_e32 v65, 1
	s_mov_b32 s10, s21
	s_mov_b32 s42, s35
	s_mov_b64 s[24:25], s[2:3]
	v_readlane_b32 s57, v250, 8
	v_readlane_b32 s58, v250, 9
	v_readlane_b32 s59, v250, 10
	v_readlane_b32 s60, v250, 11
	v_readlane_b32 s61, v250, 12
	v_readlane_b32 s62, v250, 13
	v_readlane_b32 s63, v250, 14
	v_readlane_b32 s64, v250, 15
	v_readlane_b32 s65, v250, 16
	v_readlane_b32 s66, v250, 17
	v_readlane_b32 s67, v250, 18
	v_readlane_b32 s68, v250, 19
	v_readlane_b32 s69, v250, 20
	s_waitcnt vmcnt(0)
	s_branch .LBB0_2317
.LBB0_2317:
	s_add_i32 s33, s33, s40
	s_cmp_lt_u32 s34, 2
	s_cselect_b64 s[22:23], -1, 0
	s_and_b64 vcc, exec, s[22:23]
	s_mov_b32 s43, s1
	s_mov_b32 s26, s8
	s_mov_b32 s30, s20
	s_cbranch_vccnz .Lcwp_2317
	s_add_i32 s30, s38, 0xa40
	s_cmpk_lt_i32 s30, 0x6c0
	s_cbranch_scc1 .LBB0_2314
	s_cmpk_gt_u32 s30, 0x83f
	s_mov_b64 s[26:27], -1
	s_cbranch_scc0 .LBB0_2332
	s_cmpk_gt_u32 s30, 0x93f
	s_cbranch_scc0 .LBB0_2329
	s_add_i32 s24, s38, 0x100
	s_mul_hi_u32 s10, s39, 0xaaaaaaab
	s_mul_hi_u32 s24, s24, 0xaaaaaaab
	s_lshr_b32 s10, s10, 8
	s_lshr_b32 s26, s24, 8
	s_mulk_i32 s10, 0xfe80
	s_mul_i32 s24, s26, 0xfffffe80
	s_add_i32 s46, s33, s24
	s_add_i32 s45, s38, s10
	s_addk_i32 s46, 0xf6c0
	s_add_i32 s27, s45, 0x100
	s_cmpk_gt_i32 s27, 0x7f
	s_mov_b64 s[30:31], -1
	s_cbranch_scc0 .LBB0_2326
	s_cmpk_gt_u32 s27, 0xff
	s_cbranch_scc0 .LBB0_2324
	s_add_i32 s10, s26, 16
	s_lshl_b64 s[24:25], s[10:11], 23
	s_mov_b32 s27, s11
	s_add_u32 s28, s88, s24
	s_addc_u32 s29, s89, s25
	s_lshl_b64 s[24:25], s[26:27], 22
	s_add_u32 s24, s0, s24
	s_addc_u32 s25, s9, s25
	s_mov_b64 s[30:31], 0

.LBB0_2334:
	s_movk_i32 s42, 0x400
	s_movk_i32 s44, 0x800
	s_mov_b32 s43, 0
	s_mov_b32 s10, 0
	s_cbranch_execz .LBB0_2327
	s_branch .LBB0_2328
.LBB0_2314:
	s_mov_b32 s10, 0
	s_movk_i32 s44, 0x3600
	s_movk_i32 s42, 0x800
	s_mov_b64 s[28:29], s[18:19]
	s_mov_b64 s[24:25], s[6:7]
	s_mov_b32 s45, s33
	s_mov_b32 s43, 0
.LBB0_2315:
	s_lshr_b32 s26, s44, 8
	v_cvt_f32_u32_e32 v182, s26
	s_sub_i32 s31, 0, s26
	s_abs_i32 s30, s45
	s_ashr_i32 s27, s45, 31
	v_rcp_iflag_f32_e32 v182, v182
	s_nop 0
	v_mul_f32_e32 v182, 0x4f7ffffe, v182
	v_cvt_u32_f32_e32 v182, v182
	s_nop 0
	v_readfirstlane_b32 s46, v182
	s_mul_i32 s31, s31, s46
	s_mul_hi_u32 s31, s46, s31
	s_add_i32 s46, s46, s31
	s_mul_hi_u32 s31, s30, s46
	s_mul_i32 s46, s31, s26
	s_sub_i32 s30, s30, s46
	s_add_i32 s47, s31, 1
	s_sub_i32 s46, s30, s26
	s_cmp_ge_u32 s30, s26
	s_cselect_b32 s31, s47, s31
	s_cselect_b32 s30, s46, s30
	s_add_i32 s46, s31, 1
	s_cmp_ge_u32 s30, s26
	s_cselect_b32 s30, s46, s31
	s_xor_b32 s30, s30, s27
	s_sub_i32 s27, s30, s27
	s_lshl_b32 s30, s27, 6
	s_mul_i32 s27, s27, s26
	s_sub_i32 s26, s45, s27
	s_lshl_b32 s26, s26, 8
	s_ashr_i32 s27, s26, 31
	s_lshl_b64 s[46:47], s[26:27], 2
	s_add_u32 s28, s28, s46
	v_add_u32_e32 v182, s30, v1
	s_addc_u32 s29, s29, s47
	v_add_u32_e32 v190, s30, v39
	v_add_u32_e32 v198, s30, v41
	v_add_u32_e32 v208, s30, v43
	v_ashrrev_i32_e32 v185, 31, v182
	v_lshl_add_u64 v[206:207], s[28:29], 0, v[34:35]
	v_mad_u64_u32 v[182:183], s[28:29], v182, s44, 0
	v_ashrrev_i32_e32 v193, 31, v190
	v_mad_u64_u32 v[190:191], s[28:29], v190, s44, 0
	v_ashrrev_i32_e32 v201, 31, v198
	v_mad_u64_u32 v[198:199], s[28:29], v198, s44, 0
	v_ashrrev_i32_e32 v211, 31, v208
	v_mad_u64_u32 v[208:209], s[28:29], v208, s44, 0
	v_mov_b32_e32 v184, v183
	v_mov_b32_e32 v192, v191
	v_mov_b32_e32 v200, v199
	v_mov_b32_e32 v210, v209
	v_mad_u64_u32 v[184:185], s[28:29], v185, s44, v[184:185]
	v_mad_u64_u32 v[192:193], s[28:29], v193, s44, v[192:193]
	v_mad_u64_u32 v[200:201], s[28:29], v201, s44, v[200:201]
	v_mad_u64_u32 v[210:211], s[28:29], v211, s44, v[210:211]
	v_mov_b32_e32 v183, v184
	v_add_u32_e32 v184, s30, v38
	v_mov_b32_e32 v191, v192
	v_add_u32_e32 v192, s30, v40
	v_mov_b32_e32 v199, v200
	v_add_u32_e32 v200, s30, v42
	v_mov_b32_e32 v209, v210
	v_add_u32_e32 v210, s30, v44
	v_ashrrev_i32_e32 v187, 31, v184
	v_mad_u64_u32 v[184:185], s[28:29], v184, s44, 0
	v_ashrrev_i32_e32 v195, 31, v192
	v_mad_u64_u32 v[192:193], s[28:29], v192, s44, 0
	v_ashrrev_i32_e32 v203, 31, v200
	v_mad_u64_u32 v[200:201], s[28:29], v200, s44, 0
	v_ashrrev_i32_e32 v213, 31, v210
	v_mad_u64_u32 v[210:211], s[28:29], v210, s44, 0
	v_mov_b32_e32 v186, v185
	v_mov_b32_e32 v194, v193
	v_mov_b32_e32 v202, v201
	v_mov_b32_e32 v212, v211
	v_mad_u64_u32 v[186:187], s[28:29], v187, s44, v[186:187]
	v_mad_u64_u32 v[194:195], s[28:29], v195, s44, v[194:195]
	v_mad_u64_u32 v[202:203], s[28:29], v203, s44, v[202:203]
	v_mad_u64_u32 v[212:213], s[28:29], v213, s44, v[212:213]
	v_mov_b32_e32 v185, v186
	v_mov_b32_e32 v193, v194
	v_mov_b32_e32 v201, v202
	v_mov_b32_e32 v211, v212
	v_lshl_add_u64 v[182:183], v[182:183], 2, v[206:207]
	v_lshl_add_u64 v[186:187], v[184:185], 2, v[206:207]
	v_lshl_add_u64 v[190:191], v[190:191], 2, v[206:207]
	v_lshl_add_u64 v[194:195], v[192:193], 2, v[206:207]
	v_lshl_add_u64 v[198:199], v[198:199], 2, v[206:207]
	v_lshl_add_u64 v[202:203], v[200:201], 2, v[206:207]
	v_lshl_add_u64 v[208:209], v[208:209], 2, v[206:207]
	v_lshl_add_u64 v[210:211], v[210:211], 2, v[206:207]
	v_mov_b32_e32 v188, v182
	v_mov_b32_e32 v189, v183
	v_mov_b32_e32 v196, v186
	v_mov_b32_e32 v197, v187
	v_mov_b32_e32 v204, v190
	v_mov_b32_e32 v205, v191
	v_mov_b32_e32 v214, v194
	v_mov_b32_e32 v215, v195
	v_mov_b32_e32 v216, v198
	v_mov_b32_e32 v217, v199
	v_mov_b32_e32 v218, v202
	v_mov_b32_e32 v219, v203
	v_mov_b32_e32 v220, v208
	v_mov_b32_e32 v221, v209
	v_mov_b32_e32 v222, v210
	v_mov_b32_e32 v223, v211
.Lcwp_2317:
	s_waitcnt vmcnt(4)
	s_and_b64 vcc, exec, s[22:23]
	s_cbranch_vccnz .Lcnp_2317
	global_load_dwordx4 v[150:153], v[188:189], off
	s_nop 0
	global_load_dwordx4 v[154:157], v[196:197], off
	s_nop 0
	global_load_dwordx4 v[158:161], v[204:205], off
	s_nop 0
	global_load_dwordx4 v[162:165], v[214:215], off
	s_nop 0
	global_load_dwordx4 v[166:169], v[216:217], off
	s_nop 0
	global_load_dwordx4 v[170:173], v[218:219], off
	s_nop 0
	global_load_dwordx4 v[174:177], v[220:221], off
	s_nop 0
	global_load_dwordx4 v[178:181], v[222:223], off

.Lcq2317_2334:
	s_movk_i32 s42, 0x400
	s_movk_i32 s44, 0x800
	s_mov_b32 s43, 0
	s_mov_b32 s10, 0
	s_cbranch_execz .Lcq2317_2327
	s_branch .Lcq2317_2328
.Lcq2317_2314:
	s_mov_b32 s10, 0
	s_movk_i32 s44, 0x3600
	s_movk_i32 s42, 0x800
	s_mov_b64 s[28:29], s[18:19]
	s_mov_b64 s[24:25], s[6:7]
	s_mov_b32 s45, s33
	s_mov_b32 s43, 0

.Lcwq_2317:
	s_waitcnt vmcnt(4)
	s_and_b64 vcc, exec, s[22:23]
	s_cbranch_vccnz .Lcnq_2317
	global_load_dwordx4 v[2:5], v[188:189], off
	s_nop 0
	global_load_dwordx4 v[6:9], v[196:197], off
	s_nop 0
	global_load_dwordx4 v[10:13], v[204:205], off
	s_nop 0
	global_load_dwordx4 v[14:17], v[214:215], off
	s_nop 0
	global_load_dwordx4 v[18:21], v[216:217], off
	s_nop 0
	global_load_dwordx4 v[22:25], v[218:219], off
	s_nop 0
	global_load_dwordx4 v[26:29], v[220:221], off
	s_nop 0
	global_load_dwordx4 v[30:33], v[222:223], off

.Lcq2317_2316:
	s_add_i32 s34, s34, -1
	s_cmp_eq_u32 s21, 0
	v_add_u32_e32 v66, s8, v45
	v_lshlrev_b32_e32 v37, 1, v66
	s_cselect_b64 vcc, -1, 0
	s_ashr_i32 s21, s20, 31
	v_and_b32_e32 v37, 0xffffffe0, v37
	s_lshl_b64 s[20:21], s[20:21], 1
	v_add3_u32 v67, s1, v47, v37
	s_add_u32 s2, s2, s20
	s_addc_u32 s3, s3, s21
	v_mov_b32_e32 v37, v35
	v_cndmask_b32_e32 v66, v67, v66, vcc
	v_lshl_add_u64 v[70:71], s[2:3], 0, v[36:37]
	v_ashrrev_i32_e32 v69, 31, v66
	v_mad_u64_u32 v[66:67], s[2:3], v66, s35, 0
	v_mov_b32_e32 v68, v67
	ds_read_b32 v37, v46
	ds_read_b32 v74, v46 offset:1028
	ds_read_b32 v75, v46 offset:2056
	ds_read_b32 v76, v46 offset:3084
	ds_read_b32 v77, v46 offset:4112
	ds_read_b32 v78, v46 offset:5140
	ds_read_b32 v79, v46 offset:6168
	ds_read_b32 v80, v46 offset:7196
	v_mad_u64_u32 v[68:69], s[2:3], v69, s35, v[68:69]
	v_mov_b32_e32 v67, v68
	v_lshl_add_u64 v[72:73], v[66:67], 1, v[70:71]
	s_waitcnt lgkmcnt(7)
	v_and_b32_sdwa v67, v37, v65 dst_sel:DWORD dst_unused:UNUSED_PAD src0_sel:WORD_1 src1_sel:DWORD
	v_add3_u32 v37, v37, v67, s41
	s_waitcnt lgkmcnt(4)
	v_and_b32_sdwa v67, v76, v65 dst_sel:DWORD dst_unused:UNUSED_PAD src0_sel:WORD_1 src1_sel:DWORD
	v_and_b32_sdwa v68, v74, v65 dst_sel:DWORD dst_unused:UNUSED_PAD src0_sel:WORD_1 src1_sel:DWORD
	v_and_b32_sdwa v66, v75, v65 dst_sel:DWORD dst_unused:UNUSED_PAD src0_sel:WORD_1 src1_sel:DWORD
	v_add3_u32 v67, v76, v67, s41
	v_add3_u32 v68, v74, v68, s41
	v_add3_u32 v66, v75, v66, s41
	v_and_b32_e32 v67, 0xffff0000, v67
	v_and_b32_e32 v68, 0xffff0000, v68
	s_waitcnt lgkmcnt(0)
	v_and_b32_sdwa v69, v80, v65 dst_sel:DWORD dst_unused:UNUSED_PAD src0_sel:WORD_1 src1_sel:DWORD
	v_and_b32_sdwa v74, v78, v65 dst_sel:DWORD dst_unused:UNUSED_PAD src0_sel:WORD_1 src1_sel:DWORD
	v_or_b32_sdwa v67, v67, v66 dst_sel:DWORD dst_unused:UNUSED_PAD src0_sel:DWORD src1_sel:WORD_1
	v_or_b32_sdwa v66, v68, v37 dst_sel:DWORD dst_unused:UNUSED_PAD src0_sel:DWORD src1_sel:WORD_1
	v_and_b32_sdwa v37, v79, v65 dst_sel:DWORD dst_unused:UNUSED_PAD src0_sel:WORD_1 src1_sel:DWORD
	v_and_b32_sdwa v68, v77, v65 dst_sel:DWORD dst_unused:UNUSED_PAD src0_sel:WORD_1 src1_sel:DWORD
	v_add3_u32 v69, v80, v69, s41
	v_add3_u32 v74, v78, v74, s41
	v_add3_u32 v68, v77, v68, s41
	v_add3_u32 v37, v79, v37, s41
	v_and_b32_e32 v69, 0xffff0000, v69
	v_and_b32_e32 v74, 0xffff0000, v74
	v_or_b32_sdwa v69, v69, v37 dst_sel:DWORD dst_unused:UNUSED_PAD src0_sel:DWORD src1_sel:WORD_1
	v_or_b32_sdwa v68, v74, v68 dst_sel:DWORD dst_unused:UNUSED_PAD src0_sel:DWORD src1_sel:WORD_1
	global_store_dwordx4 v[72:73], v[66:69], off
	ds_read_b32 v37, v49
	ds_read_b32 v74, v49 offset:1028
	ds_read_b32 v75, v49 offset:2056
	ds_read_b32 v76, v49 offset:3084
	ds_read_b32 v77, v49 offset:4112
	ds_read_b32 v78, v49 offset:5140
	ds_read_b32 v79, v49 offset:6168
	ds_read_b32 v80, v49 offset:7196
	v_add_u32_e32 v66, s8, v48
	v_lshlrev_b32_e32 v67, 1, v66
	v_and_b32_e32 v67, 0xffffffe0, v67
	v_add3_u32 v67, s1, v50, v67
	v_cndmask_b32_e32 v66, v67, v66, vcc
	v_ashrrev_i32_e32 v69, 31, v66
	v_mad_u64_u32 v[66:67], s[2:3], v66, s35, 0
	v_mov_b32_e32 v68, v67
	v_mad_u64_u32 v[68:69], s[2:3], v69, s35, v[68:69]
	v_mov_b32_e32 v67, v68
	v_lshl_add_u64 v[72:73], v[66:67], 1, v[70:71]
	s_waitcnt lgkmcnt(7)
	v_and_b32_sdwa v67, v37, v65 dst_sel:DWORD dst_unused:UNUSED_PAD src0_sel:WORD_1 src1_sel:DWORD
	v_add3_u32 v37, v37, v67, s41
	s_waitcnt lgkmcnt(4)
	v_and_b32_sdwa v67, v76, v65 dst_sel:DWORD dst_unused:UNUSED_PAD src0_sel:WORD_1 src1_sel:DWORD
	v_and_b32_sdwa v68, v74, v65 dst_sel:DWORD dst_unused:UNUSED_PAD src0_sel:WORD_1 src1_sel:DWORD
	v_and_b32_sdwa v66, v75, v65 dst_sel:DWORD dst_unused:UNUSED_PAD src0_sel:WORD_1 src1_sel:DWORD
	v_add3_u32 v67, v76, v67, s41
	v_add3_u32 v68, v74, v68, s41
	v_add3_u32 v66, v75, v66, s41
	v_and_b32_e32 v67, 0xffff0000, v67
	v_and_b32_e32 v68, 0xffff0000, v68
	s_waitcnt lgkmcnt(0)
	v_and_b32_sdwa v69, v80, v65 dst_sel:DWORD dst_unused:UNUSED_PAD src0_sel:WORD_1 src1_sel:DWORD
	v_and_b32_sdwa v74, v78, v65 dst_sel:DWORD dst_unused:UNUSED_PAD src0_sel:WORD_1 src1_sel:DWORD
	v_or_b32_sdwa v67, v67, v66 dst_sel:DWORD dst_unused:UNUSED_PAD src0_sel:DWORD src1_sel:WORD_1
	v_or_b32_sdwa v66, v68, v37 dst_sel:DWORD dst_unused:UNUSED_PAD src0_sel:DWORD src1_sel:WORD_1
	v_and_b32_sdwa v37, v79, v65 dst_sel:DWORD dst_unused:UNUSED_PAD src0_sel:WORD_1 src1_sel:DWORD
	v_and_b32_sdwa v68, v77, v65 dst_sel:DWORD dst_unused:UNUSED_PAD src0_sel:WORD_1 src1_sel:DWORD
	v_add3_u32 v69, v80, v69, s41
	v_add3_u32 v74, v78, v74, s41
	v_add3_u32 v68, v77, v68, s41
	v_add3_u32 v37, v79, v37, s41
	v_and_b32_e32 v69, 0xffff0000, v69
	v_and_b32_e32 v74, 0xffff0000, v74
	v_or_b32_sdwa v69, v69, v37 dst_sel:DWORD dst_unused:UNUSED_PAD src0_sel:DWORD src1_sel:WORD_1
	v_or_b32_sdwa v68, v74, v68 dst_sel:DWORD dst_unused:UNUSED_PAD src0_sel:DWORD src1_sel:WORD_1
	global_store_dwordx4 v[72:73], v[66:69], off
	ds_read_b32 v37, v52
	ds_read_b32 v74, v52 offset:1028
	ds_read_b32 v75, v52 offset:2056
	ds_read_b32 v76, v52 offset:3084
	ds_read_b32 v77, v52 offset:4112
	ds_read_b32 v78, v52 offset:5140
	ds_read_b32 v79, v52 offset:6168
	ds_read_b32 v80, v52 offset:7196
	v_add_u32_e32 v66, s8, v51
	v_lshlrev_b32_e32 v67, 1, v66
	v_and_b32_e32 v67, 0xffffffe0, v67
	v_add3_u32 v67, s1, v53, v67
	v_cndmask_b32_e32 v66, v67, v66, vcc
	v_ashrrev_i32_e32 v69, 31, v66
	v_mad_u64_u32 v[66:67], s[2:3], v66, s35, 0
	v_mov_b32_e32 v68, v67
	v_mad_u64_u32 v[68:69], s[2:3], v69, s35, v[68:69]
	v_mov_b32_e32 v67, v68
	v_lshl_add_u64 v[72:73], v[66:67], 1, v[70:71]
	s_waitcnt lgkmcnt(7)
	v_and_b32_sdwa v67, v37, v65 dst_sel:DWORD dst_unused:UNUSED_PAD src0_sel:WORD_1 src1_sel:DWORD
	v_add3_u32 v37, v37, v67, s41
	s_waitcnt lgkmcnt(4)
	v_and_b32_sdwa v67, v76, v65 dst_sel:DWORD dst_unused:UNUSED_PAD src0_sel:WORD_1 src1_sel:DWORD
	v_and_b32_sdwa v68, v74, v65 dst_sel:DWORD dst_unused:UNUSED_PAD src0_sel:WORD_1 src1_sel:DWORD
	v_and_b32_sdwa v66, v75, v65 dst_sel:DWORD dst_unused:UNUSED_PAD src0_sel:WORD_1 src1_sel:DWORD
	v_add3_u32 v67, v76, v67, s41
	v_add3_u32 v68, v74, v68, s41
	v_add3_u32 v66, v75, v66, s41
	v_and_b32_e32 v67, 0xffff0000, v67
	v_and_b32_e32 v68, 0xffff0000, v68
	s_waitcnt lgkmcnt(0)
	v_and_b32_sdwa v69, v80, v65 dst_sel:DWORD dst_unused:UNUSED_PAD src0_sel:WORD_1 src1_sel:DWORD
	v_and_b32_sdwa v74, v78, v65 dst_sel:DWORD dst_unused:UNUSED_PAD src0_sel:WORD_1 src1_sel:DWORD
	v_or_b32_sdwa v67, v67, v66 dst_sel:DWORD dst_unused:UNUSED_PAD src0_sel:DWORD src1_sel:WORD_1
	v_or_b32_sdwa v66, v68, v37 dst_sel:DWORD dst_unused:UNUSED_PAD src0_sel:DWORD src1_sel:WORD_1
	v_and_b32_sdwa v37, v79, v65 dst_sel:DWORD dst_unused:UNUSED_PAD src0_sel:WORD_1 src1_sel:DWORD
	v_and_b32_sdwa v68, v77, v65 dst_sel:DWORD dst_unused:UNUSED_PAD src0_sel:WORD_1 src1_sel:DWORD
	v_add3_u32 v69, v80, v69, s41
	v_add3_u32 v74, v78, v74, s41
	v_add3_u32 v68, v77, v68, s41
	v_add3_u32 v37, v79, v37, s41
	v_and_b32_e32 v69, 0xffff0000, v69
	v_and_b32_e32 v74, 0xffff0000, v74
	v_or_b32_sdwa v69, v69, v37 dst_sel:DWORD dst_unused:UNUSED_PAD src0_sel:DWORD src1_sel:WORD_1
	v_or_b32_sdwa v68, v74, v68 dst_sel:DWORD dst_unused:UNUSED_PAD src0_sel:DWORD src1_sel:WORD_1
	global_store_dwordx4 v[72:73], v[66:69], off
	ds_read_b32 v37, v55
	ds_read_b32 v72, v55 offset:1028
	ds_read_b32 v73, v55 offset:2056
	ds_read_b32 v74, v55 offset:3084
	ds_read_b32 v75, v55 offset:4112
	ds_read_b32 v76, v55 offset:5140
	ds_read_b32 v77, v55 offset:6168
	ds_read_b32 v78, v55 offset:7196
	v_add_u32_e32 v66, s8, v54
	v_lshlrev_b32_e32 v67, 1, v66
	v_and_b32_e32 v67, 0xffffffe0, v67
	v_add3_u32 v67, s1, v56, v67
	v_cndmask_b32_e32 v66, v67, v66, vcc
	v_ashrrev_i32_e32 v69, 31, v66
	v_mad_u64_u32 v[66:67], s[2:3], v66, s35, 0
	v_mov_b32_e32 v68, v67
	v_mad_u64_u32 v[68:69], s[2:3], v69, s35, v[68:69]
	v_mov_b32_e32 v67, v68
	v_lshl_add_u64 v[70:71], v[66:67], 1, v[70:71]
	s_waitcnt lgkmcnt(7)
	v_and_b32_sdwa v67, v37, v65 dst_sel:DWORD dst_unused:UNUSED_PAD src0_sel:WORD_1 src1_sel:DWORD
	v_add3_u32 v37, v37, v67, s41
	s_waitcnt lgkmcnt(4)
	v_and_b32_sdwa v67, v74, v65 dst_sel:DWORD dst_unused:UNUSED_PAD src0_sel:WORD_1 src1_sel:DWORD
	v_and_b32_sdwa v68, v72, v65 dst_sel:DWORD dst_unused:UNUSED_PAD src0_sel:WORD_1 src1_sel:DWORD
	v_and_b32_sdwa v66, v73, v65 dst_sel:DWORD dst_unused:UNUSED_PAD src0_sel:WORD_1 src1_sel:DWORD
	v_add3_u32 v67, v74, v67, s41
	v_add3_u32 v68, v72, v68, s41
	v_add3_u32 v66, v73, v66, s41
	v_and_b32_e32 v67, 0xffff0000, v67
	v_and_b32_e32 v68, 0xffff0000, v68
	s_waitcnt lgkmcnt(0)
	v_and_b32_sdwa v69, v78, v65 dst_sel:DWORD dst_unused:UNUSED_PAD src0_sel:WORD_1 src1_sel:DWORD
	v_and_b32_sdwa v72, v76, v65 dst_sel:DWORD dst_unused:UNUSED_PAD src0_sel:WORD_1 src1_sel:DWORD
	v_or_b32_sdwa v67, v67, v66 dst_sel:DWORD dst_unused:UNUSED_PAD src0_sel:DWORD src1_sel:WORD_1
	v_or_b32_sdwa v66, v68, v37 dst_sel:DWORD dst_unused:UNUSED_PAD src0_sel:DWORD src1_sel:WORD_1
	v_and_b32_sdwa v37, v77, v65 dst_sel:DWORD dst_unused:UNUSED_PAD src0_sel:WORD_1 src1_sel:DWORD
	v_and_b32_sdwa v68, v75, v65 dst_sel:DWORD dst_unused:UNUSED_PAD src0_sel:WORD_1 src1_sel:DWORD
	v_add3_u32 v69, v78, v69, s41
	v_add3_u32 v72, v76, v72, s41
	v_add3_u32 v68, v75, v68, s41
	v_add3_u32 v37, v77, v37, s41
	v_and_b32_e32 v69, 0xffff0000, v69
	v_and_b32_e32 v72, 0xffff0000, v72
	v_or_b32_sdwa v69, v69, v37 dst_sel:DWORD dst_unused:UNUSED_PAD src0_sel:DWORD src1_sel:WORD_1
	v_or_b32_sdwa v68, v72, v68 dst_sel:DWORD dst_unused:UNUSED_PAD src0_sel:DWORD src1_sel:WORD_1
	s_add_i32 s38, s38, s40
	s_add_i32 s39, s39, s40
	s_andn2_b64 vcc, exec, s[22:23]
	s_mov_b32 s1, s43
	s_mov_b32 s21, s10
	s_mov_b32 s8, s26
	s_mov_b32 s20, s30
	s_mov_b32 s35, s42
	s_mov_b64 s[2:3], s[24:25]
	global_store_dwordx4 v[70:71], v[66:69], off
	s_barrier
	s_cbranch_vccz .LBB0_2335
	s_branch .LBB0_2317

.LBB0_3747:
	s_waitcnt vmcnt(5)
	v_add_u32_e32 v2, 0x800, v34
	s_lshr_b32 s4, s8, 8
	v_ashrrev_i32_e32 v42, 6, v2
	v_cvt_f32_u32_e32 v2, s4
	s_sub_i32 s11, 0, s4
	s_abs_i32 s10, s9
	s_ashr_i32 s5, s9, 31
	v_rcp_iflag_f32_e32 v2, v2
	v_add_u32_e32 v3, 0xa00, v34
	v_ashrrev_i32_e32 v43, 6, v3
	v_add_u32_e32 v3, 0xc00, v34
	v_mul_f32_e32 v2, 0x4f7ffffe, v2
	v_cvt_u32_f32_e32 v2, v2
	v_lshlrev_b32_e32 v1, 2, v34
	v_ashrrev_i32_e32 v44, 6, v3
	v_add_u32_e32 v3, 0xe00, v34
	v_readfirstlane_b32 s12, v2
	s_mul_i32 s11, s11, s12
	s_mul_hi_u32 s11, s12, s11
	s_add_i32 s12, s12, s11
	s_mul_hi_u32 s11, s10, s12
	s_mul_i32 s12, s11, s4
	s_sub_i32 s10, s10, s12
	s_add_i32 s12, s11, 1
	s_sub_i32 s13, s10, s4
	s_cmp_ge_u32 s10, s4
	s_cselect_b32 s11, s12, s11
	s_cselect_b32 s10, s13, s10
	s_add_i32 s12, s11, 1
	s_cmp_ge_u32 s10, s4
	s_cselect_b32 s10, s12, s11
	s_xor_b32 s10, s10, s5
	s_sub_i32 s12, s10, s5
	s_mul_i32 s4, s12, s4
	s_sub_i32 s4, s9, s4
	s_lshl_b32 s4, s4, 8
	s_ashr_i32 s5, s4, 31
	s_lshl_b64 s[10:11], s[4:5], 2
	s_add_u32 s6, s6, s10
	v_and_b32_e32 v38, 0xfc, v1
	v_ashrrev_i32_e32 v45, 6, v3
	s_addc_u32 s7, s7, s11
	s_lshl_b32 s18, s12, 6
	v_mov_b32_e32 v37, 0
	v_lshlrev_b32_e32 v36, 2, v38
	v_add_u32_e32 v2, s18, v45
	v_lshl_add_u64 v[26:27], s[6:7], 0, v[36:37]
	v_ashrrev_i32_e32 v5, 31, v2
	v_mad_u64_u32 v[2:3], s[6:7], v2, s8, 0
	v_mov_b32_e32 v4, v3
	v_mad_u64_u32 v[4:5], s[6:7], v5, s8, v[4:5]
	v_mov_b32_e32 v3, v4
	v_lshl_add_u64 v[10:11], v[2:3], 2, v[26:27]
	v_add_u32_e32 v2, s18, v44
	v_ashrrev_i32_e32 v5, 31, v2
	v_mad_u64_u32 v[2:3], s[6:7], v2, s8, 0
	v_mov_b32_e32 v4, v3
	v_mad_u64_u32 v[4:5], s[6:7], v5, s8, v[4:5]
	v_mov_b32_e32 v3, v4
	v_lshl_add_u64 v[12:13], v[2:3], 2, v[26:27]
	global_load_dwordx4 v[6:9], v[10:11], off
	global_load_dwordx4 v[2:5], v[12:13], off
	v_add_u32_e32 v10, s18, v43
	v_ashrrev_i32_e32 v13, 31, v10
	v_mad_u64_u32 v[10:11], s[6:7], v10, s8, 0
	v_mov_b32_e32 v12, v11
	v_mad_u64_u32 v[12:13], s[6:7], v13, s8, v[12:13]
	v_mov_b32_e32 v11, v12
	v_lshl_add_u64 v[18:19], v[10:11], 2, v[26:27]
	v_add_u32_e32 v10, s18, v42
	v_ashrrev_i32_e32 v13, 31, v10
	v_mad_u64_u32 v[10:11], s[6:7], v10, s8, 0
	v_mov_b32_e32 v12, v11
	v_add_u32_e32 v55, 0x600, v34
	v_mad_u64_u32 v[12:13], s[6:7], v13, s8, v[12:13]
	v_ashrrev_i32_e32 v41, 6, v55
	v_mov_b32_e32 v11, v12
	v_lshl_add_u64 v[20:21], v[10:11], 2, v[26:27]
	global_load_dwordx4 v[14:17], v[18:19], off
	global_load_dwordx4 v[10:13], v[20:21], off
	v_add_u32_e32 v18, s18, v41
	v_ashrrev_i32_e32 v21, 31, v18
	v_mad_u64_u32 v[18:19], s[6:7], v18, s8, 0
	v_mov_b32_e32 v20, v19
	v_add_u32_e32 v52, 0x400, v34
	v_mad_u64_u32 v[20:21], s[6:7], v21, s8, v[20:21]
	v_ashrrev_i32_e32 v40, 6, v52
	v_mov_b32_e32 v19, v20
	v_lshl_add_u64 v[28:29], v[18:19], 2, v[26:27]
	v_add_u32_e32 v18, s18, v40
	v_ashrrev_i32_e32 v21, 31, v18
	v_mad_u64_u32 v[18:19], s[6:7], v18, s8, 0
	v_mov_b32_e32 v20, v19
	v_add_u32_e32 v39, 0x200, v34
	v_mad_u64_u32 v[20:21], s[6:7], v21, s8, v[20:21]
	v_ashrrev_i32_e32 v35, 6, v39
	v_mov_b32_e32 v19, v20
	s_waitcnt vmcnt(8)
	v_lshl_add_u64 v[30:31], v[18:19], 2, v[26:27]
	global_load_dwordx4 v[22:25], v[28:29], off
	global_load_dwordx4 v[18:21], v[30:31], off
	v_add_u32_e32 v28, s18, v35
	v_ashrrev_i32_e32 v31, 31, v28
	v_mad_u64_u32 v[28:29], s[6:7], v28, s8, 0
	v_mov_b32_e32 v30, v29
	v_mad_u64_u32 v[30:31], s[6:7], v31, s8, v[30:31]
	v_ashrrev_i32_e32 v1, 6, v34
	v_mov_b32_e32 v29, v30
	v_lshl_add_u64 v[46:47], v[28:29], 2, v[26:27]
	v_add_u32_e32 v28, s18, v1
	v_ashrrev_i32_e32 v31, 31, v28
	v_mad_u64_u32 v[28:29], s[6:7], v28, s8, 0
	v_mov_b32_e32 v30, v29
	v_mad_u64_u32 v[30:31], s[6:7], v31, s8, v[30:31]
	v_mov_b32_e32 v29, v30
	v_lshl_add_u64 v[48:49], v[28:29], 2, v[26:27]
	global_load_dwordx4 v[30:33], v[46:47], off
	global_load_dwordx4 v[26:29], v[48:49], off
	v_lshlrev_b32_e32 v46, 3, v34
	v_and_b32_e32 v66, 56, v46
	s_movk_i32 s5, 0x404
	v_readlane_b32 s16, v252, 3
	v_mad_u32_u24 v56, v66, s5, 0
	v_mul_lo_u32 v58, v1, s5
	v_mul_lo_u32 v59, v35, s5
	v_mul_lo_u32 v60, v40, s5
	v_mul_lo_u32 v61, v41, s5
	v_mul_lo_u32 v62, v42, s5
	v_mul_lo_u32 v63, v43, s5
	v_mul_lo_u32 v64, v44, s5
	v_mul_lo_u32 v65, v45, s5
	v_readlane_b32 s17, v252, 4
	s_add_u32 s5, s16, 0x1e940000
	s_addc_u32 s30, s17, 0
	s_add_u32 s8, s16, 0x16940000
	s_addc_u32 s9, s17, 0
	s_add_u32 s10, s78, 0x1000000
	s_addc_u32 s11, s79, 0
	s_add_u32 s12, s16, 0x16140000
	s_addc_u32 s13, s17, 0
	v_readlane_b32 s36, v250, 7
	s_add_u32 s31, s16, 0x15540000
	v_readlane_b32 s50, v250, 21
	v_readlane_b32 s51, v250, 22
	s_addc_u32 s33, s17, 0
	s_mov_b64 s[14:15], s[50:51]
	s_add_u32 s14, s14, 0x6c00000
	s_addc_u32 s15, s15, 0
	v_add_u32_e32 v36, 0, v36
	v_ashrrev_i32_e32 v46, 3, v34
	v_ashrrev_i32_e32 v49, 3, v39
	v_ashrrev_i32_e32 v52, 3, v52
	v_ashrrev_i32_e32 v55, 3, v55
	v_readlane_b32 s38, v250, 9
	s_add_u32 s16, s16, 0x11f40000
	s_mov_b32 s7, 0
	v_lshl_add_u32 v47, v46, 2, v56
	v_and_b32_e32 v48, 15, v46
	v_lshl_add_u32 v50, v49, 2, v56
	v_and_b32_e32 v51, 15, v49
	v_lshl_add_u32 v53, v52, 2, v56
	v_and_b32_e32 v54, 15, v52
	v_lshl_add_u32 v56, v55, 2, v56
	v_and_b32_e32 v57, 15, v55
	s_addc_u32 s17, s17, 0
	s_add_i32 s34, s20, 0x15e1
	s_mov_b32 s35, 17
	v_add_u32_e32 v58, v36, v58
	v_add_u32_e32 v59, v36, v59
	v_add_u32_e32 v60, v36, v60
	v_add_u32_e32 v61, v36, v61
	v_add_u32_e32 v62, v36, v62
	v_add_u32_e32 v63, v36, v63
	v_add_u32_e32 v64, v36, v64
	v_add_u32_e32 v65, v36, v65
	v_lshlrev_b32_e32 v36, 2, v38
	v_lshlrev_b32_e32 v38, 1, v66
	s_movk_i32 s36, 0x7fff
	v_mov_b32_e32 v66, 1
	s_mov_b32 s6, s19
	s_mov_b32 s38, s0
	s_mov_b64 s[22:23], s[2:3]
	v_readlane_b32 s37, v250, 8
	v_readlane_b32 s39, v250, 10
	v_readlane_b32 s40, v250, 11
	v_readlane_b32 s41, v250, 12
	v_readlane_b32 s42, v250, 13
	v_readlane_b32 s43, v250, 14
	v_readlane_b32 s44, v250, 15
	v_readlane_b32 s45, v250, 16
	v_readlane_b32 s46, v250, 17
	v_readlane_b32 s47, v250, 18
	v_readlane_b32 s48, v250, 19
	v_readlane_b32 s49, v250, 20
	s_waitcnt vmcnt(0)
	s_branch .LBB0_3751
.LBB0_3751:
	s_add_i32 s37, s28, 1
	s_cmp_lt_u32 s35, 2
	s_cselect_b64 s[20:21], -1, 0
	s_and_b64 vcc, exec, s[20:21]
	s_mov_b32 s39, s1
	s_mov_b32 s24, s4
	s_mov_b32 s29, s18
	s_cbranch_vccnz .Lcwp_3751
	s_add_i32 s6, s34, 0x93f
	s_cmpk_lt_i32 s6, 0x6bf
	s_cbranch_scc1 .LBB0_3748
	s_add_i32 s29, s34, 0x940
	s_cmpk_gt_u32 s29, 0x83f
	s_mov_b64 s[24:25], -1
	s_cbranch_scc0 .LBB0_3766
	s_cmpk_gt_u32 s29, 0x93f
	s_cbranch_scc0 .LBB0_3763
	s_mul_hi_u32 s6, s34, 0xaaaaaaab
	s_lshr_b32 s24, s6, 8
	s_mul_i32 s6, s24, 0xfffffe80
	s_add_i32 s42, s28, s6
	s_addk_i32 s42, 0xf6c1
	s_add_i32 s25, s34, s6
	s_cmpk_gt_i32 s25, 0x7f
	s_mov_b64 s[28:29], -1
	s_cbranch_scc0 .LBB0_3760
	s_cmpk_gt_u32 s25, 0xff
	s_cbranch_scc0 .LBB0_3758
	s_add_i32 s6, s24, 16
	s_add_i32 s41, s42, 0xffffff00
	s_lshl_b64 s[22:23], s[6:7], 23
	s_mov_b32 s25, s7
	s_add_u32 s26, s88, s22
	s_addc_u32 s27, s89, s23
	s_lshl_b64 s[22:23], s[24:25], 22
	s_add_u32 s22, s5, s22
	s_addc_u32 s23, s30, s23
	s_mov_b64 s[28:29], 0

.LBB0_3768:
	s_movk_i32 s38, 0x400
	s_movk_i32 s40, 0x800
	s_mov_b32 s39, 0
	s_mov_b32 s6, 0
	s_cbranch_execz .LBB0_3761
	s_branch .LBB0_3762
.LBB0_3748:
	s_mov_b32 s6, 0
	s_movk_i32 s40, 0x3600
	s_movk_i32 s38, 0x800
	s_mov_b64 s[26:27], s[14:15]
	s_mov_b64 s[22:23], s[16:17]
	s_mov_b32 s41, s37
	s_mov_b32 s39, 0
.LBB0_3749:
	s_lshr_b32 s24, s40, 8
	v_cvt_f32_u32_e32 v182, s24
	s_sub_i32 s29, 0, s24
	s_abs_i32 s28, s41
	s_ashr_i32 s25, s41, 31
	v_rcp_iflag_f32_e32 v182, v182
	s_nop 0
	v_mul_f32_e32 v182, 0x4f7ffffe, v182
	v_cvt_u32_f32_e32 v182, v182
	s_nop 0
	v_readfirstlane_b32 s42, v182
	s_mul_i32 s29, s29, s42
	s_mul_hi_u32 s29, s42, s29
	s_add_i32 s42, s42, s29
	s_mul_hi_u32 s29, s28, s42
	s_mul_i32 s42, s29, s24
	s_sub_i32 s28, s28, s42
	s_add_i32 s43, s29, 1
	s_sub_i32 s42, s28, s24
	s_cmp_ge_u32 s28, s24
	s_cselect_b32 s29, s43, s29
	s_cselect_b32 s28, s42, s28
	s_add_i32 s42, s29, 1
	s_cmp_ge_u32 s28, s24
	s_cselect_b32 s28, s42, s29
	s_xor_b32 s28, s28, s25
	s_sub_i32 s25, s28, s25
	s_lshl_b32 s29, s25, 6
	s_mul_i32 s25, s25, s24
	s_sub_i32 s24, s41, s25
	s_lshl_b32 s24, s24, 8
	s_ashr_i32 s25, s24, 31
	s_lshl_b64 s[42:43], s[24:25], 2
	s_add_u32 s26, s26, s42
	v_add_u32_e32 v184, s29, v1
	s_addc_u32 s27, s27, s43
	v_ashrrev_i32_e32 v187, 31, v184
	v_lshl_add_u64 v[182:183], s[26:27], 0, v[36:37]
	v_mad_u64_u32 v[184:185], s[26:27], v184, s40, 0
	v_mov_b32_e32 v186, v185
	v_mad_u64_u32 v[186:187], s[26:27], v187, s40, v[186:187]
	v_mov_b32_e32 v185, v186
	v_add_u32_e32 v186, s29, v35
	v_ashrrev_i32_e32 v189, 31, v186
	v_mad_u64_u32 v[186:187], s[26:27], v186, s40, 0
	v_mov_b32_e32 v188, v187
	v_mad_u64_u32 v[188:189], s[26:27], v189, s40, v[188:189]
	v_lshl_add_u64 v[184:185], v[184:185], 2, v[182:183]
	v_mov_b32_e32 v187, v188
	v_lshl_add_u64 v[186:187], v[186:187], 2, v[182:183]
	v_mov_b32_e32 v190, v184
	v_mov_b32_e32 v191, v185
	v_mov_b32_e32 v192, v186
	v_mov_b32_e32 v193, v187
	v_add_u32_e32 v184, s29, v40
	v_ashrrev_i32_e32 v187, 31, v184
	v_mad_u64_u32 v[184:185], s[26:27], v184, s40, 0
	v_mov_b32_e32 v186, v185
	v_mad_u64_u32 v[186:187], s[26:27], v187, s40, v[186:187]
	v_mov_b32_e32 v185, v186
	v_add_u32_e32 v186, s29, v41
	v_ashrrev_i32_e32 v189, 31, v186
	v_mad_u64_u32 v[186:187], s[26:27], v186, s40, 0
	v_mov_b32_e32 v188, v187
	v_mad_u64_u32 v[188:189], s[26:27], v189, s40, v[188:189]
	v_lshl_add_u64 v[184:185], v[184:185], 2, v[182:183]
	v_mov_b32_e32 v187, v188
	v_lshl_add_u64 v[186:187], v[186:187], 2, v[182:183]
	v_mov_b32_e32 v194, v184
	v_mov_b32_e32 v195, v185
	v_mov_b32_e32 v196, v186
	v_mov_b32_e32 v197, v187
	v_add_u32_e32 v184, s29, v42
	v_ashrrev_i32_e32 v187, 31, v184
	v_mad_u64_u32 v[184:185], s[26:27], v184, s40, 0
	v_mov_b32_e32 v186, v185
	v_mad_u64_u32 v[186:187], s[26:27], v187, s40, v[186:187]
	v_mov_b32_e32 v185, v186
	v_add_u32_e32 v186, s29, v43
	v_ashrrev_i32_e32 v189, 31, v186
	v_mad_u64_u32 v[186:187], s[26:27], v186, s40, 0
	v_mov_b32_e32 v188, v187
	v_mad_u64_u32 v[188:189], s[26:27], v189, s40, v[188:189]
	v_lshl_add_u64 v[184:185], v[184:185], 2, v[182:183]
	v_mov_b32_e32 v187, v188
	v_lshl_add_u64 v[186:187], v[186:187], 2, v[182:183]
	v_mov_b32_e32 v198, v184
	v_mov_b32_e32 v199, v185
	v_mov_b32_e32 v200, v186
	v_mov_b32_e32 v201, v187
	v_add_u32_e32 v184, s29, v44
	v_ashrrev_i32_e32 v187, 31, v184
	v_mad_u64_u32 v[184:185], s[26:27], v184, s40, 0
	v_mov_b32_e32 v186, v185
	v_mad_u64_u32 v[186:187], s[26:27], v187, s40, v[186:187]
	v_mov_b32_e32 v185, v186
	v_add_u32_e32 v186, s29, v45
	v_ashrrev_i32_e32 v189, 31, v186
	v_mad_u64_u32 v[186:187], s[26:27], v186, s40, 0
	v_mov_b32_e32 v188, v187
	v_mad_u64_u32 v[188:189], s[26:27], v189, s40, v[188:189]
	v_mov_b32_e32 v187, v188
	v_lshl_add_u64 v[184:185], v[184:185], 2, v[182:183]
	v_lshl_add_u64 v[186:187], v[186:187], 2, v[182:183]
	v_mov_b32_e32 v202, v184
	v_mov_b32_e32 v203, v185
	v_mov_b32_e32 v204, v186
	v_mov_b32_e32 v205, v187
.Lcwp_3751:
	s_waitcnt vmcnt(4)
	s_and_b64 vcc, exec, s[20:21]
	s_cbranch_vccnz .Lcnp_3751
	global_load_dwordx4 v[174:177], v[190:191], off
	s_nop 0
	global_load_dwordx4 v[178:181], v[192:193], off
	s_nop 0
	global_load_dwordx4 v[166:169], v[194:195], off
	s_nop 0
	global_load_dwordx4 v[170:173], v[196:197], off
	s_nop 0
	global_load_dwordx4 v[158:161], v[198:199], off
	s_nop 0
	global_load_dwordx4 v[162:165], v[200:201], off
	s_nop 0
	global_load_dwordx4 v[150:153], v[202:203], off
	s_nop 0
	global_load_dwordx4 v[154:157], v[204:205], off
.Lcnp_3751:
	ds_write2_b32 v58, v26, v27 offset1:1
	ds_write2_b32 v58, v28, v29 offset0:2 offset1:3
	ds_write2_b32 v59, v30, v31 offset1:1
	ds_write2_b32 v59, v32, v33 offset0:2 offset1:3
	ds_write2_b32 v60, v18, v19 offset1:1
	ds_write2_b32 v60, v20, v21 offset0:2 offset1:3
	ds_write2_b32 v61, v22, v23 offset1:1
	ds_write2_b32 v61, v24, v25 offset0:2 offset1:3
	ds_write2_b32 v62, v10, v11 offset1:1
	ds_write2_b32 v62, v12, v13 offset0:2 offset1:3
	ds_write2_b32 v63, v14, v15 offset1:1
	ds_write2_b32 v63, v16, v17 offset0:2 offset1:3
	ds_write2_b32 v64, v2, v3 offset1:1
	ds_write2_b32 v64, v4, v5 offset0:2 offset1:3
	ds_write2_b32 v65, v6, v7 offset1:1
	ds_write2_b32 v65, v8, v9 offset0:2 offset1:3
	s_waitcnt lgkmcnt(0)
	s_barrier

.Lcq3751_3768:
	s_movk_i32 s38, 0x400
	s_movk_i32 s40, 0x800
	s_mov_b32 s39, 0
	s_mov_b32 s6, 0
	s_cbranch_execz .Lcq3751_3761
	s_branch .Lcq3751_3762
.Lcq3751_3748:
	s_mov_b32 s6, 0
	s_movk_i32 s40, 0x3600
	s_movk_i32 s38, 0x800
	s_mov_b64 s[26:27], s[14:15]
	s_mov_b64 s[22:23], s[16:17]
	s_mov_b32 s41, s37
	s_mov_b32 s39, 0

.Lcwq_3751:
	s_waitcnt vmcnt(4)
	s_and_b64 vcc, exec, s[20:21]
	s_cbranch_vccnz .Lcnq_3751
	global_load_dwordx4 v[26:29], v[190:191], off
	s_nop 0
	global_load_dwordx4 v[30:33], v[192:193], off
	s_nop 0
	global_load_dwordx4 v[18:21], v[194:195], off
	s_nop 0
	global_load_dwordx4 v[22:25], v[196:197], off
	s_nop 0
	global_load_dwordx4 v[10:13], v[198:199], off
	s_nop 0
	global_load_dwordx4 v[14:17], v[200:201], off
	s_nop 0
	global_load_dwordx4 v[2:5], v[202:203], off
	s_nop 0
	global_load_dwordx4 v[6:9], v[204:205], off
.Lcnq_3751:
	ds_write2_b32 v58, v174, v175 offset1:1
	ds_write2_b32 v58, v176, v177 offset0:2 offset1:3
	ds_write2_b32 v59, v178, v179 offset1:1
	ds_write2_b32 v59, v180, v181 offset0:2 offset1:3
	ds_write2_b32 v60, v166, v167 offset1:1
	ds_write2_b32 v60, v168, v169 offset0:2 offset1:3
	ds_write2_b32 v61, v170, v171 offset1:1
	ds_write2_b32 v61, v172, v173 offset0:2 offset1:3
	ds_write2_b32 v62, v158, v159 offset1:1
	ds_write2_b32 v62, v160, v161 offset0:2 offset1:3
	ds_write2_b32 v63, v162, v163 offset1:1
	ds_write2_b32 v63, v164, v165 offset0:2 offset1:3
	ds_write2_b32 v64, v150, v151 offset1:1
	ds_write2_b32 v64, v152, v153 offset0:2 offset1:3
	ds_write2_b32 v65, v154, v155 offset1:1
	ds_write2_b32 v65, v156, v157 offset0:2 offset1:3
	s_waitcnt lgkmcnt(0)
	s_barrier
.Lcq3751_3750:
	s_add_i32 s35, s35, -1
	s_cmp_eq_u32 s19, 0
	v_add_u32_e32 v67, s4, v46
	v_lshlrev_b32_e32 v39, 1, v67
	s_cselect_b64 vcc, -1, 0
	s_ashr_i32 s19, s18, 31
	v_and_b32_e32 v39, 0xffffffe0, v39
	s_lshl_b64 s[18:19], s[18:19], 1
	v_add3_u32 v68, s1, v48, v39
	s_add_u32 s2, s2, s18
	s_addc_u32 s3, s3, s19
	v_mov_b32_e32 v39, v37
	v_cndmask_b32_e32 v67, v68, v67, vcc
	v_lshl_add_u64 v[72:73], s[2:3], 0, v[38:39]
	v_mad_u64_u32 v[68:69], s[2:3], v67, s0, 0
	v_ashrrev_i32_e32 v71, 31, v67
	v_mov_b32_e32 v70, v69
	v_mad_u64_u32 v[70:71], s[2:3], v71, s0, v[70:71]
	ds_read_b32 v39, v47
	ds_read_b32 v76, v47 offset:1028
	ds_read_b32 v77, v47 offset:2056
	ds_read_b32 v78, v47 offset:3084
	ds_read_b32 v79, v47 offset:4112
	ds_read_b32 v80, v47 offset:5140
	ds_read_b32 v81, v47 offset:6168
	ds_read_b32 v82, v47 offset:7196
	v_mov_b32_e32 v69, v70
	v_lshl_add_u64 v[74:75], v[68:69], 1, v[72:73]
	s_waitcnt lgkmcnt(7)
	v_and_b32_sdwa v68, v39, v66 dst_sel:DWORD dst_unused:UNUSED_PAD src0_sel:WORD_1 src1_sel:DWORD
	v_add3_u32 v39, v39, v68, s36
	s_waitcnt lgkmcnt(4)
	v_and_b32_sdwa v68, v78, v66 dst_sel:DWORD dst_unused:UNUSED_PAD src0_sel:WORD_1 src1_sel:DWORD
	v_and_b32_sdwa v69, v76, v66 dst_sel:DWORD dst_unused:UNUSED_PAD src0_sel:WORD_1 src1_sel:DWORD
	v_and_b32_sdwa v67, v77, v66 dst_sel:DWORD dst_unused:UNUSED_PAD src0_sel:WORD_1 src1_sel:DWORD
	v_add3_u32 v68, v78, v68, s36
	v_add3_u32 v69, v76, v69, s36
	v_add3_u32 v67, v77, v67, s36
	v_and_b32_e32 v68, 0xffff0000, v68
	v_and_b32_e32 v70, 0xffff0000, v69
	v_or_b32_sdwa v69, v68, v67 dst_sel:DWORD dst_unused:UNUSED_PAD src0_sel:DWORD src1_sel:WORD_1
	v_or_b32_sdwa v68, v70, v39 dst_sel:DWORD dst_unused:UNUSED_PAD src0_sel:DWORD src1_sel:WORD_1
	s_waitcnt lgkmcnt(0)
	v_and_b32_sdwa v70, v82, v66 dst_sel:DWORD dst_unused:UNUSED_PAD src0_sel:WORD_1 src1_sel:DWORD
	v_and_b32_sdwa v71, v80, v66 dst_sel:DWORD dst_unused:UNUSED_PAD src0_sel:WORD_1 src1_sel:DWORD
	v_and_b32_sdwa v39, v81, v66 dst_sel:DWORD dst_unused:UNUSED_PAD src0_sel:WORD_1 src1_sel:DWORD
	v_and_b32_sdwa v67, v79, v66 dst_sel:DWORD dst_unused:UNUSED_PAD src0_sel:WORD_1 src1_sel:DWORD
	v_add3_u32 v70, v82, v70, s36
	v_add3_u32 v71, v80, v71, s36
	v_add3_u32 v67, v79, v67, s36
	v_add3_u32 v39, v81, v39, s36
	v_and_b32_e32 v70, 0xffff0000, v70
	v_and_b32_e32 v76, 0xffff0000, v71
	v_or_b32_sdwa v71, v70, v39 dst_sel:DWORD dst_unused:UNUSED_PAD src0_sel:DWORD src1_sel:WORD_1
	v_or_b32_sdwa v70, v76, v67 dst_sel:DWORD dst_unused:UNUSED_PAD src0_sel:DWORD src1_sel:WORD_1
	global_store_dwordx4 v[74:75], v[68:71], off
	ds_read_b32 v39, v50
	ds_read_b32 v67, v50 offset:1028
	ds_read_b32 v76, v50 offset:2056
	ds_read_b32 v77, v50 offset:3084
	ds_read_b32 v78, v50 offset:4112
	ds_read_b32 v79, v50 offset:5140
	ds_read_b32 v80, v50 offset:6168
	ds_read_b32 v81, v50 offset:7196
	v_add_u32_e32 v68, s4, v49
	v_lshlrev_b32_e32 v69, 1, v68
	v_and_b32_e32 v69, 0xffffffe0, v69
	v_add3_u32 v69, s1, v51, v69
	v_cndmask_b32_e32 v68, v69, v68, vcc
	v_ashrrev_i32_e32 v71, 31, v68
	v_mad_u64_u32 v[68:69], s[2:3], v68, s0, 0
	v_mov_b32_e32 v70, v69
	v_mad_u64_u32 v[70:71], s[2:3], v71, s0, v[70:71]
	v_mov_b32_e32 v69, v70
	v_lshl_add_u64 v[74:75], v[68:69], 1, v[72:73]
	s_waitcnt lgkmcnt(7)
	v_and_b32_sdwa v69, v39, v66 dst_sel:DWORD dst_unused:UNUSED_PAD src0_sel:WORD_1 src1_sel:DWORD
	v_add3_u32 v39, v39, v69, s36
	s_waitcnt lgkmcnt(4)
	v_and_b32_sdwa v69, v77, v66 dst_sel:DWORD dst_unused:UNUSED_PAD src0_sel:WORD_1 src1_sel:DWORD
	v_and_b32_sdwa v70, v67, v66 dst_sel:DWORD dst_unused:UNUSED_PAD src0_sel:WORD_1 src1_sel:DWORD
	v_and_b32_sdwa v68, v76, v66 dst_sel:DWORD dst_unused:UNUSED_PAD src0_sel:WORD_1 src1_sel:DWORD
	v_add3_u32 v69, v77, v69, s36
	v_add3_u32 v67, v67, v70, s36
	v_add3_u32 v68, v76, v68, s36
	v_and_b32_e32 v69, 0xffff0000, v69
	v_and_b32_e32 v67, 0xffff0000, v67
	s_waitcnt lgkmcnt(0)
	v_and_b32_sdwa v70, v81, v66 dst_sel:DWORD dst_unused:UNUSED_PAD src0_sel:WORD_1 src1_sel:DWORD
	v_and_b32_sdwa v71, v79, v66 dst_sel:DWORD dst_unused:UNUSED_PAD src0_sel:WORD_1 src1_sel:DWORD
	v_or_b32_sdwa v69, v69, v68 dst_sel:DWORD dst_unused:UNUSED_PAD src0_sel:DWORD src1_sel:WORD_1
	v_or_b32_sdwa v68, v67, v39 dst_sel:DWORD dst_unused:UNUSED_PAD src0_sel:DWORD src1_sel:WORD_1
	v_and_b32_sdwa v39, v80, v66 dst_sel:DWORD dst_unused:UNUSED_PAD src0_sel:WORD_1 src1_sel:DWORD
	v_and_b32_sdwa v67, v78, v66 dst_sel:DWORD dst_unused:UNUSED_PAD src0_sel:WORD_1 src1_sel:DWORD
	v_add3_u32 v70, v81, v70, s36
	v_add3_u32 v71, v79, v71, s36
	v_add3_u32 v67, v78, v67, s36
	v_add3_u32 v39, v80, v39, s36
	v_and_b32_e32 v70, 0xffff0000, v70
	v_and_b32_e32 v76, 0xffff0000, v71
	v_or_b32_sdwa v71, v70, v39 dst_sel:DWORD dst_unused:UNUSED_PAD src0_sel:DWORD src1_sel:WORD_1
	v_or_b32_sdwa v70, v76, v67 dst_sel:DWORD dst_unused:UNUSED_PAD src0_sel:DWORD src1_sel:WORD_1
	global_store_dwordx4 v[74:75], v[68:71], off
	ds_read_b32 v39, v53
	ds_read_b32 v67, v53 offset:1028
	ds_read_b32 v76, v53 offset:2056
	ds_read_b32 v77, v53 offset:3084
	ds_read_b32 v78, v53 offset:4112
	ds_read_b32 v79, v53 offset:5140
	ds_read_b32 v80, v53 offset:6168
	ds_read_b32 v81, v53 offset:7196
	v_add_u32_e32 v68, s4, v52
	v_lshlrev_b32_e32 v69, 1, v68
	v_and_b32_e32 v69, 0xffffffe0, v69
	v_add3_u32 v69, s1, v54, v69
	v_cndmask_b32_e32 v68, v69, v68, vcc
	v_ashrrev_i32_e32 v71, 31, v68
	v_mad_u64_u32 v[68:69], s[2:3], v68, s0, 0
	v_mov_b32_e32 v70, v69
	v_mad_u64_u32 v[70:71], s[2:3], v71, s0, v[70:71]
	v_mov_b32_e32 v69, v70
	v_lshl_add_u64 v[74:75], v[68:69], 1, v[72:73]
	s_waitcnt lgkmcnt(7)
	v_and_b32_sdwa v69, v39, v66 dst_sel:DWORD dst_unused:UNUSED_PAD src0_sel:WORD_1 src1_sel:DWORD
	v_add3_u32 v39, v39, v69, s36
	s_waitcnt lgkmcnt(4)
	v_and_b32_sdwa v69, v77, v66 dst_sel:DWORD dst_unused:UNUSED_PAD src0_sel:WORD_1 src1_sel:DWORD
	v_and_b32_sdwa v70, v67, v66 dst_sel:DWORD dst_unused:UNUSED_PAD src0_sel:WORD_1 src1_sel:DWORD
	v_and_b32_sdwa v68, v76, v66 dst_sel:DWORD dst_unused:UNUSED_PAD src0_sel:WORD_1 src1_sel:DWORD
	v_add3_u32 v69, v77, v69, s36
	v_add3_u32 v67, v67, v70, s36
	v_add3_u32 v68, v76, v68, s36
	v_and_b32_e32 v69, 0xffff0000, v69
	v_and_b32_e32 v67, 0xffff0000, v67
	s_waitcnt lgkmcnt(0)
	v_and_b32_sdwa v70, v81, v66 dst_sel:DWORD dst_unused:UNUSED_PAD src0_sel:WORD_1 src1_sel:DWORD
	v_and_b32_sdwa v71, v79, v66 dst_sel:DWORD dst_unused:UNUSED_PAD src0_sel:WORD_1 src1_sel:DWORD
	v_or_b32_sdwa v69, v69, v68 dst_sel:DWORD dst_unused:UNUSED_PAD src0_sel:DWORD src1_sel:WORD_1
	v_or_b32_sdwa v68, v67, v39 dst_sel:DWORD dst_unused:UNUSED_PAD src0_sel:DWORD src1_sel:WORD_1
	v_and_b32_sdwa v39, v80, v66 dst_sel:DWORD dst_unused:UNUSED_PAD src0_sel:WORD_1 src1_sel:DWORD
	v_and_b32_sdwa v67, v78, v66 dst_sel:DWORD dst_unused:UNUSED_PAD src0_sel:WORD_1 src1_sel:DWORD
	v_add3_u32 v70, v81, v70, s36
	v_add3_u32 v71, v79, v71, s36
	v_add3_u32 v67, v78, v67, s36
	v_add3_u32 v39, v80, v39, s36
	v_and_b32_e32 v70, 0xffff0000, v70
	v_and_b32_e32 v76, 0xffff0000, v71
	v_or_b32_sdwa v71, v70, v39 dst_sel:DWORD dst_unused:UNUSED_PAD src0_sel:DWORD src1_sel:WORD_1
	v_or_b32_sdwa v70, v76, v67 dst_sel:DWORD dst_unused:UNUSED_PAD src0_sel:DWORD src1_sel:WORD_1
	global_store_dwordx4 v[74:75], v[68:71], off
	ds_read_b32 v39, v56
	ds_read_b32 v67, v56 offset:1028
	ds_read_b32 v74, v56 offset:2056
	ds_read_b32 v75, v56 offset:3084
	ds_read_b32 v76, v56 offset:4112
	ds_read_b32 v77, v56 offset:5140
	ds_read_b32 v78, v56 offset:6168
	ds_read_b32 v79, v56 offset:7196
	v_add_u32_e32 v68, s4, v55
	v_lshlrev_b32_e32 v69, 1, v68
	v_and_b32_e32 v69, 0xffffffe0, v69
	v_add3_u32 v69, s1, v57, v69
	v_cndmask_b32_e32 v68, v69, v68, vcc
	v_ashrrev_i32_e32 v71, 31, v68
	v_mad_u64_u32 v[68:69], s[2:3], v68, s0, 0
	v_mov_b32_e32 v70, v69
	v_mad_u64_u32 v[70:71], s[0:1], v71, s0, v[70:71]
	v_mov_b32_e32 v69, v70
	v_lshl_add_u64 v[72:73], v[68:69], 1, v[72:73]
	s_waitcnt lgkmcnt(7)
	v_and_b32_sdwa v69, v39, v66 dst_sel:DWORD dst_unused:UNUSED_PAD src0_sel:WORD_1 src1_sel:DWORD
	v_add3_u32 v39, v39, v69, s36
	s_waitcnt lgkmcnt(4)
	v_and_b32_sdwa v69, v75, v66 dst_sel:DWORD dst_unused:UNUSED_PAD src0_sel:WORD_1 src1_sel:DWORD
	v_and_b32_sdwa v70, v67, v66 dst_sel:DWORD dst_unused:UNUSED_PAD src0_sel:WORD_1 src1_sel:DWORD
	v_and_b32_sdwa v68, v74, v66 dst_sel:DWORD dst_unused:UNUSED_PAD src0_sel:WORD_1 src1_sel:DWORD
	v_add3_u32 v69, v75, v69, s36
	v_add3_u32 v67, v67, v70, s36
	v_add3_u32 v68, v74, v68, s36
	v_and_b32_e32 v69, 0xffff0000, v69
	v_and_b32_e32 v67, 0xffff0000, v67
	s_waitcnt lgkmcnt(0)
	v_and_b32_sdwa v70, v79, v66 dst_sel:DWORD dst_unused:UNUSED_PAD src0_sel:WORD_1 src1_sel:DWORD
	v_and_b32_sdwa v71, v77, v66 dst_sel:DWORD dst_unused:UNUSED_PAD src0_sel:WORD_1 src1_sel:DWORD
	v_or_b32_sdwa v69, v69, v68 dst_sel:DWORD dst_unused:UNUSED_PAD src0_sel:DWORD src1_sel:WORD_1
	v_or_b32_sdwa v68, v67, v39 dst_sel:DWORD dst_unused:UNUSED_PAD src0_sel:DWORD src1_sel:WORD_1
	v_and_b32_sdwa v39, v78, v66 dst_sel:DWORD dst_unused:UNUSED_PAD src0_sel:WORD_1 src1_sel:DWORD
	v_and_b32_sdwa v67, v76, v66 dst_sel:DWORD dst_unused:UNUSED_PAD src0_sel:WORD_1 src1_sel:DWORD
	v_add3_u32 v70, v79, v70, s36
	v_add3_u32 v71, v77, v71, s36
	v_add3_u32 v67, v76, v67, s36
	v_add3_u32 v39, v78, v39, s36
	v_and_b32_e32 v70, 0xffff0000, v70
	v_and_b32_e32 v74, 0xffff0000, v71
	v_or_b32_sdwa v71, v70, v39 dst_sel:DWORD dst_unused:UNUSED_PAD src0_sel:DWORD src1_sel:WORD_1
	v_or_b32_sdwa v70, v74, v67 dst_sel:DWORD dst_unused:UNUSED_PAD src0_sel:DWORD src1_sel:WORD_1
	s_add_i32 s34, s34, 1
	s_and_b64 vcc, exec, s[20:21]
	s_mov_b32 s28, s37
	s_mov_b32 s1, s39
	s_mov_b32 s19, s6
	s_mov_b32 s4, s24
	s_mov_b32 s18, s29
	s_mov_b32 s0, s38
	s_mov_b64 s[2:3], s[22:23]
	global_store_dwordx4 v[72:73], v[68:71], off
	s_barrier
	s_cbranch_vccnz .LBB0_3769
	s_branch .LBB0_3751

.LBB0_3796:
	s_waitcnt vmcnt(5)
	v_add_u32_e32 v2, 0x800, v34
	s_lshr_b32 s0, s8, 8
	v_ashrrev_i32_e32 v42, 6, v2
	v_cvt_f32_u32_e32 v2, s0
	s_sub_i32 s10, 0, s0
	s_abs_i32 s5, s9
	s_ashr_i32 s4, s9, 31
	v_rcp_iflag_f32_e32 v2, v2
	v_add_u32_e32 v3, 0xa00, v34
	v_ashrrev_i32_e32 v43, 6, v3
	v_add_u32_e32 v3, 0xc00, v34
	v_mul_f32_e32 v2, 0x4f7ffffe, v2
	v_cvt_u32_f32_e32 v2, v2
	v_lshlrev_b32_e32 v1, 2, v34
	v_ashrrev_i32_e32 v44, 6, v3
	v_add_u32_e32 v3, 0xe00, v34
	v_readfirstlane_b32 s11, v2
	s_mul_i32 s10, s10, s11
	s_mul_hi_u32 s10, s11, s10
	s_add_i32 s11, s11, s10
	s_mul_hi_u32 s10, s5, s11
	s_mul_i32 s11, s10, s0
	s_sub_i32 s5, s5, s11
	s_add_i32 s11, s10, 1
	s_sub_i32 s12, s5, s0
	s_cmp_ge_u32 s5, s0
	s_cselect_b32 s10, s11, s10
	s_cselect_b32 s5, s12, s5
	s_add_i32 s11, s10, 1
	s_cmp_ge_u32 s5, s0
	s_cselect_b32 s5, s11, s10
	s_xor_b32 s5, s5, s4
	s_sub_i32 s12, s5, s4
	s_mul_i32 s0, s12, s0
	s_sub_i32 s0, s9, s0
	s_lshl_b32 s4, s0, 8
	s_ashr_i32 s5, s4, 31
	s_lshl_b64 s[10:11], s[4:5], 2
	s_add_u32 s6, s6, s10
	v_and_b32_e32 v38, 0xfc, v1
	v_ashrrev_i32_e32 v45, 6, v3
	s_addc_u32 s7, s7, s11
	s_lshl_b32 s18, s12, 6
	v_mov_b32_e32 v37, 0
	v_lshlrev_b32_e32 v36, 2, v38
	v_add_u32_e32 v2, s18, v45
	v_lshl_add_u64 v[26:27], s[6:7], 0, v[36:37]
	v_ashrrev_i32_e32 v5, 31, v2
	v_mad_u64_u32 v[2:3], s[6:7], v2, s8, 0
	v_mov_b32_e32 v4, v3
	v_mad_u64_u32 v[4:5], s[6:7], v5, s8, v[4:5]
	v_mov_b32_e32 v3, v4
	v_lshl_add_u64 v[10:11], v[2:3], 2, v[26:27]
	v_add_u32_e32 v2, s18, v44
	v_ashrrev_i32_e32 v5, 31, v2
	v_mad_u64_u32 v[2:3], s[6:7], v2, s8, 0
	v_mov_b32_e32 v4, v3
	v_mad_u64_u32 v[4:5], s[6:7], v5, s8, v[4:5]
	v_mov_b32_e32 v3, v4
	v_lshl_add_u64 v[12:13], v[2:3], 2, v[26:27]
	global_load_dwordx4 v[6:9], v[10:11], off
	global_load_dwordx4 v[2:5], v[12:13], off
	v_add_u32_e32 v10, s18, v43
	v_ashrrev_i32_e32 v13, 31, v10
	v_mad_u64_u32 v[10:11], s[6:7], v10, s8, 0
	v_mov_b32_e32 v12, v11
	v_mad_u64_u32 v[12:13], s[6:7], v13, s8, v[12:13]
	v_mov_b32_e32 v11, v12
	v_lshl_add_u64 v[18:19], v[10:11], 2, v[26:27]
	v_add_u32_e32 v10, s18, v42
	v_ashrrev_i32_e32 v13, 31, v10
	v_mad_u64_u32 v[10:11], s[6:7], v10, s8, 0
	v_mov_b32_e32 v12, v11
	v_add_u32_e32 v55, 0x600, v34
	v_mad_u64_u32 v[12:13], s[6:7], v13, s8, v[12:13]
	v_ashrrev_i32_e32 v41, 6, v55
	v_mov_b32_e32 v11, v12
	v_lshl_add_u64 v[20:21], v[10:11], 2, v[26:27]
	global_load_dwordx4 v[14:17], v[18:19], off
	global_load_dwordx4 v[10:13], v[20:21], off
	v_add_u32_e32 v18, s18, v41
	v_ashrrev_i32_e32 v21, 31, v18
	v_mad_u64_u32 v[18:19], s[6:7], v18, s8, 0
	v_mov_b32_e32 v20, v19
	v_add_u32_e32 v52, 0x400, v34
	v_mad_u64_u32 v[20:21], s[6:7], v21, s8, v[20:21]
	v_ashrrev_i32_e32 v40, 6, v52
	v_mov_b32_e32 v19, v20
	v_lshl_add_u64 v[28:29], v[18:19], 2, v[26:27]
	v_add_u32_e32 v18, s18, v40
	v_ashrrev_i32_e32 v21, 31, v18
	v_mad_u64_u32 v[18:19], s[6:7], v18, s8, 0
	v_mov_b32_e32 v20, v19
	v_add_u32_e32 v35, 0x200, v34
	v_mad_u64_u32 v[20:21], s[6:7], v21, s8, v[20:21]
	v_ashrrev_i32_e32 v39, 6, v35
	v_mov_b32_e32 v19, v20
	s_waitcnt vmcnt(8)
	v_lshl_add_u64 v[30:31], v[18:19], 2, v[26:27]
	global_load_dwordx4 v[22:25], v[28:29], off
	global_load_dwordx4 v[18:21], v[30:31], off
	v_add_u32_e32 v28, s18, v39
	v_ashrrev_i32_e32 v31, 31, v28
	v_mad_u64_u32 v[28:29], s[6:7], v28, s8, 0
	v_mov_b32_e32 v30, v29
	v_mad_u64_u32 v[30:31], s[6:7], v31, s8, v[30:31]
	v_ashrrev_i32_e32 v1, 6, v34
	v_mov_b32_e32 v29, v30
	v_lshl_add_u64 v[46:47], v[28:29], 2, v[26:27]
	v_add_u32_e32 v28, s18, v1
	v_ashrrev_i32_e32 v31, 31, v28
	v_mad_u64_u32 v[28:29], s[6:7], v28, s8, 0
	v_mov_b32_e32 v30, v29
	v_mad_u64_u32 v[30:31], s[6:7], v31, s8, v[30:31]
	v_mov_b32_e32 v29, v30
	v_lshl_add_u64 v[48:49], v[28:29], 2, v[26:27]
	global_load_dwordx4 v[30:33], v[46:47], off
	global_load_dwordx4 v[26:29], v[48:49], off
	v_lshlrev_b32_e32 v46, 3, v34
	v_and_b32_e32 v66, 56, v46
	s_movk_i32 s0, 0x404
	v_readlane_b32 s16, v252, 3
	v_mad_u32_u24 v56, v66, s0, 0
	v_mul_lo_u32 v58, v1, s0
	v_mul_lo_u32 v59, v39, s0
	v_mul_lo_u32 v60, v40, s0
	v_mul_lo_u32 v61, v41, s0
	v_mul_lo_u32 v62, v42, s0
	v_mul_lo_u32 v63, v43, s0
	v_mul_lo_u32 v64, v44, s0
	v_mul_lo_u32 v65, v45, s0
	v_readlane_b32 s17, v252, 4
	s_add_u32 s0, s16, 0x1e940000
	s_addc_u32 s5, s17, 0
	s_add_u32 s8, s16, 0x16940000
	s_addc_u32 s9, s17, 0
	s_add_u32 s10, s78, 0x1000000
	s_addc_u32 s11, s79, 0
	s_add_u32 s12, s16, 0x16140000
	s_addc_u32 s13, s17, 0
	v_readlane_b32 s36, v250, 7
	s_add_u32 s31, s16, 0x15540000
	v_readlane_b32 s50, v250, 21
	v_readlane_b32 s51, v250, 22
	s_addc_u32 s33, s17, 0
	s_mov_b64 s[14:15], s[50:51]
	s_add_u32 s14, s14, 0x6c00000
	s_addc_u32 s15, s15, 0
	v_add_u32_e32 v36, 0, v36
	v_ashrrev_i32_e32 v46, 3, v34
	v_ashrrev_i32_e32 v49, 3, v35
	v_ashrrev_i32_e32 v52, 3, v52
	v_ashrrev_i32_e32 v55, 3, v55
	v_readlane_b32 s38, v250, 9
	s_add_u32 s16, s16, 0x11f40000
	s_mov_b32 s7, 0
	v_lshl_add_u32 v47, v46, 2, v56
	v_and_b32_e32 v48, 15, v46
	v_lshl_add_u32 v50, v49, 2, v56
	v_and_b32_e32 v51, 15, v49
	v_lshl_add_u32 v53, v52, 2, v56
	v_and_b32_e32 v54, 15, v52
	v_lshl_add_u32 v56, v55, 2, v56
	v_and_b32_e32 v57, 15, v55
	s_addc_u32 s17, s17, 0
	s_add_i32 s34, s20, 0xfffffce1
	s_mov_b32 s35, 25
	v_add_u32_e32 v58, v36, v58
	v_add_u32_e32 v59, v36, v59
	v_add_u32_e32 v60, v36, v60
	v_add_u32_e32 v61, v36, v61
	v_add_u32_e32 v62, v36, v62
	v_add_u32_e32 v63, v36, v63
	v_add_u32_e32 v64, v36, v64
	v_add_u32_e32 v65, v36, v65
	v_lshlrev_b32_e32 v36, 2, v38
	v_lshlrev_b32_e32 v34, 1, v66
	s_movk_i32 s36, 0x7fff
	v_mov_b32_e32 v38, 1
	s_mov_b32 s6, s19
	s_mov_b32 s38, s30
	s_mov_b64 s[22:23], s[2:3]
	v_readlane_b32 s37, v250, 8
	v_readlane_b32 s39, v250, 10
	v_readlane_b32 s40, v250, 11
	v_readlane_b32 s41, v250, 12
	v_readlane_b32 s42, v250, 13
	v_readlane_b32 s43, v250, 14
	v_readlane_b32 s44, v250, 15
	v_readlane_b32 s45, v250, 16
	v_readlane_b32 s46, v250, 17
	v_readlane_b32 s47, v250, 18
	v_readlane_b32 s48, v250, 19
	v_readlane_b32 s49, v250, 20
	s_waitcnt vmcnt(0)
	s_branch .LBB0_3800
.LBB0_3800:
	s_add_i32 s37, s28, 1
	s_cmp_lt_u32 s35, 2
	s_cselect_b64 s[20:21], -1, 0
	s_and_b64 vcc, exec, s[20:21]
	s_mov_b32 s39, s1
	s_mov_b32 s24, s4
	s_mov_b32 s29, s18
	s_cbranch_vccnz .Lcwp_3800
	s_add_i32 s6, s34, 0x93f
	s_cmpk_lt_i32 s6, 0x6bf
	s_cbranch_scc1 .LBB0_3797
	s_add_i32 s29, s34, 0x940
	s_cmpk_gt_u32 s29, 0x83f
	s_mov_b64 s[24:25], -1
	s_cbranch_scc0 .LBB0_3815
	s_cmpk_gt_u32 s29, 0x93f
	s_cbranch_scc0 .LBB0_3812
	s_mul_hi_u32 s6, s34, 0xaaaaaaab
	s_lshr_b32 s24, s6, 8
	s_mul_i32 s6, s24, 0xfffffe80
	s_add_i32 s42, s28, s6
	s_addk_i32 s42, 0xf6c1
	s_add_i32 s25, s34, s6
	s_cmpk_gt_i32 s25, 0x7f
	s_mov_b64 s[28:29], -1
	s_cbranch_scc0 .LBB0_3809
	s_cmpk_gt_u32 s25, 0xff
	s_cbranch_scc0 .LBB0_3807
	s_add_i32 s6, s24, 16
	s_add_i32 s41, s42, 0xffffff00
	s_lshl_b64 s[22:23], s[6:7], 23
	s_mov_b32 s25, s7
	s_add_u32 s26, s88, s22
	s_addc_u32 s27, s89, s23
	s_lshl_b64 s[22:23], s[24:25], 22
	s_add_u32 s22, s0, s22
	s_addc_u32 s23, s5, s23
	s_mov_b64 s[28:29], 0

.LBB0_3817:
	s_movk_i32 s38, 0x400
	s_movk_i32 s40, 0x800
	s_mov_b32 s39, 0
	s_mov_b32 s6, 0
	s_cbranch_execz .LBB0_3810
	s_branch .LBB0_3811
.LBB0_3797:
	s_mov_b32 s6, 0
	s_movk_i32 s40, 0x3600
	s_movk_i32 s38, 0x800
	s_mov_b64 s[26:27], s[14:15]
	s_mov_b64 s[22:23], s[16:17]
	s_mov_b32 s41, s37
	s_mov_b32 s39, 0
.LBB0_3798:
	s_lshr_b32 s24, s40, 8
	v_cvt_f32_u32_e32 v182, s24
	s_sub_i32 s29, 0, s24
	s_abs_i32 s28, s41
	s_ashr_i32 s25, s41, 31
	v_rcp_iflag_f32_e32 v182, v182
	s_nop 0
	v_mul_f32_e32 v182, 0x4f7ffffe, v182
	v_cvt_u32_f32_e32 v182, v182
	s_nop 0
	v_readfirstlane_b32 s42, v182
	s_mul_i32 s29, s29, s42
	s_mul_hi_u32 s29, s42, s29
	s_add_i32 s42, s42, s29
	s_mul_hi_u32 s29, s28, s42
	s_mul_i32 s42, s29, s24
	s_sub_i32 s28, s28, s42
	s_add_i32 s43, s29, 1
	s_sub_i32 s42, s28, s24
	s_cmp_ge_u32 s28, s24
	s_cselect_b32 s29, s43, s29
	s_cselect_b32 s28, s42, s28
	s_add_i32 s42, s29, 1
	s_cmp_ge_u32 s28, s24
	s_cselect_b32 s28, s42, s29
	s_xor_b32 s28, s28, s25
	s_sub_i32 s25, s28, s25
	s_lshl_b32 s29, s25, 6
	s_mul_i32 s25, s25, s24
	s_sub_i32 s24, s41, s25
	s_lshl_b32 s24, s24, 8
	s_ashr_i32 s25, s24, 31
	s_lshl_b64 s[42:43], s[24:25], 2
	s_add_u32 s26, s26, s42
	v_add_u32_e32 v184, s29, v1
	s_addc_u32 s27, s27, s43
	v_ashrrev_i32_e32 v187, 31, v184
	v_lshl_add_u64 v[182:183], s[26:27], 0, v[36:37]
	v_mad_u64_u32 v[184:185], s[26:27], v184, s40, 0
	v_mov_b32_e32 v186, v185
	v_mad_u64_u32 v[186:187], s[26:27], v187, s40, v[186:187]
	v_mov_b32_e32 v185, v186
	v_add_u32_e32 v186, s29, v39
	v_ashrrev_i32_e32 v189, 31, v186
	v_mad_u64_u32 v[186:187], s[26:27], v186, s40, 0
	v_mov_b32_e32 v188, v187
	v_mad_u64_u32 v[188:189], s[26:27], v189, s40, v[188:189]
	v_lshl_add_u64 v[184:185], v[184:185], 2, v[182:183]
	v_mov_b32_e32 v187, v188
	v_lshl_add_u64 v[186:187], v[186:187], 2, v[182:183]
	v_mov_b32_e32 v190, v184
	v_mov_b32_e32 v191, v185
	v_mov_b32_e32 v192, v186
	v_mov_b32_e32 v193, v187
	v_add_u32_e32 v184, s29, v40
	v_ashrrev_i32_e32 v187, 31, v184
	v_mad_u64_u32 v[184:185], s[26:27], v184, s40, 0
	v_mov_b32_e32 v186, v185
	v_mad_u64_u32 v[186:187], s[26:27], v187, s40, v[186:187]
	v_mov_b32_e32 v185, v186
	v_add_u32_e32 v186, s29, v41
	v_ashrrev_i32_e32 v189, 31, v186
	v_mad_u64_u32 v[186:187], s[26:27], v186, s40, 0
	v_mov_b32_e32 v188, v187
	v_mad_u64_u32 v[188:189], s[26:27], v189, s40, v[188:189]
	v_lshl_add_u64 v[184:185], v[184:185], 2, v[182:183]
	v_mov_b32_e32 v187, v188
	v_lshl_add_u64 v[186:187], v[186:187], 2, v[182:183]
	v_mov_b32_e32 v194, v184
	v_mov_b32_e32 v195, v185
	v_mov_b32_e32 v196, v186
	v_mov_b32_e32 v197, v187
	v_add_u32_e32 v184, s29, v42
	v_ashrrev_i32_e32 v187, 31, v184
	v_mad_u64_u32 v[184:185], s[26:27], v184, s40, 0
	v_mov_b32_e32 v186, v185
	v_mad_u64_u32 v[186:187], s[26:27], v187, s40, v[186:187]
	v_mov_b32_e32 v185, v186
	v_add_u32_e32 v186, s29, v43
	v_ashrrev_i32_e32 v189, 31, v186
	v_mad_u64_u32 v[186:187], s[26:27], v186, s40, 0
	v_mov_b32_e32 v188, v187
	v_mad_u64_u32 v[188:189], s[26:27], v189, s40, v[188:189]
	v_lshl_add_u64 v[184:185], v[184:185], 2, v[182:183]
	v_mov_b32_e32 v187, v188
	v_lshl_add_u64 v[186:187], v[186:187], 2, v[182:183]
	v_mov_b32_e32 v198, v184
	v_mov_b32_e32 v199, v185
	v_mov_b32_e32 v200, v186
	v_mov_b32_e32 v201, v187
	v_add_u32_e32 v184, s29, v44
	v_ashrrev_i32_e32 v187, 31, v184
	v_mad_u64_u32 v[184:185], s[26:27], v184, s40, 0
	v_mov_b32_e32 v186, v185
	v_mad_u64_u32 v[186:187], s[26:27], v187, s40, v[186:187]
	v_mov_b32_e32 v185, v186
	v_add_u32_e32 v186, s29, v45
	v_ashrrev_i32_e32 v189, 31, v186
	v_mad_u64_u32 v[186:187], s[26:27], v186, s40, 0
	v_mov_b32_e32 v188, v187
	v_mad_u64_u32 v[188:189], s[26:27], v189, s40, v[188:189]
	v_mov_b32_e32 v187, v188
	v_lshl_add_u64 v[184:185], v[184:185], 2, v[182:183]
	v_lshl_add_u64 v[186:187], v[186:187], 2, v[182:183]
	v_mov_b32_e32 v202, v184
	v_mov_b32_e32 v203, v185
	v_mov_b32_e32 v204, v186
	v_mov_b32_e32 v205, v187

.Lcq3800_3817:
	s_movk_i32 s38, 0x400
	s_movk_i32 s40, 0x800
	s_mov_b32 s39, 0
	s_mov_b32 s6, 0
	s_cbranch_execz .Lcq3800_3810
	s_branch .Lcq3800_3811
.Lcq3800_3797:
	s_mov_b32 s6, 0
	s_movk_i32 s40, 0x3600
	s_movk_i32 s38, 0x800
	s_mov_b64 s[26:27], s[14:15]
	s_mov_b64 s[22:23], s[16:17]
	s_mov_b32 s41, s37
	s_mov_b32 s39, 0

.Lcq3800_3799:
	s_add_i32 s35, s35, -1
	s_cmp_eq_u32 s19, 0
	v_add_u32_e32 v66, s4, v46
	v_lshlrev_b32_e32 v35, 1, v66
	s_cselect_b64 vcc, -1, 0
	s_ashr_i32 s19, s18, 31
	v_and_b32_e32 v35, 0xffffffe0, v35
	s_lshl_b64 s[18:19], s[18:19], 1
	v_add3_u32 v67, s1, v48, v35
	s_add_u32 s2, s2, s18
	s_addc_u32 s3, s3, s19
	v_mov_b32_e32 v35, v37
	v_cndmask_b32_e32 v66, v67, v66, vcc
	v_lshl_add_u64 v[70:71], s[2:3], 0, v[34:35]
	v_ashrrev_i32_e32 v69, 31, v66
	v_mad_u64_u32 v[66:67], s[2:3], v66, s30, 0
	v_mov_b32_e32 v68, v67
	ds_read_b32 v35, v47
	ds_read_b32 v74, v47 offset:1028
	ds_read_b32 v75, v47 offset:2056
	ds_read_b32 v76, v47 offset:3084
	ds_read_b32 v77, v47 offset:4112
	ds_read_b32 v78, v47 offset:5140
	ds_read_b32 v79, v47 offset:6168
	ds_read_b32 v80, v47 offset:7196
	v_mad_u64_u32 v[68:69], s[2:3], v69, s30, v[68:69]
	v_mov_b32_e32 v67, v68
	v_lshl_add_u64 v[72:73], v[66:67], 1, v[70:71]
	s_waitcnt lgkmcnt(7)
	v_and_b32_sdwa v67, v35, v38 dst_sel:DWORD dst_unused:UNUSED_PAD src0_sel:WORD_1 src1_sel:DWORD
	v_add3_u32 v35, v35, v67, s36
	s_waitcnt lgkmcnt(4)
	v_and_b32_sdwa v67, v76, v38 dst_sel:DWORD dst_unused:UNUSED_PAD src0_sel:WORD_1 src1_sel:DWORD
	v_and_b32_sdwa v68, v74, v38 dst_sel:DWORD dst_unused:UNUSED_PAD src0_sel:WORD_1 src1_sel:DWORD
	v_and_b32_sdwa v66, v75, v38 dst_sel:DWORD dst_unused:UNUSED_PAD src0_sel:WORD_1 src1_sel:DWORD
	v_add3_u32 v67, v76, v67, s36
	v_add3_u32 v68, v74, v68, s36
	v_add3_u32 v66, v75, v66, s36
	v_and_b32_e32 v67, 0xffff0000, v67
	v_and_b32_e32 v68, 0xffff0000, v68
	s_waitcnt lgkmcnt(0)
	v_and_b32_sdwa v69, v80, v38 dst_sel:DWORD dst_unused:UNUSED_PAD src0_sel:WORD_1 src1_sel:DWORD
	v_and_b32_sdwa v74, v78, v38 dst_sel:DWORD dst_unused:UNUSED_PAD src0_sel:WORD_1 src1_sel:DWORD
	v_or_b32_sdwa v67, v67, v66 dst_sel:DWORD dst_unused:UNUSED_PAD src0_sel:DWORD src1_sel:WORD_1
	v_or_b32_sdwa v66, v68, v35 dst_sel:DWORD dst_unused:UNUSED_PAD src0_sel:DWORD src1_sel:WORD_1
	v_and_b32_sdwa v35, v79, v38 dst_sel:DWORD dst_unused:UNUSED_PAD src0_sel:WORD_1 src1_sel:DWORD
	v_and_b32_sdwa v68, v77, v38 dst_sel:DWORD dst_unused:UNUSED_PAD src0_sel:WORD_1 src1_sel:DWORD
	v_add3_u32 v69, v80, v69, s36
	v_add3_u32 v74, v78, v74, s36
	v_add3_u32 v68, v77, v68, s36
	v_add3_u32 v35, v79, v35, s36
	v_and_b32_e32 v69, 0xffff0000, v69
	v_and_b32_e32 v74, 0xffff0000, v74
	v_or_b32_sdwa v69, v69, v35 dst_sel:DWORD dst_unused:UNUSED_PAD src0_sel:DWORD src1_sel:WORD_1
	v_or_b32_sdwa v68, v74, v68 dst_sel:DWORD dst_unused:UNUSED_PAD src0_sel:DWORD src1_sel:WORD_1
	global_store_dwordx4 v[72:73], v[66:69], off
	ds_read_b32 v35, v50
	ds_read_b32 v74, v50 offset:1028
	ds_read_b32 v75, v50 offset:2056
	ds_read_b32 v76, v50 offset:3084
	ds_read_b32 v77, v50 offset:4112
	ds_read_b32 v78, v50 offset:5140
	ds_read_b32 v79, v50 offset:6168
	ds_read_b32 v80, v50 offset:7196
	v_add_u32_e32 v66, s4, v49
	v_lshlrev_b32_e32 v67, 1, v66
	v_and_b32_e32 v67, 0xffffffe0, v67
	v_add3_u32 v67, s1, v51, v67
	v_cndmask_b32_e32 v66, v67, v66, vcc
	v_ashrrev_i32_e32 v69, 31, v66
	v_mad_u64_u32 v[66:67], s[2:3], v66, s30, 0
	v_mov_b32_e32 v68, v67
	v_mad_u64_u32 v[68:69], s[2:3], v69, s30, v[68:69]
	v_mov_b32_e32 v67, v68
	v_lshl_add_u64 v[72:73], v[66:67], 1, v[70:71]
	s_waitcnt lgkmcnt(7)
	v_and_b32_sdwa v67, v35, v38 dst_sel:DWORD dst_unused:UNUSED_PAD src0_sel:WORD_1 src1_sel:DWORD
	v_add3_u32 v35, v35, v67, s36
	s_waitcnt lgkmcnt(4)
	v_and_b32_sdwa v67, v76, v38 dst_sel:DWORD dst_unused:UNUSED_PAD src0_sel:WORD_1 src1_sel:DWORD
	v_and_b32_sdwa v68, v74, v38 dst_sel:DWORD dst_unused:UNUSED_PAD src0_sel:WORD_1 src1_sel:DWORD
	v_and_b32_sdwa v66, v75, v38 dst_sel:DWORD dst_unused:UNUSED_PAD src0_sel:WORD_1 src1_sel:DWORD
	v_add3_u32 v67, v76, v67, s36
	v_add3_u32 v68, v74, v68, s36
	v_add3_u32 v66, v75, v66, s36
	v_and_b32_e32 v67, 0xffff0000, v67
	v_and_b32_e32 v68, 0xffff0000, v68
	s_waitcnt lgkmcnt(0)
	v_and_b32_sdwa v69, v80, v38 dst_sel:DWORD dst_unused:UNUSED_PAD src0_sel:WORD_1 src1_sel:DWORD
	v_and_b32_sdwa v74, v78, v38 dst_sel:DWORD dst_unused:UNUSED_PAD src0_sel:WORD_1 src1_sel:DWORD
	v_or_b32_sdwa v67, v67, v66 dst_sel:DWORD dst_unused:UNUSED_PAD src0_sel:DWORD src1_sel:WORD_1
	v_or_b32_sdwa v66, v68, v35 dst_sel:DWORD dst_unused:UNUSED_PAD src0_sel:DWORD src1_sel:WORD_1
	v_and_b32_sdwa v35, v79, v38 dst_sel:DWORD dst_unused:UNUSED_PAD src0_sel:WORD_1 src1_sel:DWORD
	v_and_b32_sdwa v68, v77, v38 dst_sel:DWORD dst_unused:UNUSED_PAD src0_sel:WORD_1 src1_sel:DWORD
	v_add3_u32 v69, v80, v69, s36
	v_add3_u32 v74, v78, v74, s36
	v_add3_u32 v68, v77, v68, s36
	v_add3_u32 v35, v79, v35, s36
	v_and_b32_e32 v69, 0xffff0000, v69
	v_and_b32_e32 v74, 0xffff0000, v74
	v_or_b32_sdwa v69, v69, v35 dst_sel:DWORD dst_unused:UNUSED_PAD src0_sel:DWORD src1_sel:WORD_1
	v_or_b32_sdwa v68, v74, v68 dst_sel:DWORD dst_unused:UNUSED_PAD src0_sel:DWORD src1_sel:WORD_1
	global_store_dwordx4 v[72:73], v[66:69], off
	ds_read_b32 v35, v53
	ds_read_b32 v74, v53 offset:1028
	ds_read_b32 v75, v53 offset:2056
	ds_read_b32 v76, v53 offset:3084
	ds_read_b32 v77, v53 offset:4112
	ds_read_b32 v78, v53 offset:5140
	ds_read_b32 v79, v53 offset:6168
	ds_read_b32 v80, v53 offset:7196
	v_add_u32_e32 v66, s4, v52
	v_lshlrev_b32_e32 v67, 1, v66
	v_and_b32_e32 v67, 0xffffffe0, v67
	v_add3_u32 v67, s1, v54, v67
	v_cndmask_b32_e32 v66, v67, v66, vcc
	v_ashrrev_i32_e32 v69, 31, v66
	v_mad_u64_u32 v[66:67], s[2:3], v66, s30, 0
	v_mov_b32_e32 v68, v67
	v_mad_u64_u32 v[68:69], s[2:3], v69, s30, v[68:69]
	v_mov_b32_e32 v67, v68
	v_lshl_add_u64 v[72:73], v[66:67], 1, v[70:71]
	s_waitcnt lgkmcnt(7)
	v_and_b32_sdwa v67, v35, v38 dst_sel:DWORD dst_unused:UNUSED_PAD src0_sel:WORD_1 src1_sel:DWORD
	v_add3_u32 v35, v35, v67, s36
	s_waitcnt lgkmcnt(4)
	v_and_b32_sdwa v67, v76, v38 dst_sel:DWORD dst_unused:UNUSED_PAD src0_sel:WORD_1 src1_sel:DWORD
	v_and_b32_sdwa v68, v74, v38 dst_sel:DWORD dst_unused:UNUSED_PAD src0_sel:WORD_1 src1_sel:DWORD
	v_and_b32_sdwa v66, v75, v38 dst_sel:DWORD dst_unused:UNUSED_PAD src0_sel:WORD_1 src1_sel:DWORD
	v_add3_u32 v67, v76, v67, s36
	v_add3_u32 v68, v74, v68, s36
	v_add3_u32 v66, v75, v66, s36
	v_and_b32_e32 v67, 0xffff0000, v67
	v_and_b32_e32 v68, 0xffff0000, v68
	s_waitcnt lgkmcnt(0)
	v_and_b32_sdwa v69, v80, v38 dst_sel:DWORD dst_unused:UNUSED_PAD src0_sel:WORD_1 src1_sel:DWORD
	v_and_b32_sdwa v74, v78, v38 dst_sel:DWORD dst_unused:UNUSED_PAD src0_sel:WORD_1 src1_sel:DWORD
	v_or_b32_sdwa v67, v67, v66 dst_sel:DWORD dst_unused:UNUSED_PAD src0_sel:DWORD src1_sel:WORD_1
	v_or_b32_sdwa v66, v68, v35 dst_sel:DWORD dst_unused:UNUSED_PAD src0_sel:DWORD src1_sel:WORD_1
	v_and_b32_sdwa v35, v79, v38 dst_sel:DWORD dst_unused:UNUSED_PAD src0_sel:WORD_1 src1_sel:DWORD
	v_and_b32_sdwa v68, v77, v38 dst_sel:DWORD dst_unused:UNUSED_PAD src0_sel:WORD_1 src1_sel:DWORD
	v_add3_u32 v69, v80, v69, s36
	v_add3_u32 v74, v78, v74, s36
	v_add3_u32 v68, v77, v68, s36
	v_add3_u32 v35, v79, v35, s36
	v_and_b32_e32 v69, 0xffff0000, v69
	v_and_b32_e32 v74, 0xffff0000, v74
	v_or_b32_sdwa v69, v69, v35 dst_sel:DWORD dst_unused:UNUSED_PAD src0_sel:DWORD src1_sel:WORD_1
	v_or_b32_sdwa v68, v74, v68 dst_sel:DWORD dst_unused:UNUSED_PAD src0_sel:DWORD src1_sel:WORD_1
	global_store_dwordx4 v[72:73], v[66:69], off
	ds_read_b32 v35, v56
	ds_read_b32 v72, v56 offset:1028
	ds_read_b32 v73, v56 offset:2056
	ds_read_b32 v74, v56 offset:3084
	ds_read_b32 v75, v56 offset:4112
	ds_read_b32 v76, v56 offset:5140
	ds_read_b32 v77, v56 offset:6168
	ds_read_b32 v78, v56 offset:7196
	v_add_u32_e32 v66, s4, v55
	v_lshlrev_b32_e32 v67, 1, v66
	v_and_b32_e32 v67, 0xffffffe0, v67
	v_add3_u32 v67, s1, v57, v67
	v_cndmask_b32_e32 v66, v67, v66, vcc
	v_ashrrev_i32_e32 v69, 31, v66
	v_mad_u64_u32 v[66:67], s[2:3], v66, s30, 0
	v_mov_b32_e32 v68, v67
	v_mad_u64_u32 v[68:69], s[2:3], v69, s30, v[68:69]
	v_mov_b32_e32 v67, v68
	v_lshl_add_u64 v[70:71], v[66:67], 1, v[70:71]
	s_waitcnt lgkmcnt(7)
	v_and_b32_sdwa v67, v35, v38 dst_sel:DWORD dst_unused:UNUSED_PAD src0_sel:WORD_1 src1_sel:DWORD
	v_add3_u32 v35, v35, v67, s36
	s_waitcnt lgkmcnt(4)
	v_and_b32_sdwa v67, v74, v38 dst_sel:DWORD dst_unused:UNUSED_PAD src0_sel:WORD_1 src1_sel:DWORD
	v_and_b32_sdwa v68, v72, v38 dst_sel:DWORD dst_unused:UNUSED_PAD src0_sel:WORD_1 src1_sel:DWORD
	v_and_b32_sdwa v66, v73, v38 dst_sel:DWORD dst_unused:UNUSED_PAD src0_sel:WORD_1 src1_sel:DWORD
	v_add3_u32 v67, v74, v67, s36
	v_add3_u32 v68, v72, v68, s36
	v_add3_u32 v66, v73, v66, s36
	v_and_b32_e32 v67, 0xffff0000, v67
	v_and_b32_e32 v68, 0xffff0000, v68
	s_waitcnt lgkmcnt(0)
	v_and_b32_sdwa v69, v78, v38 dst_sel:DWORD dst_unused:UNUSED_PAD src0_sel:WORD_1 src1_sel:DWORD
	v_and_b32_sdwa v72, v76, v38 dst_sel:DWORD dst_unused:UNUSED_PAD src0_sel:WORD_1 src1_sel:DWORD
	v_or_b32_sdwa v67, v67, v66 dst_sel:DWORD dst_unused:UNUSED_PAD src0_sel:DWORD src1_sel:WORD_1
	v_or_b32_sdwa v66, v68, v35 dst_sel:DWORD dst_unused:UNUSED_PAD src0_sel:DWORD src1_sel:WORD_1
	v_and_b32_sdwa v35, v77, v38 dst_sel:DWORD dst_unused:UNUSED_PAD src0_sel:WORD_1 src1_sel:DWORD
	v_and_b32_sdwa v68, v75, v38 dst_sel:DWORD dst_unused:UNUSED_PAD src0_sel:WORD_1 src1_sel:DWORD
	v_add3_u32 v69, v78, v69, s36
	v_add3_u32 v72, v76, v72, s36
	v_add3_u32 v68, v75, v68, s36
	v_add3_u32 v35, v77, v35, s36
	v_and_b32_e32 v69, 0xffff0000, v69
	v_and_b32_e32 v72, 0xffff0000, v72
	v_or_b32_sdwa v69, v69, v35 dst_sel:DWORD dst_unused:UNUSED_PAD src0_sel:DWORD src1_sel:WORD_1
	v_or_b32_sdwa v68, v72, v68 dst_sel:DWORD dst_unused:UNUSED_PAD src0_sel:DWORD src1_sel:WORD_1
	s_add_i32 s34, s34, 1
	s_and_b64 vcc, exec, s[20:21]
	s_mov_b32 s28, s37
	s_mov_b32 s1, s39
	s_mov_b32 s19, s6
	s_mov_b32 s4, s24
	s_mov_b32 s18, s29
	s_mov_b32 s30, s38
	s_mov_b64 s[2:3], s[22:23]
	global_store_dwordx4 v[70:71], v[66:69], off
	s_barrier
	s_cbranch_vccnz .LBB0_3818
	s_branch .LBB0_3800
